# adds: P16 output rows and P10 X1B rows stored non-temporal
# baseline (speedup 1.0000x reference)
.LBB0_3478:
	s_add_i32 s14, s8, -7
	s_ashr_i32 s15, s14, 31
	s_lshl_b64 s[4:5], s[14:15], 11
	s_lshl_b64 s[18:19], s[14:15], 12
	s_add_u32 s16, s96, s18
	s_addc_u32 s17, s97, s19
	global_load_dwordx2 v[34:35], v234, s[16:17]
	global_load_dwordx2 v[36:37], v234, s[16:17] offset:512
	global_load_dwordx2 v[42:43], v234, s[16:17] offset:1024
	global_load_dwordx2 v[44:45], v234, s[16:17] offset:1536
	global_load_dwordx2 v[46:47], v234, s[16:17] offset:2048
	global_load_dwordx2 v[48:49], v234, s[16:17] offset:2560
	global_load_dwordx2 v[40:41], v234, s[16:17] offset:3072
	global_load_dwordx2 v[38:39], v234, s[16:17] offset:3584
	s_lshl_b64 s[14:15], s[14:15], 13
	s_add_u32 s14, s6, s14
	s_addc_u32 s15, s7, s15
	global_load_dwordx4 v[30:33], v178, s[14:15]
	global_load_dwordx4 v[26:29], v178, s[14:15] offset:1024
	global_load_dwordx4 v[22:25], v178, s[14:15] offset:2048
	global_load_dwordx4 v[18:21], v178, s[14:15] offset:3072
	v_lshl_add_u64 v[2:3], s[14:15], 0, v[178:179]
	v_add_co_u32_e32 v2, vcc, s41, v2
	s_add_i32 s22, s8, -6
	s_nop 0
	v_addc_co_u32_e32 v3, vcc, 0, v3, vcc
	global_load_dwordx4 v[14:17], v[2:3], off
	global_load_dwordx4 v[10:13], v[2:3], off offset:1024
	global_load_dwordx4 v[6:9], v[2:3], off offset:2048
	s_nop 0
	global_load_dwordx4 v[2:5], v[2:3], off offset:3072
	s_ashr_i32 s23, s22, 31
	s_lshl_b64 s[14:15], s[22:23], 11
	s_lshl_b64 s[16:17], s[22:23], 12
	s_add_u32 s20, s96, s16
	s_addc_u32 s21, s97, s17
	s_lshl_b64 s[22:23], s[22:23], 13
	s_add_u32 s22, s6, s22
	s_addc_u32 s23, s7, s23
	global_load_dwordx2 v[158:159], v234, s[20:21]
	global_load_dwordx4 v[134:137], v178, s[22:23]
	global_load_dwordx2 v[94:95], v234, s[20:21] offset:512
	v_lshlrev_b32_e32 v237, 2, v170
	s_waitcnt vmcnt(0)
	v_and_b32_e32 v85, 0xffff0000, v34
	v_and_b32_e32 v87, 0xffff0000, v35
	v_lshlrev_b32_e32 v84, 16, v34
	v_lshlrev_b32_e32 v86, 16, v35
	v_lshlrev_b32_e32 v81, 16, v37
	v_lshlrev_b32_e32 v80, 16, v36
	v_and_b32_e32 v83, 0xffff0000, v37
	v_and_b32_e32 v82, 0xffff0000, v36
	v_and_b32_e32 v75, 0xffff0000, v43
	v_lshlrev_b32_e32 v37, 16, v44
	v_and_b32_e32 v35, 0xffff0000, v44
	v_mul_f32_e32 v34, v87, v87
	v_mul_f32_e32 v36, v85, v85
	v_lshlrev_b32_e32 v70, 16, v42
	v_and_b32_e32 v71, 0xffff0000, v42
	v_lshlrev_b32_e32 v74, 16, v43
	v_lshlrev_b32_e32 v50, 16, v45
	v_and_b32_e32 v51, 0xffff0000, v45
	v_pk_mul_f32 v[42:43], v[82:83], v[82:83]
	v_mov_b32_e32 v45, v37
	v_mul_f32_e32 v44, v75, v75
	v_pk_fma_f32 v[54:55], v[86:87], v[86:87], v[34:35] op_sel_hi:[1,1,0]
	v_pk_fma_f32 v[56:57], v[84:85], v[84:85], v[36:37] op_sel_hi:[1,1,0]
	v_lshlrev_b32_e32 v52, 16, v40
	v_and_b32_e32 v53, 0xffff0000, v40
	v_mul_f32_e32 v40, v71, v71
	v_pk_fma_f32 v[42:43], v[80:81], v[80:81], v[42:43]
	v_pk_fma_f32 v[60:61], v[74:75], v[74:75], v[44:45] op_sel_hi:[1,1,0]
	v_mov_b32_e32 v36, v56
	v_mov_b32_e32 v44, v54
	v_mul_f32_e32 v63, v35, v35
	v_mul_f32_e32 v66, v50, v50
	v_mul_f32_e32 v67, v51, v51
	v_pk_fma_f32 v[58:59], v[70:71], v[70:71], v[40:41] op_sel_hi:[1,1,0]
	v_pk_add_f32 v[54:55], v[56:57], v[54:55]
	v_pk_add_f32 v[42:43], v[42:43], v[42:43] op_sel:[0,1] op_sel_hi:[1,0]
	v_pk_mul_f32 v[44:45], v[36:37], v[44:45]
	v_and_b32_e32 v79, 0xffff0000, v47
	v_and_b32_e32 v78, 0xffff0000, v46
	v_mov_b32_e32 v59, v66
	v_mov_b32_e32 v61, v67
	v_mov_b32_e32 v43, v63
	v_mov_b32_e32 v55, v45
	v_lshlrev_b32_e32 v77, 16, v47
	v_lshlrev_b32_e32 v76, 16, v46
	v_pk_mul_f32 v[46:47], v[78:79], v[78:79]
	v_pk_add_f32 v[56:57], v[58:59], v[60:61]
	v_pk_add_f32 v[42:43], v[54:55], v[42:43]
	v_pk_fma_f32 v[46:47], v[76:77], v[76:77], v[46:47]
	v_pk_add_f32 v[42:43], v[42:43], v[56:57]
	v_and_b32_e32 v73, 0xffff0000, v49
	v_and_b32_e32 v72, 0xffff0000, v48
	v_pk_add_f32 v[46:47], v[46:47], v[46:47] op_sel:[0,1] op_sel_hi:[1,0]
	v_lshlrev_b32_e32 v93, 16, v38
	v_and_b32_e32 v91, 0xffff0000, v38
	v_lshlrev_b32_e32 v88, 16, v39
	v_and_b32_e32 v89, 0xffff0000, v39
	v_pk_add_f32 v[38:39], v[42:43], v[42:43] op_sel:[0,1] op_sel_hi:[1,0]
	v_lshlrev_b32_e32 v65, 16, v49
	v_lshlrev_b32_e32 v64, 16, v48
	v_lshlrev_b32_e32 v62, 16, v41
	v_pk_mul_f32 v[48:49], v[72:73], v[72:73]
	v_and_b32_e32 v63, 0xffff0000, v41
	v_mov_b32_e32 v92, v38
	v_mov_b32_e32 v40, v46
	v_mov_b32_e32 v41, v93
	v_pk_fma_f32 v[48:49], v[64:65], v[64:65], v[48:49]
	v_pk_add_f32 v[38:39], v[38:39], v[46:47]
	v_pk_mul_f32 v[40:41], v[92:93], v[40:41]
	v_mul_f32_e32 v34, v91, v91
	v_mov_b32_e32 v39, v41
	v_pk_add_f32 v[40:41], v[48:49], v[48:49] op_sel:[0,1] op_sel_hi:[1,0]
	v_mul_f32_e32 v36, v88, v88
	v_mov_b32_e32 v41, v34
	v_mul_f32_e32 v34, v53, v53
	v_pk_add_f32 v[38:39], v[38:39], v[40:41]
	v_pk_fma_f32 v[40:41], v[52:53], v[52:53], v[34:35] op_sel_hi:[1,1,0]
	v_mul_f32_e32 v34, v63, v63
	v_mul_f32_e32 v44, v89, v89
	v_pk_fma_f32 v[42:43], v[62:63], v[62:63], v[34:35] op_sel_hi:[1,1,0]
	v_mov_b32_e32 v41, v36
	v_mov_b32_e32 v43, v44
	v_pk_add_f32 v[40:41], v[40:41], v[42:43]
	global_load_dwordx4 v[138:141], v178, s[22:23] offset:1024
	global_load_dwordx2 v[168:169], v234, s[20:21] offset:1024
	global_load_dwordx4 v[66:69], v178, s[22:23] offset:2048
	global_load_dwordx2 v[166:167], v234, s[20:21] offset:1536
	v_pk_add_f32 v[38:39], v[38:39], v[40:41]
	global_load_dwordx4 v[58:61], v178, s[22:23] offset:3072
	global_load_dwordx2 v[96:97], v234, s[20:21] offset:2048
	v_add_f32_e32 v34, v38, v39
	ds_bpermute_b32 v36, v171, v34
	v_lshl_add_u64 v[38:39], s[22:23], 0, v[178:179]
	v_add_co_u32_e32 v38, vcc, s41, v38
	v_mov_b32_e32 v90, v93
	s_waitcnt lgkmcnt(0)
	v_add_f32_e32 v34, v34, v36
	ds_bpermute_b32 v36, v226, v34
	v_addc_co_u32_e32 v39, vcc, 0, v39, vcc
	global_load_dwordx4 v[54:57], v[38:39], off
	global_load_dwordx2 v[160:161], v234, s[20:21] offset:2560
	global_load_dwordx4 v[46:49], v[38:39], off offset:1024
	global_load_dwordx2 v[182:183], v234, s[20:21] offset:3072
	global_load_dwordx4 v[42:45], v[38:39], off offset:2048
	global_load_dwordx2 v[180:181], v234, s[20:21] offset:3584
	s_nop 0
	global_load_dwordx4 v[38:41], v[38:39], off offset:3072
	s_waitcnt lgkmcnt(0)
	v_add_f32_e32 v34, v34, v36
	ds_bpermute_b32 v36, v228, v34
	ds_read_b128 v[98:101], v233
	ds_read_b128 v[102:105], v233 offset:1024
	s_add_u32 s20, s35, s18
	s_addc_u32 s21, s36, s19
	s_waitcnt lgkmcnt(2)
	v_add_f32_e32 v34, v34, v36
	ds_bpermute_b32 v36, v229, v34
	ds_read_b128 v[106:109], v233 offset:2048
	ds_read_b128 v[110:113], v233 offset:3072
	ds_read_b128 v[114:117], v233 offset:4096
	ds_read_b128 v[118:121], v233 offset:5120
	s_waitcnt lgkmcnt(4)
	v_add_f32_e32 v34, v34, v36
	ds_bpermute_b32 v36, v230, v34
	ds_read_b128 v[122:125], v233 offset:6144
	ds_read_b128 v[126:129], v233 offset:7168
	v_and_b32_e32 v207, 0xffff0000, v158
	v_and_b32_e32 v209, 0xffff0000, v159
	s_waitcnt lgkmcnt(2)
	v_add_f32_e32 v34, v34, v36
	ds_bpermute_b32 v36, v231, v34
	v_lshlrev_b32_e32 v206, 16, v158
	v_lshlrev_b32_e32 v208, 16, v159
	v_and_b32_e32 v205, 0xffff0000, v95
	v_and_b32_e32 v204, 0xffff0000, v94
	s_waitcnt lgkmcnt(0)
	v_add_f32_e32 v34, v34, v36
	v_fmamk_f32 v34, v34, 0x3a000000, v232
	v_cmp_gt_f32_e32 vcc, s43, v34
	v_mul_f32_e32 v36, 0x4b800000, v34
	v_lshlrev_b32_e32 v203, 16, v95
	v_cndmask_b32_e32 v34, v34, v36, vcc
	v_rsq_f32_e32 v34, v34
	v_lshlrev_b32_e32 v202, 16, v94
	s_add_u32 s24, s11, s18
	s_addc_u32 s25, s13, s19
	v_mul_f32_e32 v36, 0x45800000, v34
	v_cndmask_b32_e32 v36, v34, v36, vcc
	v_pk_mul_f32 v[84:85], v[36:37], v[84:85] op_sel_hi:[0,1]
	v_pk_mul_f32 v[86:87], v[36:37], v[86:87] op_sel_hi:[0,1]
	v_pk_fma_f32 v[142:143], v[98:99], v[84:85], v[30:31]
	v_pk_fma_f32 v[144:145], v[100:101], v[86:87], v[32:33]
	v_and_b32_sdwa v31, v142, v235 dst_sel:DWORD dst_unused:UNUSED_PAD src0_sel:WORD_1 src1_sel:DWORD
	v_add3_u32 v32, v142, v31, s44
	v_and_b32_sdwa v31, v145, v235 dst_sel:DWORD dst_unused:UNUSED_PAD src0_sel:WORD_1 src1_sel:DWORD
	v_and_b32_sdwa v33, v143, v235 dst_sel:DWORD dst_unused:UNUSED_PAD src0_sel:WORD_1 src1_sel:DWORD
	v_and_b32_sdwa v30, v144, v235 dst_sel:DWORD dst_unused:UNUSED_PAD src0_sel:WORD_1 src1_sel:DWORD
	v_add3_u32 v31, v145, v31, s44
	v_add3_u32 v33, v143, v33, s44
	v_add3_u32 v30, v144, v30, s44
	v_and_b32_e32 v31, 0xffff0000, v31
	v_and_b32_e32 v33, 0xffff0000, v33
	v_or_b32_sdwa v31, v31, v30 dst_sel:DWORD dst_unused:UNUSED_PAD src0_sel:DWORD src1_sel:WORD_1
	v_or_b32_sdwa v30, v33, v32 dst_sel:DWORD dst_unused:UNUSED_PAD src0_sel:DWORD src1_sel:WORD_1
	global_store_dwordx2 v234, v[30:31], s[20:21] nt
	v_mov_b32_e32 v30, v81
	v_mov_b32_e32 v81, v82
	v_mov_b32_e32 v31, v83
	v_pk_mul_f32 v[32:33], v[36:37], v[80:81] op_sel_hi:[0,1]
	v_pk_mul_f32 v[30:31], v[36:37], v[30:31] op_sel_hi:[0,1]
	v_pk_fma_f32 v[130:131], v[102:103], v[32:33], v[26:27]
	v_pk_fma_f32 v[132:133], v[104:105], v[30:31], v[28:29]
	v_and_b32_sdwa v27, v130, v235 dst_sel:DWORD dst_unused:UNUSED_PAD src0_sel:WORD_1 src1_sel:DWORD
	v_add3_u32 v28, v130, v27, s44
	v_and_b32_sdwa v27, v133, v235 dst_sel:DWORD dst_unused:UNUSED_PAD src0_sel:WORD_1 src1_sel:DWORD
	v_and_b32_sdwa v29, v131, v235 dst_sel:DWORD dst_unused:UNUSED_PAD src0_sel:WORD_1 src1_sel:DWORD
	v_and_b32_sdwa v26, v132, v235 dst_sel:DWORD dst_unused:UNUSED_PAD src0_sel:WORD_1 src1_sel:DWORD
	v_add3_u32 v27, v133, v27, s44
	v_add3_u32 v29, v131, v29, s44
	v_add3_u32 v26, v132, v26, s44
	v_and_b32_e32 v27, 0xffff0000, v27
	v_and_b32_e32 v29, 0xffff0000, v29
	v_or_b32_sdwa v27, v27, v26 dst_sel:DWORD dst_unused:UNUSED_PAD src0_sel:DWORD src1_sel:WORD_1
	v_or_b32_sdwa v26, v29, v28 dst_sel:DWORD dst_unused:UNUSED_PAD src0_sel:DWORD src1_sel:WORD_1
	v_mov_b32_e32 v28, v143
	v_mov_b32_e32 v29, v131
	global_store_dwordx2 v234, v[26:27], s[20:21] offset:512 nt
	v_mov_b32_e32 v26, v142
	v_mov_b32_e32 v27, v130
	v_pk_mul_f32 v[28:29], v[28:29], v[28:29]
	v_mov_b32_e32 v30, v145
	v_pk_fma_f32 v[26:27], v[26:27], v[26:27], v[28:29]
	v_mov_b32_e32 v28, v144
	v_mov_b32_e32 v29, v132
	v_pk_mul_f32 v[28:29], v[28:29], v[28:29]
	v_mov_b32_e32 v31, v133
	v_pk_fma_f32 v[28:29], v[30:31], v[30:31], v[28:29]
	v_pk_mul_f32 v[30:31], v[36:37], v[70:71] op_sel_hi:[0,1]
	v_pk_add_f32 v[26:27], v[26:27], v[28:29]
	v_pk_mul_f32 v[28:29], v[36:37], v[74:75] op_sel_hi:[0,1]
	v_pk_fma_f32 v[146:147], v[106:107], v[30:31], v[22:23]
	v_pk_fma_f32 v[148:149], v[108:109], v[28:29], v[24:25]
	v_and_b32_sdwa v23, v146, v235 dst_sel:DWORD dst_unused:UNUSED_PAD src0_sel:WORD_1 src1_sel:DWORD
	v_add3_u32 v24, v146, v23, s44
	v_and_b32_sdwa v23, v149, v235 dst_sel:DWORD dst_unused:UNUSED_PAD src0_sel:WORD_1 src1_sel:DWORD
	v_and_b32_sdwa v25, v147, v235 dst_sel:DWORD dst_unused:UNUSED_PAD src0_sel:WORD_1 src1_sel:DWORD
	v_and_b32_sdwa v22, v148, v235 dst_sel:DWORD dst_unused:UNUSED_PAD src0_sel:WORD_1 src1_sel:DWORD
	v_add3_u32 v23, v149, v23, s44
	v_add3_u32 v25, v147, v25, s44
	v_add3_u32 v22, v148, v22, s44
	v_and_b32_e32 v23, 0xffff0000, v23
	v_and_b32_e32 v25, 0xffff0000, v25
	v_or_b32_sdwa v23, v23, v22 dst_sel:DWORD dst_unused:UNUSED_PAD src0_sel:DWORD src1_sel:WORD_1
	v_or_b32_sdwa v22, v25, v24 dst_sel:DWORD dst_unused:UNUSED_PAD src0_sel:DWORD src1_sel:WORD_1
	global_store_dwordx2 v234, v[22:23], s[20:21] offset:1024 nt
	v_pk_mul_f32 v[22:23], v[148:149], v[148:149]
	v_pk_mul_f32 v[24:25], v[146:147], v[146:147]
	v_mov_b32_e32 v34, v37
	v_pk_mov_b32 v[28:29], v[24:25], v[22:23] op_sel:[1,0]
	v_mov_b32_e32 v25, v23
	v_pk_add_f32 v[22:23], v[24:25], v[28:29]
	v_pk_mul_f32 v[28:29], v[34:35], v[36:37] op_sel_hi:[1,0]
	v_pk_mul_f32 v[24:25], v[50:51], v[36:37] op_sel_hi:[1,0]
	v_pk_fma_f32 v[150:151], v[110:111], v[28:29], v[18:19]
	v_pk_fma_f32 v[152:153], v[112:113], v[24:25], v[20:21]
	v_and_b32_sdwa v19, v150, v235 dst_sel:DWORD dst_unused:UNUSED_PAD src0_sel:WORD_1 src1_sel:DWORD
	v_add3_u32 v20, v150, v19, s44
	v_and_b32_sdwa v19, v153, v235 dst_sel:DWORD dst_unused:UNUSED_PAD src0_sel:WORD_1 src1_sel:DWORD
	v_and_b32_sdwa v21, v151, v235 dst_sel:DWORD dst_unused:UNUSED_PAD src0_sel:WORD_1 src1_sel:DWORD
	v_and_b32_sdwa v18, v152, v235 dst_sel:DWORD dst_unused:UNUSED_PAD src0_sel:WORD_1 src1_sel:DWORD
	v_add3_u32 v19, v153, v19, s44
	v_add3_u32 v21, v151, v21, s44
	v_mov_b32_e32 v24, v76
	v_mov_b32_e32 v25, v78
	v_add3_u32 v18, v152, v18, s44
	v_and_b32_e32 v19, 0xffff0000, v19
	v_and_b32_e32 v21, 0xffff0000, v21
	v_pk_mul_f32 v[24:25], v[36:37], v[24:25] op_sel_hi:[0,1]
	v_mov_b32_e32 v78, v77
	v_or_b32_sdwa v19, v19, v18 dst_sel:DWORD dst_unused:UNUSED_PAD src0_sel:DWORD src1_sel:WORD_1
	v_or_b32_sdwa v18, v21, v20 dst_sel:DWORD dst_unused:UNUSED_PAD src0_sel:DWORD src1_sel:WORD_1
	v_pk_mul_f32 v[28:29], v[36:37], v[78:79] op_sel_hi:[0,1]
	v_pk_fma_f32 v[154:155], v[114:115], v[24:25], v[14:15]
	global_store_dwordx2 v234, v[18:19], s[20:21] offset:1536 nt
	v_mul_f32_e32 v18, v150, v150
	v_pk_fma_f32 v[50:51], v[116:117], v[28:29], v[16:17]
	v_and_b32_sdwa v15, v154, v235 dst_sel:DWORD dst_unused:UNUSED_PAD src0_sel:WORD_1 src1_sel:DWORD
	v_pk_fma_f32 v[18:19], v[150:151], v[150:151], v[18:19] op_sel_hi:[1,1,0]
	v_add3_u32 v16, v154, v15, s44
	v_and_b32_sdwa v15, v51, v235 dst_sel:DWORD dst_unused:UNUSED_PAD src0_sel:WORD_1 src1_sel:DWORD
	v_and_b32_sdwa v17, v155, v235 dst_sel:DWORD dst_unused:UNUSED_PAD src0_sel:WORD_1 src1_sel:DWORD
	v_mul_f32_e32 v18, v152, v152
	v_and_b32_sdwa v14, v50, v235 dst_sel:DWORD dst_unused:UNUSED_PAD src0_sel:WORD_1 src1_sel:DWORD
	v_add3_u32 v15, v51, v15, s44
	v_add3_u32 v17, v155, v17, s44
	v_pk_add_f32 v[26:27], v[26:27], v[26:27] op_sel_hi:[0,1]
	v_pk_add_f32 v[22:23], v[22:23], v[22:23] op_sel_hi:[0,1]
	v_pk_fma_f32 v[20:21], v[152:153], v[152:153], v[18:19] op_sel_hi:[1,1,0]
	v_add3_u32 v14, v50, v14, s44
	v_and_b32_e32 v15, 0xffff0000, v15
	v_and_b32_e32 v17, 0xffff0000, v17
	v_or_b32_sdwa v15, v15, v14 dst_sel:DWORD dst_unused:UNUSED_PAD src0_sel:DWORD src1_sel:WORD_1
	v_or_b32_sdwa v14, v17, v16 dst_sel:DWORD dst_unused:UNUSED_PAD src0_sel:DWORD src1_sel:WORD_1
	v_mul_f32_e32 v18, v154, v154
	v_mul_f32_e32 v20, v155, v155
	v_mul_f32_e32 v26, v50, v50
	v_mul_f32_e32 v22, v51, v51
	global_store_dwordx2 v234, v[14:15], s[20:21] offset:2048 nt
	v_pk_add_f32 v[14:15], v[18:19], v[20:21]
	v_pk_add_f32 v[16:17], v[22:23], v[26:27]
	s_waitcnt vmcnt(14)
	v_lshlrev_b32_e32 v191, 16, v166
	v_pk_add_f32 v[14:15], v[14:15], v[16:17]
	v_mov_b32_e32 v16, v65
	v_mov_b32_e32 v65, v72
	v_mov_b32_e32 v17, v73
	v_pk_mul_f32 v[18:19], v[36:37], v[64:65] op_sel_hi:[0,1]
	v_pk_mul_f32 v[16:17], v[36:37], v[16:17] op_sel_hi:[0,1]
	v_pk_fma_f32 v[162:163], v[118:119], v[18:19], v[10:11]
	v_pk_fma_f32 v[164:165], v[120:121], v[16:17], v[12:13]
	v_and_b32_sdwa v11, v162, v235 dst_sel:DWORD dst_unused:UNUSED_PAD src0_sel:WORD_1 src1_sel:DWORD
	v_add3_u32 v12, v162, v11, s44
	v_and_b32_sdwa v11, v165, v235 dst_sel:DWORD dst_unused:UNUSED_PAD src0_sel:WORD_1 src1_sel:DWORD
	v_and_b32_sdwa v13, v163, v235 dst_sel:DWORD dst_unused:UNUSED_PAD src0_sel:WORD_1 src1_sel:DWORD
	v_and_b32_sdwa v10, v164, v235 dst_sel:DWORD dst_unused:UNUSED_PAD src0_sel:WORD_1 src1_sel:DWORD
	v_add3_u32 v11, v165, v11, s44
	v_add3_u32 v13, v163, v13, s44
	v_add3_u32 v10, v164, v10, s44
	v_and_b32_e32 v11, 0xffff0000, v11
	v_and_b32_e32 v13, 0xffff0000, v13
	v_or_b32_sdwa v11, v11, v10 dst_sel:DWORD dst_unused:UNUSED_PAD src0_sel:DWORD src1_sel:WORD_1
	v_or_b32_sdwa v10, v13, v12 dst_sel:DWORD dst_unused:UNUSED_PAD src0_sel:DWORD src1_sel:WORD_1
	global_store_dwordx2 v234, v[10:11], s[20:21] offset:2560 nt
	v_pk_mul_f32 v[10:11], v[164:165], v[164:165]
	v_pk_mul_f32 v[12:13], v[162:163], v[162:163]
	v_pk_add_f32 v[14:15], v[14:15], v[14:15] op_sel_hi:[0,1]
	v_pk_mov_b32 v[16:17], v[12:13], v[10:11] op_sel:[1,0]
	v_mov_b32_e32 v13, v11
	v_pk_add_f32 v[10:11], v[12:13], v[16:17]
	v_pk_mul_f32 v[16:17], v[36:37], v[52:53] op_sel_hi:[0,1]
	v_pk_mul_f32 v[12:13], v[36:37], v[62:63] op_sel_hi:[0,1]
	v_pk_fma_f32 v[64:65], v[16:17], v[122:123], v[6:7]
	v_pk_fma_f32 v[156:157], v[12:13], v[124:125], v[8:9]
	v_and_b32_sdwa v7, v64, v235 dst_sel:DWORD dst_unused:UNUSED_PAD src0_sel:WORD_1 src1_sel:DWORD
	v_add3_u32 v8, v64, v7, s44
	v_and_b32_sdwa v7, v157, v235 dst_sel:DWORD dst_unused:UNUSED_PAD src0_sel:WORD_1 src1_sel:DWORD
	v_and_b32_sdwa v9, v65, v235 dst_sel:DWORD dst_unused:UNUSED_PAD src0_sel:WORD_1 src1_sel:DWORD
	v_and_b32_sdwa v6, v156, v235 dst_sel:DWORD dst_unused:UNUSED_PAD src0_sel:WORD_1 src1_sel:DWORD
	v_add3_u32 v7, v157, v7, s44
	v_add3_u32 v9, v65, v9, s44
	v_add3_u32 v6, v156, v6, s44
	v_and_b32_e32 v7, 0xffff0000, v7
	v_and_b32_e32 v9, 0xffff0000, v9
	v_pk_mul_f32 v[12:13], v[90:91], v[36:37] op_sel_hi:[1,0]
	v_or_b32_sdwa v7, v7, v6 dst_sel:DWORD dst_unused:UNUSED_PAD src0_sel:DWORD src1_sel:WORD_1
	v_or_b32_sdwa v6, v9, v8 dst_sel:DWORD dst_unused:UNUSED_PAD src0_sel:DWORD src1_sel:WORD_1
	v_pk_mul_f32 v[16:17], v[88:89], v[36:37] op_sel_hi:[1,0]
	v_pk_fma_f32 v[62:63], v[12:13], v[126:127], v[2:3]
	global_store_dwordx2 v234, v[6:7], s[20:21] offset:3072 nt
	v_mul_f32_e32 v6, v64, v64
	v_pk_fma_f32 v[52:53], v[16:17], v[128:129], v[4:5]
	v_and_b32_sdwa v3, v62, v235 dst_sel:DWORD dst_unused:UNUSED_PAD src0_sel:WORD_1 src1_sel:DWORD
	v_pk_fma_f32 v[6:7], v[64:65], v[64:65], v[6:7] op_sel_hi:[1,1,0]
	v_add3_u32 v4, v62, v3, s44
	v_and_b32_sdwa v3, v53, v235 dst_sel:DWORD dst_unused:UNUSED_PAD src0_sel:WORD_1 src1_sel:DWORD
	v_and_b32_sdwa v5, v63, v235 dst_sel:DWORD dst_unused:UNUSED_PAD src0_sel:WORD_1 src1_sel:DWORD
	v_mul_f32_e32 v6, v156, v156
	v_and_b32_sdwa v2, v52, v235 dst_sel:DWORD dst_unused:UNUSED_PAD src0_sel:WORD_1 src1_sel:DWORD
	v_add3_u32 v3, v53, v3, s44
	v_add3_u32 v5, v63, v5, s44
	v_pk_add_f32 v[10:11], v[10:11], v[10:11] op_sel_hi:[0,1]
	v_pk_fma_f32 v[8:9], v[156:157], v[156:157], v[6:7] op_sel_hi:[1,1,0]
	v_add3_u32 v2, v52, v2, s44
	v_and_b32_e32 v3, 0xffff0000, v3
	v_and_b32_e32 v5, 0xffff0000, v5
	v_or_b32_sdwa v3, v3, v2 dst_sel:DWORD dst_unused:UNUSED_PAD src0_sel:DWORD src1_sel:WORD_1
	v_or_b32_sdwa v2, v5, v4 dst_sel:DWORD dst_unused:UNUSED_PAD src0_sel:DWORD src1_sel:WORD_1
	v_mul_f32_e32 v6, v62, v62
	v_mul_f32_e32 v8, v63, v63
	v_mul_f32_e32 v14, v52, v52
	v_mul_f32_e32 v10, v53, v53
	global_store_dwordx2 v234, v[2:3], s[20:21] offset:3584 nt
	v_pk_add_f32 v[2:3], v[6:7], v[8:9]
	v_pk_add_f32 v[4:5], v[10:11], v[14:15]
	v_mul_f32_e32 v8, v207, v207
	v_pk_add_f32 v[2:3], v[2:3], v[4:5]
	v_mul_f32_e32 v4, v209, v209
	v_pk_fma_f32 v[4:5], v[208:209], v[208:209], v[4:5] op_sel_hi:[1,1,0]
	v_pk_mul_f32 v[6:7], v[204:205], v[204:205]
	v_pk_fma_f32 v[8:9], v[206:207], v[206:207], v[8:9] op_sel_hi:[1,1,0]
	v_pk_fma_f32 v[6:7], v[202:203], v[202:203], v[6:7]
	v_and_b32_e32 v189, 0xffff0000, v166
	v_mov_b32_e32 v190, v8
	v_mov_b32_e32 v10, v4
	v_mov_b32_e32 v11, v191
	v_mul_f32_e32 v12, v189, v189
	v_pk_add_f32 v[4:5], v[8:9], v[4:5]
	v_pk_mul_f32 v[8:9], v[190:191], v[10:11]
	v_pk_add_f32 v[6:7], v[6:7], v[6:7] op_sel:[0,1] op_sel_hi:[1,0]
	v_and_b32_e32 v199, 0xffff0000, v168
	v_and_b32_e32 v201, 0xffff0000, v169
	v_mov_b32_e32 v5, v9
	v_mov_b32_e32 v7, v12
	v_lshlrev_b32_e32 v198, 16, v168
	v_lshlrev_b32_e32 v200, 16, v169
	v_lshlrev_b32_e32 v196, 16, v167
	v_and_b32_e32 v197, 0xffff0000, v167
	v_pk_add_f32 v[4:5], v[4:5], v[6:7]
	v_mul_f32_e32 v6, v199, v199
	v_mul_f32_e32 v8, v201, v201
	v_mul_f32_e32 v13, v196, v196
	v_mul_f32_e32 v14, v197, v197
	v_pk_fma_f32 v[6:7], v[198:199], v[198:199], v[6:7] op_sel_hi:[1,1,0]
	v_pk_fma_f32 v[8:9], v[200:201], v[200:201], v[8:9] op_sel_hi:[1,1,0]
	v_mov_b32_e32 v7, v13
	v_mov_b32_e32 v9, v14
	v_pk_add_f32 v[6:7], v[6:7], v[8:9]
	s_waitcnt vmcnt(15)
	v_and_b32_e32 v195, 0xffff0000, v97
	v_and_b32_e32 v194, 0xffff0000, v96
	v_pk_add_f32 v[4:5], v[4:5], v[6:7]
	v_lshlrev_b32_e32 v193, 16, v97
	v_lshlrev_b32_e32 v192, 16, v96
	v_pk_mul_f32 v[6:7], v[194:195], v[194:195]
	s_waitcnt vmcnt(13)
	v_and_b32_e32 v187, 0xffff0000, v161
	v_pk_fma_f32 v[6:7], v[192:193], v[192:193], v[6:7]
	v_and_b32_e32 v186, 0xffff0000, v160
	v_pk_add_f32 v[6:7], v[6:7], v[6:7] op_sel:[0,1] op_sel_hi:[1,0]
	s_waitcnt vmcnt(9)
	v_lshlrev_b32_e32 v167, 16, v180
	v_pk_add_f32 v[4:5], v[4:5], v[4:5] op_sel:[0,1] op_sel_hi:[1,0]
	v_lshlrev_b32_e32 v185, 16, v161
	v_lshlrev_b32_e32 v184, 16, v160
	v_pk_mul_f32 v[8:9], v[186:187], v[186:187]
	v_mov_b32_e32 v166, v4
	v_mov_b32_e32 v10, v6
	v_mov_b32_e32 v11, v167
	v_pk_fma_f32 v[8:9], v[184:185], v[184:185], v[8:9]
	v_and_b32_e32 v161, 0xffff0000, v180
	v_pk_add_f32 v[4:5], v[4:5], v[6:7]
	v_pk_mul_f32 v[6:7], v[166:167], v[10:11]
	v_mul_f32_e32 v12, v161, v161
	v_mov_b32_e32 v5, v7
	v_pk_add_f32 v[6:7], v[8:9], v[8:9] op_sel:[0,1] op_sel_hi:[1,0]
	v_lshlrev_b32_e32 v168, 16, v182
	v_and_b32_e32 v169, 0xffff0000, v182
	v_lshlrev_b32_e32 v182, 16, v183
	v_and_b32_e32 v183, 0xffff0000, v183
	v_mov_b32_e32 v7, v12
	v_lshlrev_b32_e32 v158, 16, v181
	v_and_b32_e32 v159, 0xffff0000, v181
	v_pk_add_f32 v[4:5], v[4:5], v[6:7]
	v_mul_f32_e32 v6, v169, v169
	v_mul_f32_e32 v8, v183, v183
	v_mul_f32_e32 v13, v158, v158
	v_mul_f32_e32 v14, v159, v159
	v_pk_fma_f32 v[6:7], v[168:169], v[168:169], v[6:7] op_sel_hi:[1,1,0]
	v_pk_fma_f32 v[8:9], v[182:183], v[182:183], v[8:9] op_sel_hi:[1,1,0]
	v_mov_b32_e32 v7, v13
	v_mov_b32_e32 v9, v14
	v_pk_add_f32 v[6:7], v[6:7], v[8:9]
	s_add_u32 s26, s33, s4
	v_pk_add_f32 v[4:5], v[4:5], v[6:7]
	v_mov_b32_e32 v7, v2
	v_mov_b32_e32 v6, v4
	v_mov_b32_e32 v2, v5
	v_pk_add_f32 v[2:3], v[6:7], v[2:3]
	ds_bpermute_b32 v5, v171, v3
	ds_bpermute_b32 v4, v171, v2
	s_addc_u32 s27, s34, s5
	s_add_i32 s4, s8, -5
	s_ashr_i32 s5, s4, 31
	s_lshl_b64 s[18:19], s[4:5], 11
	s_waitcnt lgkmcnt(0)
	v_pk_add_f32 v[2:3], v[2:3], v[4:5]
	ds_bpermute_b32 v5, v226, v3
	ds_bpermute_b32 v4, v226, v2
	s_lshl_b64 s[20:21], s[4:5], 12
	s_add_u32 s28, s96, s20
	s_addc_u32 s29, s97, s21
	s_lshl_b64 s[4:5], s[4:5], 13
	s_waitcnt lgkmcnt(0)
	v_pk_add_f32 v[2:3], v[2:3], v[4:5]
	ds_bpermute_b32 v5, v228, v3
	ds_bpermute_b32 v4, v228, v2
	s_add_u32 s30, s6, s4
	s_addc_u32 s31, s7, s5
	ds_read_b128 v[26:29], v233 offset:8192
	ds_read_b128 v[30:33], v233 offset:16384
	ds_read_b128 v[90:93], v233 offset:9216
	ds_read_b128 v[94:97], v233 offset:17408
	ds_read_b128 v[82:85], v233 offset:10240
	ds_read_b128 v[86:89], v233 offset:18432
	s_waitcnt lgkmcnt(6)
	v_pk_add_f32 v[180:181], v[2:3], v[4:5]
	ds_bpermute_b32 v211, v229, v181
	ds_bpermute_b32 v210, v229, v180
	ds_read_b128 v[74:77], v233 offset:11264
	ds_read_b128 v[78:81], v233 offset:19456
	ds_read_b128 v[34:37], v233 offset:12288
	ds_read_b128 v[70:73], v233 offset:20480
	ds_read_b128 v[18:21], v233 offset:13312
	ds_read_b128 v[22:25], v233 offset:21504
	ds_read_b128 v[10:13], v233 offset:14336
	ds_read_b128 v[14:17], v233 offset:22528
	ds_read_b128 v[2:5], v233 offset:15360
	ds_read_b128 v[6:9], v233 offset:23552
	v_lshl_add_u64 v[212:213], s[30:31], 0, v[178:179]
	s_waitcnt lgkmcnt(10)
	v_pk_add_f32 v[180:181], v[180:181], v[210:211]
	ds_bpermute_b32 v211, v230, v181
	ds_bpermute_b32 v210, v230, v180
	s_add_u32 s22, s35, s16
	s_addc_u32 s23, s36, s17
	s_waitcnt lgkmcnt(0)
	v_pk_add_f32 v[180:181], v[180:181], v[210:211]
	ds_bpermute_b32 v211, v231, v181
	ds_bpermute_b32 v210, v231, v180
	s_waitcnt lgkmcnt(0)
	v_pk_add_f32 v[210:211], v[180:181], v[210:211]
	v_mov_b64_e32 v[180:181], s[12:13]
	v_pk_fma_f32 v[210:211], v[210:211], s[10:11], v[180:181] op_sel_hi:[1,0,0]
	s_nop 0
	v_mul_f32_e32 v160, 0x4b800000, v211
	v_cmp_gt_f32_e64 s[4:5], s43, v211
	v_cmp_gt_f32_e32 vcc, s43, v210
	s_nop 0
	v_cndmask_b32_e64 v160, v211, v160, s[4:5]
	v_rsq_f32_e32 v160, v160
	s_nop 0
	v_mul_f32_e32 v166, 0x45800000, v160
	v_cndmask_b32_e64 v160, v160, v166, s[4:5]
	v_pk_mul_f32 v[142:143], v[142:143], v[160:161] op_sel_hi:[1,0]
	v_pk_mul_f32 v[144:145], v[144:145], v[160:161] op_sel_hi:[1,0]
	v_pk_fma_f32 v[142:143], v[26:27], v[142:143], v[30:31]
	v_pk_fma_f32 v[144:145], v[28:29], v[144:145], v[32:33]
	v_bfe_u32 v166, v142, 16, 1
	v_add3_u32 v166, v142, v166, s44
	v_bfe_u32 v188, v143, 16, 1
	v_lshrrev_b32_e32 v166, 16, v166
	v_add3_u32 v188, v143, v188, s44
	v_and_or_b32 v214, v188, s42, v166
	v_med3_f32 v142, v142, s45, v236
	v_med3_f32 v143, v143, s45, v236
	v_mov_b32_e32 v188, 0
	v_cvt_pk_fp8_f32 v188, v142, v143
	v_bfe_u32 v166, v144, 16, 1
	v_add3_u32 v166, v144, v166, s44
	v_bfe_u32 v142, v145, 16, 1
	v_pk_mul_f32 v[130:131], v[130:131], v[160:161] op_sel_hi:[1,0]
	v_lshrrev_b32_e32 v166, 16, v166
	v_med3_f32 v143, v144, s45, v236
	v_med3_f32 v144, v145, s45, v236
	v_add3_u32 v142, v145, v142, s44
	v_pk_fma_f32 v[130:131], v[90:91], v[130:131], v[94:95]
	v_cvt_pk_fp8_f32 v188, v143, v144 op_sel:[0,0,1]
	v_and_or_b32 v215, v142, s42, v166
	v_bfe_u32 v142, v130, 16, 1
	v_bfe_u32 v143, v131, 16, 1
	v_add3_u32 v142, v130, v142, s44
	v_add3_u32 v143, v131, v143, s44
	v_med3_f32 v130, v130, s45, v236
	v_med3_f32 v131, v131, s45, v236
	v_mov_b32_e32 v144, 0
	v_pk_mul_f32 v[132:133], v[132:133], v[160:161] op_sel_hi:[1,0]
	v_cvt_pk_fp8_f32 v144, v130, v131
	v_pk_fma_f32 v[132:133], v[92:93], v[132:133], v[96:97]
	v_lshrrev_b32_e32 v142, 16, v142
	v_and_or_b32 v142, v143, s42, v142
	v_bfe_u32 v143, v132, 16, 1
	v_add3_u32 v143, v132, v143, s44
	v_bfe_u32 v130, v133, 16, 1
	v_med3_f32 v131, v132, s45, v236
	v_med3_f32 v132, v133, s45, v236
	v_lshrrev_b32_e32 v143, 16, v143
	v_cvt_pk_fp8_f32 v144, v131, v132 op_sel:[0,0,1]
	v_add3_u32 v130, v133, v130, s44
	v_and_or_b32 v143, v130, s42, v143
	v_pk_mul_f32 v[130:131], v[146:147], v[160:161] op_sel_hi:[1,0]
	global_store_dwordx2 v234, v[214:215], s[24:25]
	global_store_dword v237, v188, s[26:27]
	v_pk_fma_f32 v[130:131], v[82:83], v[130:131], v[86:87]
	global_store_dwordx2 v234, v[142:143], s[24:25] offset:512
	global_store_dword v237, v144, s[26:27] offset:256
	v_bfe_u32 v142, v130, 16, 1
	v_bfe_u32 v143, v131, 16, 1
	v_add3_u32 v142, v130, v142, s44
	v_add3_u32 v143, v131, v143, s44
	v_med3_f32 v130, v130, s45, v236
	v_med3_f32 v131, v131, s45, v236
	v_mov_b32_e32 v144, 0
	v_pk_mul_f32 v[132:133], v[148:149], v[160:161] op_sel_hi:[1,0]
	v_cvt_pk_fp8_f32 v144, v130, v131
	v_pk_fma_f32 v[132:133], v[84:85], v[132:133], v[88:89]
	v_lshrrev_b32_e32 v142, 16, v142
	v_and_or_b32 v142, v143, s42, v142
	v_bfe_u32 v143, v132, 16, 1
	v_add3_u32 v143, v132, v143, s44
	v_bfe_u32 v130, v133, 16, 1
	v_med3_f32 v131, v132, s45, v236
	v_med3_f32 v132, v133, s45, v236
	v_lshrrev_b32_e32 v143, 16, v143
	v_cvt_pk_fp8_f32 v144, v131, v132 op_sel:[0,0,1]
	v_add3_u32 v130, v133, v130, s44
	v_and_or_b32 v143, v130, s42, v143
	v_pk_mul_f32 v[130:131], v[150:151], v[160:161] op_sel_hi:[1,0]
	global_store_dwordx2 v234, v[142:143], s[24:25] offset:1024
	global_store_dword v237, v144, s[26:27] offset:512
	v_pk_fma_f32 v[130:131], v[130:131], v[74:75], v[78:79]
	v_pk_mul_f32 v[132:133], v[152:153], v[160:161] op_sel_hi:[1,0]
	v_bfe_u32 v142, v130, 16, 1
	v_bfe_u32 v143, v131, 16, 1
	v_add3_u32 v142, v130, v142, s44
	v_add3_u32 v143, v131, v143, s44
	v_med3_f32 v130, v130, s45, v236
	v_med3_f32 v131, v131, s45, v236
	v_mov_b32_e32 v144, 0
	v_pk_fma_f32 v[132:133], v[132:133], v[76:77], v[80:81]
	v_lshrrev_b32_e32 v142, 16, v142
	v_cvt_pk_fp8_f32 v144, v130, v131
	v_and_or_b32 v142, v143, s42, v142
	v_bfe_u32 v143, v132, 16, 1
	v_add3_u32 v143, v132, v143, s44
	v_bfe_u32 v130, v133, 16, 1
	v_lshrrev_b32_e32 v143, 16, v143
	v_med3_f32 v131, v132, s45, v236
	v_med3_f32 v132, v133, s45, v236
	v_add3_u32 v130, v133, v130, s44
	v_cvt_pk_fp8_f32 v144, v131, v132 op_sel:[0,0,1]
	v_and_or_b32 v143, v130, s42, v143
	v_pk_mul_f32 v[130:131], v[154:155], v[160:161] op_sel_hi:[1,0]
	global_store_dwordx2 v234, v[142:143], s[24:25] offset:1536
	global_store_dword v237, v144, s[26:27] offset:768
	v_pk_fma_f32 v[130:131], v[130:131], v[34:35], v[70:71]
	v_mov_b32_e32 v142, 0
	v_bfe_u32 v132, v130, 16, 1
	v_bfe_u32 v133, v131, 16, 1
	v_add3_u32 v132, v130, v132, s44
	v_add3_u32 v133, v131, v133, s44
	v_med3_f32 v130, v130, s45, v236
	v_med3_f32 v131, v131, s45, v236
	v_pk_mul_f32 v[50:51], v[50:51], v[160:161] op_sel_hi:[1,0]
	v_cvt_pk_fp8_f32 v142, v130, v131
	v_pk_fma_f32 v[50:51], v[50:51], v[36:37], v[72:73]
	v_lshrrev_b32_e32 v132, 16, v132
	v_and_or_b32 v132, v133, s42, v132
	v_bfe_u32 v133, v50, 16, 1
	v_add3_u32 v133, v50, v133, s44
	v_bfe_u32 v130, v51, 16, 1
	v_med3_f32 v50, v50, s45, v236
	v_med3_f32 v131, v51, s45, v236
	v_lshrrev_b32_e32 v133, 16, v133
	v_cvt_pk_fp8_f32 v142, v50, v131 op_sel:[0,0,1]
	v_add3_u32 v50, v51, v130, s44
	v_and_or_b32 v133, v50, s42, v133
	v_pk_mul_f32 v[50:51], v[162:163], v[160:161] op_sel_hi:[1,0]
	global_store_dwordx2 v234, v[132:133], s[24:25] offset:2048
	global_store_dword v237, v142, s[26:27] offset:1024
	v_pk_fma_f32 v[50:51], v[50:51], v[18:19], v[22:23]
	v_pk_mul_f32 v[130:131], v[164:165], v[160:161] op_sel_hi:[1,0]
	v_bfe_u32 v132, v50, 16, 1
	v_bfe_u32 v133, v51, 16, 1
	v_add3_u32 v132, v50, v132, s44
	v_add3_u32 v133, v51, v133, s44
	v_med3_f32 v50, v50, s45, v236
	v_med3_f32 v51, v51, s45, v236
	v_mov_b32_e32 v142, 0
	v_pk_fma_f32 v[130:131], v[130:131], v[20:21], v[24:25]
	v_lshrrev_b32_e32 v132, 16, v132
	v_cvt_pk_fp8_f32 v142, v50, v51
	v_and_or_b32 v132, v133, s42, v132
	v_bfe_u32 v133, v130, 16, 1
	v_add3_u32 v133, v130, v133, s44
	v_bfe_u32 v50, v131, 16, 1
	v_lshrrev_b32_e32 v133, 16, v133
	v_med3_f32 v51, v130, s45, v236
	v_med3_f32 v130, v131, s45, v236
	v_add3_u32 v50, v131, v50, s44
	v_cvt_pk_fp8_f32 v142, v51, v130 op_sel:[0,0,1]
	v_and_or_b32 v133, v50, s42, v133
	v_pk_mul_f32 v[50:51], v[64:65], v[160:161] op_sel_hi:[1,0]
	global_store_dwordx2 v234, v[132:133], s[24:25] offset:2560
	global_store_dword v237, v142, s[26:27] offset:1280
	v_pk_fma_f32 v[50:51], v[50:51], v[10:11], v[14:15]
	v_pk_mul_f32 v[64:65], v[156:157], v[160:161] op_sel_hi:[1,0]
	v_bfe_u32 v130, v50, 16, 1
	v_bfe_u32 v131, v51, 16, 1
	v_add3_u32 v130, v50, v130, s44
	v_add3_u32 v131, v51, v131, s44
	v_med3_f32 v50, v50, s45, v236
	v_med3_f32 v51, v51, s45, v236
	v_mov_b32_e32 v132, 0
	v_pk_fma_f32 v[64:65], v[64:65], v[12:13], v[16:17]
	v_lshrrev_b32_e32 v130, 16, v130
	v_cvt_pk_fp8_f32 v132, v50, v51
	v_and_or_b32 v130, v131, s42, v130
	v_bfe_u32 v131, v64, 16, 1
	v_add3_u32 v131, v64, v131, s44
	v_bfe_u32 v50, v65, 16, 1
	v_lshrrev_b32_e32 v131, 16, v131
	v_med3_f32 v51, v64, s45, v236
	v_med3_f32 v64, v65, s45, v236
	v_add3_u32 v50, v65, v50, s44
	v_cvt_pk_fp8_f32 v132, v51, v64 op_sel:[0,0,1]
	v_and_or_b32 v131, v50, s42, v131
	v_pk_mul_f32 v[50:51], v[62:63], v[160:161] op_sel_hi:[1,0]
	v_mov_b32_e32 v64, 0
	v_pk_fma_f32 v[50:51], v[50:51], v[2:3], v[6:7]
	v_pk_mul_f32 v[52:53], v[52:53], v[160:161] op_sel_hi:[1,0]
	v_bfe_u32 v62, v50, 16, 1
	v_bfe_u32 v63, v51, 16, 1
	v_add3_u32 v62, v50, v62, s44
	v_add3_u32 v63, v51, v63, s44
	v_med3_f32 v50, v50, s45, v236
	v_med3_f32 v51, v51, s45, v236
	v_cvt_pk_fp8_f32 v64, v50, v51
	v_pk_fma_f32 v[52:53], v[52:53], v[4:5], v[8:9]
	v_lshrrev_b32_e32 v62, 16, v62
	v_and_or_b32 v62, v63, s42, v62
	v_bfe_u32 v63, v52, 16, 1
	v_add3_u32 v63, v52, v63, s44
	v_med3_f32 v51, v52, s45, v236
	v_med3_f32 v52, v53, s45, v236
	v_bfe_u32 v50, v53, 16, 1
	v_cvt_pk_fp8_f32 v64, v51, v52 op_sel:[0,0,1]
	v_lshrrev_b32_e32 v63, 16, v63
	v_add3_u32 v50, v53, v50, s44
	v_and_or_b32 v63, v50, s42, v63
	global_store_dwordx2 v234, v[130:131], s[24:25] offset:3072
	global_store_dword v237, v132, s[26:27] offset:1536
	global_store_dwordx2 v234, v[62:63], s[24:25] offset:3584
	global_store_dword v237, v64, s[26:27] offset:1792
	global_load_dwordx2 v[220:221], v234, s[28:29]
	global_load_dwordx4 v[162:165], v178, s[30:31]
	global_load_dwordx2 v[222:223], v234, s[28:29] offset:512
	global_load_dwordx4 v[154:157], v178, s[30:31] offset:1024
	global_load_dwordx2 v[224:225], v234, s[28:29] offset:1024
	global_load_dwordx4 v[150:153], v178, s[30:31] offset:2048
	global_load_dwordx2 v[238:239], v234, s[28:29] offset:1536
	global_load_dwordx4 v[146:149], v178, s[30:31] offset:3072
	global_load_dwordx2 v[240:241], v234, s[28:29] offset:2048
	v_add_co_u32_e64 v50, s[4:5], s41, v212
	v_mul_f32_e32 v52, 0x4b800000, v210
	s_nop 0
	v_addc_co_u32_e64 v51, s[4:5], 0, v213, s[4:5]
	v_cndmask_b32_e32 v52, v210, v52, vcc
	global_load_dwordx4 v[142:145], v[50:51], off
	global_load_dwordx2 v[242:243], v234, s[28:29] offset:2560
	global_load_dwordx4 v[130:133], v[50:51], off offset:1024
	global_load_dwordx2 v[218:219], v234, s[28:29] offset:3072
	v_rsq_f32_e32 v160, v52
	global_load_dwordx4 v[62:65], v[50:51], off offset:2048
	global_load_dwordx2 v[244:245], v234, s[28:29] offset:3584
	s_nop 0
	global_load_dwordx4 v[50:53], v[50:51], off offset:3072
	v_mov_b32_e32 v188, v191
	s_add_u32 s26, s11, s16
	v_mul_f32_e32 v166, 0x45800000, v160
	v_cndmask_b32_e32 v166, v160, v166, vcc
	v_pk_mul_f32 v[206:207], v[166:167], v[206:207] op_sel_hi:[0,1]
	v_pk_mul_f32 v[208:209], v[166:167], v[208:209] op_sel_hi:[0,1]
	v_pk_fma_f32 v[214:215], v[98:99], v[206:207], v[134:135]
	v_pk_fma_f32 v[216:217], v[100:101], v[208:209], v[136:137]
	v_and_b32_sdwa v135, v214, v235 dst_sel:DWORD dst_unused:UNUSED_PAD src0_sel:WORD_1 src1_sel:DWORD
	v_add3_u32 v136, v214, v135, s44
	v_and_b32_sdwa v135, v217, v235 dst_sel:DWORD dst_unused:UNUSED_PAD src0_sel:WORD_1 src1_sel:DWORD
	v_and_b32_sdwa v137, v215, v235 dst_sel:DWORD dst_unused:UNUSED_PAD src0_sel:WORD_1 src1_sel:DWORD
	v_and_b32_sdwa v134, v216, v235 dst_sel:DWORD dst_unused:UNUSED_PAD src0_sel:WORD_1 src1_sel:DWORD
	v_add3_u32 v135, v217, v135, s44
	v_add3_u32 v137, v215, v137, s44
	v_add3_u32 v134, v216, v134, s44
	v_and_b32_e32 v135, 0xffff0000, v135
	v_and_b32_e32 v137, 0xffff0000, v137
	v_or_b32_sdwa v135, v135, v134 dst_sel:DWORD dst_unused:UNUSED_PAD src0_sel:DWORD src1_sel:WORD_1
	v_or_b32_sdwa v134, v137, v136 dst_sel:DWORD dst_unused:UNUSED_PAD src0_sel:DWORD src1_sel:WORD_1
	global_store_dwordx2 v234, v[134:135], s[22:23] nt
	v_mov_b32_e32 v134, v203
	v_mov_b32_e32 v203, v204
	v_mov_b32_e32 v135, v205
	v_pk_mul_f32 v[136:137], v[166:167], v[202:203] op_sel_hi:[0,1]
	v_pk_mul_f32 v[134:135], v[166:167], v[134:135] op_sel_hi:[0,1]
	v_pk_fma_f32 v[210:211], v[102:103], v[136:137], v[138:139]
	v_pk_fma_f32 v[212:213], v[104:105], v[134:135], v[140:141]
	v_and_b32_sdwa v135, v210, v235 dst_sel:DWORD dst_unused:UNUSED_PAD src0_sel:WORD_1 src1_sel:DWORD
	v_add3_u32 v136, v210, v135, s44
	v_and_b32_sdwa v135, v213, v235 dst_sel:DWORD dst_unused:UNUSED_PAD src0_sel:WORD_1 src1_sel:DWORD
	v_and_b32_sdwa v137, v211, v235 dst_sel:DWORD dst_unused:UNUSED_PAD src0_sel:WORD_1 src1_sel:DWORD
	v_and_b32_sdwa v134, v212, v235 dst_sel:DWORD dst_unused:UNUSED_PAD src0_sel:WORD_1 src1_sel:DWORD
	v_add3_u32 v135, v213, v135, s44
	v_add3_u32 v137, v211, v137, s44
	v_add3_u32 v134, v212, v134, s44
	v_and_b32_e32 v135, 0xffff0000, v135
	v_and_b32_e32 v137, 0xffff0000, v137
	v_or_b32_sdwa v135, v135, v134 dst_sel:DWORD dst_unused:UNUSED_PAD src0_sel:DWORD src1_sel:WORD_1
	v_or_b32_sdwa v134, v137, v136 dst_sel:DWORD dst_unused:UNUSED_PAD src0_sel:DWORD src1_sel:WORD_1
	v_mov_b32_e32 v136, v215
	v_mov_b32_e32 v137, v211
	global_store_dwordx2 v234, v[134:135], s[22:23] offset:512 nt
	v_mov_b32_e32 v134, v214
	v_mov_b32_e32 v135, v210
	v_pk_mul_f32 v[136:137], v[136:137], v[136:137]
	v_mov_b32_e32 v138, v217
	v_pk_fma_f32 v[134:135], v[134:135], v[134:135], v[136:137]
	v_mov_b32_e32 v136, v216
	v_mov_b32_e32 v137, v212
	v_pk_mul_f32 v[136:137], v[136:137], v[136:137]
	v_mov_b32_e32 v139, v213
	v_pk_fma_f32 v[136:137], v[138:139], v[138:139], v[136:137]
	v_pk_mul_f32 v[138:139], v[166:167], v[198:199] op_sel_hi:[0,1]
	v_pk_add_f32 v[134:135], v[134:135], v[136:137]
	v_pk_mul_f32 v[136:137], v[166:167], v[200:201] op_sel_hi:[0,1]
	v_pk_fma_f32 v[66:67], v[106:107], v[138:139], v[66:67]
	v_pk_fma_f32 v[68:69], v[108:109], v[136:137], v[68:69]
	v_pk_add_f32 v[134:135], v[134:135], v[134:135] op_sel_hi:[0,1]
	v_and_b32_sdwa v137, v69, v235 dst_sel:DWORD dst_unused:UNUSED_PAD src0_sel:WORD_1 src1_sel:DWORD
	v_and_b32_sdwa v138, v67, v235 dst_sel:DWORD dst_unused:UNUSED_PAD src0_sel:WORD_1 src1_sel:DWORD
	v_and_b32_sdwa v134, v68, v235 dst_sel:DWORD dst_unused:UNUSED_PAD src0_sel:WORD_1 src1_sel:DWORD
	v_and_b32_sdwa v136, v66, v235 dst_sel:DWORD dst_unused:UNUSED_PAD src0_sel:WORD_1 src1_sel:DWORD
	v_add3_u32 v137, v69, v137, s44
	v_add3_u32 v138, v67, v138, s44
	v_add3_u32 v136, v66, v136, s44
	v_add3_u32 v134, v68, v134, s44
	v_and_b32_e32 v137, 0xffff0000, v137
	v_and_b32_e32 v138, 0xffff0000, v138
	v_or_b32_sdwa v137, v137, v134 dst_sel:DWORD dst_unused:UNUSED_PAD src0_sel:DWORD src1_sel:WORD_1
	v_or_b32_sdwa v136, v138, v136 dst_sel:DWORD dst_unused:UNUSED_PAD src0_sel:DWORD src1_sel:WORD_1
	global_store_dwordx2 v234, v[136:137], s[22:23] offset:1024 nt
	v_pk_mul_f32 v[136:137], v[68:69], v[68:69]
	v_pk_mul_f32 v[138:139], v[66:67], v[66:67]
	v_mov_b32_e32 v160, v167
	v_pk_mov_b32 v[140:141], v[138:139], v[136:137] op_sel:[1,0]
	v_mov_b32_e32 v139, v137
	v_pk_add_f32 v[136:137], v[138:139], v[140:141]
	v_pk_mul_f32 v[138:139], v[196:197], v[166:167] op_sel_hi:[1,0]
	v_pk_mul_f32 v[140:141], v[188:189], v[166:167] op_sel_hi:[1,0]
	v_pk_fma_f32 v[60:61], v[112:113], v[138:139], v[60:61]
	v_pk_fma_f32 v[58:59], v[110:111], v[140:141], v[58:59]
	v_pk_add_f32 v[136:137], v[136:137], v[136:137] op_sel_hi:[0,1]
	v_and_b32_sdwa v138, v61, v235 dst_sel:DWORD dst_unused:UNUSED_PAD src0_sel:WORD_1 src1_sel:DWORD
	v_and_b32_sdwa v139, v59, v235 dst_sel:DWORD dst_unused:UNUSED_PAD src0_sel:WORD_1 src1_sel:DWORD
	v_and_b32_sdwa v134, v60, v235 dst_sel:DWORD dst_unused:UNUSED_PAD src0_sel:WORD_1 src1_sel:DWORD
	v_and_b32_sdwa v136, v58, v235 dst_sel:DWORD dst_unused:UNUSED_PAD src0_sel:WORD_1 src1_sel:DWORD
	v_add3_u32 v138, v61, v138, s44
	v_add3_u32 v139, v59, v139, s44
	v_add3_u32 v136, v58, v136, s44
	v_add3_u32 v134, v60, v134, s44
	v_and_b32_e32 v138, 0xffff0000, v138
	v_and_b32_e32 v140, 0xffff0000, v139
	v_or_b32_sdwa v139, v138, v134 dst_sel:DWORD dst_unused:UNUSED_PAD src0_sel:DWORD src1_sel:WORD_1
	v_or_b32_sdwa v138, v140, v136 dst_sel:DWORD dst_unused:UNUSED_PAD src0_sel:DWORD src1_sel:WORD_1
	v_mul_f32_e32 v134, v58, v58
	v_mov_b32_e32 v188, v192
	v_mov_b32_e32 v189, v194
	v_mov_b32_e32 v194, v193
	global_store_dwordx2 v234, v[138:139], s[22:23] offset:1536 nt
	v_pk_fma_f32 v[138:139], v[58:59], v[58:59], v[134:135] op_sel_hi:[1,1,0]
	v_mul_f32_e32 v134, v60, v60
	v_pk_mul_f32 v[188:189], v[166:167], v[188:189] op_sel_hi:[0,1]
	v_pk_mul_f32 v[190:191], v[166:167], v[194:195] op_sel_hi:[0,1]
	v_pk_fma_f32 v[140:141], v[60:61], v[60:61], v[134:135] op_sel_hi:[1,1,0]
	v_pk_fma_f32 v[56:57], v[116:117], v[190:191], v[56:57]
	v_pk_fma_f32 v[54:55], v[114:115], v[188:189], v[54:55]
	v_and_b32_sdwa v138, v57, v235 dst_sel:DWORD dst_unused:UNUSED_PAD src0_sel:WORD_1 src1_sel:DWORD
	v_and_b32_sdwa v140, v55, v235 dst_sel:DWORD dst_unused:UNUSED_PAD src0_sel:WORD_1 src1_sel:DWORD
	v_and_b32_sdwa v134, v56, v235 dst_sel:DWORD dst_unused:UNUSED_PAD src0_sel:WORD_1 src1_sel:DWORD
	v_and_b32_sdwa v136, v54, v235 dst_sel:DWORD dst_unused:UNUSED_PAD src0_sel:WORD_1 src1_sel:DWORD
	v_add3_u32 v138, v57, v138, s44
	v_add3_u32 v140, v55, v140, s44
	v_add3_u32 v136, v54, v136, s44
	v_add3_u32 v134, v56, v134, s44
	v_and_b32_e32 v138, 0xffff0000, v138
	v_and_b32_e32 v140, 0xffff0000, v140
	v_or_b32_sdwa v189, v138, v134 dst_sel:DWORD dst_unused:UNUSED_PAD src0_sel:DWORD src1_sel:WORD_1
	v_or_b32_sdwa v188, v140, v136 dst_sel:DWORD dst_unused:UNUSED_PAD src0_sel:DWORD src1_sel:WORD_1
	v_mul_f32_e32 v138, v54, v54
	v_mul_f32_e32 v140, v55, v55
	v_mul_f32_e32 v134, v56, v56
	v_mul_f32_e32 v136, v57, v57
	v_pk_add_f32 v[138:139], v[138:139], v[140:141]
	v_pk_add_f32 v[134:135], v[136:137], v[134:135]
	v_mov_b32_e32 v136, v185
	v_mov_b32_e32 v137, v187
	v_mov_b32_e32 v185, v186
	v_pk_add_f32 v[134:135], v[138:139], v[134:135]
	v_pk_mul_f32 v[136:137], v[166:167], v[136:137] op_sel_hi:[0,1]
	v_pk_mul_f32 v[138:139], v[166:167], v[184:185] op_sel_hi:[0,1]
	v_pk_fma_f32 v[46:47], v[118:119], v[138:139], v[46:47]
	v_pk_fma_f32 v[48:49], v[120:121], v[136:137], v[48:49]
	v_pk_add_f32 v[134:135], v[134:135], v[134:135] op_sel_hi:[0,1]
	v_and_b32_sdwa v137, v49, v235 dst_sel:DWORD dst_unused:UNUSED_PAD src0_sel:WORD_1 src1_sel:DWORD
	v_and_b32_sdwa v138, v47, v235 dst_sel:DWORD dst_unused:UNUSED_PAD src0_sel:WORD_1 src1_sel:DWORD
	v_and_b32_sdwa v134, v48, v235 dst_sel:DWORD dst_unused:UNUSED_PAD src0_sel:WORD_1 src1_sel:DWORD
	v_and_b32_sdwa v136, v46, v235 dst_sel:DWORD dst_unused:UNUSED_PAD src0_sel:WORD_1 src1_sel:DWORD
	v_add3_u32 v137, v49, v137, s44
	v_add3_u32 v138, v47, v138, s44
	v_add3_u32 v136, v46, v136, s44
	v_add3_u32 v134, v48, v134, s44
	v_and_b32_e32 v137, 0xffff0000, v137
	v_and_b32_e32 v138, 0xffff0000, v138
	v_or_b32_sdwa v137, v137, v134 dst_sel:DWORD dst_unused:UNUSED_PAD src0_sel:DWORD src1_sel:WORD_1
	v_or_b32_sdwa v136, v138, v136 dst_sel:DWORD dst_unused:UNUSED_PAD src0_sel:DWORD src1_sel:WORD_1
	global_store_dwordx2 v234, v[136:137], s[22:23] offset:2560 nt
	v_pk_mul_f32 v[136:137], v[48:49], v[48:49]
	v_pk_mul_f32 v[138:139], v[46:47], v[46:47]
	v_pk_mul_f32 v[160:161], v[160:161], v[166:167] op_sel_hi:[1,0]
	v_pk_mov_b32 v[140:141], v[138:139], v[136:137] op_sel:[1,0]
	v_mov_b32_e32 v139, v137
	v_pk_add_f32 v[136:137], v[138:139], v[140:141]
	v_pk_mul_f32 v[138:139], v[166:167], v[182:183] op_sel_hi:[0,1]
	v_pk_mul_f32 v[140:141], v[166:167], v[168:169] op_sel_hi:[0,1]
	v_pk_fma_f32 v[42:43], v[122:123], v[140:141], v[42:43]
	v_pk_fma_f32 v[44:45], v[124:125], v[138:139], v[44:45]
	v_pk_add_f32 v[136:137], v[136:137], v[136:137] op_sel_hi:[0,1]
	v_and_b32_sdwa v138, v45, v235 dst_sel:DWORD dst_unused:UNUSED_PAD src0_sel:WORD_1 src1_sel:DWORD
	v_and_b32_sdwa v139, v43, v235 dst_sel:DWORD dst_unused:UNUSED_PAD src0_sel:WORD_1 src1_sel:DWORD
	v_and_b32_sdwa v134, v44, v235 dst_sel:DWORD dst_unused:UNUSED_PAD src0_sel:WORD_1 src1_sel:DWORD
	v_and_b32_sdwa v136, v42, v235 dst_sel:DWORD dst_unused:UNUSED_PAD src0_sel:WORD_1 src1_sel:DWORD
	v_add3_u32 v138, v45, v138, s44
	v_add3_u32 v139, v43, v139, s44
	v_add3_u32 v136, v42, v136, s44
	v_add3_u32 v134, v44, v134, s44
	v_and_b32_e32 v138, 0xffff0000, v138
	v_and_b32_e32 v140, 0xffff0000, v139
	v_or_b32_sdwa v139, v138, v134 dst_sel:DWORD dst_unused:UNUSED_PAD src0_sel:DWORD src1_sel:WORD_1
	v_or_b32_sdwa v138, v140, v136 dst_sel:DWORD dst_unused:UNUSED_PAD src0_sel:DWORD src1_sel:WORD_1
	v_mul_f32_e32 v134, v42, v42
	global_store_dwordx2 v234, v[138:139], s[22:23] offset:3072 nt
	v_pk_fma_f32 v[138:139], v[42:43], v[42:43], v[134:135] op_sel_hi:[1,1,0]
	v_mul_f32_e32 v134, v44, v44
	v_pk_mul_f32 v[158:159], v[158:159], v[166:167] op_sel_hi:[1,0]
	s_waitcnt vmcnt(46)
	v_pk_fma_f32 v[38:39], v[126:127], v[160:161], v[38:39]
	v_pk_fma_f32 v[140:141], v[44:45], v[44:45], v[134:135] op_sel_hi:[1,1,0]
	v_pk_fma_f32 v[40:41], v[128:129], v[158:159], v[40:41]
	v_and_b32_sdwa v134, v38, v235 dst_sel:DWORD dst_unused:UNUSED_PAD src0_sel:WORD_1 src1_sel:DWORD
	v_add3_u32 v246, v38, v134, s44
	v_mul_f32_e32 v138, v38, v38
	v_mul_f32_e32 v140, v39, v39
	v_mul_f32_e32 v134, v40, v40
	v_mul_f32_e32 v136, v41, v41
	v_pk_add_f32 v[138:139], v[138:139], v[140:141]
	v_pk_add_f32 v[134:135], v[136:137], v[134:135]
	s_waitcnt vmcnt(21)
	v_and_b32_e32 v207, 0xffff0000, v220
	v_and_b32_e32 v209, 0xffff0000, v221
	v_pk_add_f32 v[158:159], v[138:139], v[134:135]
	v_lshlrev_b32_e32 v206, 16, v220
	v_lshlrev_b32_e32 v208, 16, v221
	v_mul_f32_e32 v134, v209, v209
	s_waitcnt vmcnt(19)
	v_and_b32_e32 v205, 0xffff0000, v223
	v_and_b32_e32 v204, 0xffff0000, v222
	v_mul_f32_e32 v138, v207, v207
	v_pk_fma_f32 v[134:135], v[208:209], v[208:209], v[134:135] op_sel_hi:[1,1,0]
	v_lshlrev_b32_e32 v203, 16, v223
	v_lshlrev_b32_e32 v202, 16, v222
	v_pk_mul_f32 v[136:137], v[204:205], v[204:205]
	s_waitcnt vmcnt(15)
	v_lshlrev_b32_e32 v191, 16, v238
	v_pk_fma_f32 v[138:139], v[206:207], v[206:207], v[138:139] op_sel_hi:[1,1,0]
	global_store_dwordx2 v234, v[188:189], s[22:23] offset:2048 nt
	v_pk_fma_f32 v[136:137], v[202:203], v[202:203], v[136:137]
	v_and_b32_e32 v189, 0xffff0000, v238
	v_mov_b32_e32 v190, v138
	v_mov_b32_e32 v140, v134
	v_mov_b32_e32 v141, v191
	v_mul_f32_e32 v160, v189, v189
	v_pk_add_f32 v[134:135], v[138:139], v[134:135]
	v_pk_mul_f32 v[138:139], v[190:191], v[140:141]
	v_pk_add_f32 v[136:137], v[136:137], v[136:137] op_sel:[0,1] op_sel_hi:[1,0]
	v_and_b32_e32 v199, 0xffff0000, v224
	v_and_b32_e32 v201, 0xffff0000, v225
	v_mov_b32_e32 v135, v139
	v_mov_b32_e32 v137, v160
	v_lshlrev_b32_e32 v198, 16, v224
	v_lshlrev_b32_e32 v200, 16, v225
	v_lshlrev_b32_e32 v196, 16, v239
	v_and_b32_e32 v197, 0xffff0000, v239
	v_pk_add_f32 v[134:135], v[134:135], v[136:137]
	v_mul_f32_e32 v136, v199, v199
	v_mul_f32_e32 v138, v201, v201
	v_mul_f32_e32 v161, v196, v196
	v_mul_f32_e32 v166, v197, v197
	v_pk_fma_f32 v[136:137], v[198:199], v[198:199], v[136:137] op_sel_hi:[1,1,0]
	v_pk_fma_f32 v[138:139], v[200:201], v[200:201], v[138:139] op_sel_hi:[1,1,0]
	v_mov_b32_e32 v137, v161
	v_mov_b32_e32 v139, v166
	v_pk_add_f32 v[136:137], v[136:137], v[138:139]
	s_waitcnt vmcnt(14)
	v_and_b32_e32 v195, 0xffff0000, v241
	v_and_b32_e32 v194, 0xffff0000, v240
	v_pk_add_f32 v[160:161], v[134:135], v[136:137]
	v_lshlrev_b32_e32 v193, 16, v241
	v_lshlrev_b32_e32 v192, 16, v240
	v_pk_mul_f32 v[134:135], v[194:195], v[194:195]
	s_waitcnt vmcnt(12)
	v_and_b32_e32 v187, 0xffff0000, v243
	v_pk_fma_f32 v[134:135], v[192:193], v[192:193], v[134:135]
	v_and_b32_e32 v186, 0xffff0000, v242
	v_pk_add_f32 v[166:167], v[134:135], v[134:135] op_sel:[0,1] op_sel_hi:[1,0]
	s_waitcnt vmcnt(8)
	v_lshlrev_b32_e32 v139, 16, v244
	v_pk_add_f32 v[160:161], v[160:161], v[160:161] op_sel:[0,1] op_sel_hi:[1,0]
	v_lshlrev_b32_e32 v185, 16, v243
	v_lshlrev_b32_e32 v184, 16, v242
	v_pk_mul_f32 v[134:135], v[186:187], v[186:187]
	v_lshlrev_b32_e32 v140, 16, v218
	v_and_b32_e32 v141, 0xffff0000, v218
	v_lshlrev_b32_e32 v182, 16, v219
	v_and_b32_e32 v183, 0xffff0000, v219
	v_mov_b32_e32 v138, v160
	v_mov_b32_e32 v218, v166
	v_mov_b32_e32 v219, v139
	v_pk_fma_f32 v[168:169], v[184:185], v[184:185], v[134:135]
	v_and_b32_e32 v137, 0xffff0000, v244
	v_pk_add_f32 v[160:161], v[160:161], v[166:167]
	v_pk_mul_f32 v[166:167], v[138:139], v[218:219]
	v_mul_f32_e32 v136, v137, v137
	v_mov_b32_e32 v161, v167
	v_pk_add_f32 v[166:167], v[168:169], v[168:169] op_sel:[0,1] op_sel_hi:[1,0]
	v_lshlrev_b32_e32 v134, 16, v245
	v_mov_b32_e32 v167, v136
	v_mul_f32_e32 v136, v141, v141
	v_and_b32_e32 v135, 0xffff0000, v245
	v_pk_add_f32 v[160:161], v[160:161], v[166:167]
	v_pk_fma_f32 v[166:167], v[140:141], v[140:141], v[136:137] op_sel_hi:[1,1,0]
	v_mul_f32_e32 v136, v183, v183
	v_mul_f32_e32 v190, v134, v134
	v_mul_f32_e32 v220, v135, v135
	v_pk_fma_f32 v[168:169], v[182:183], v[182:183], v[136:137] op_sel_hi:[1,1,0]
	v_mov_b32_e32 v167, v190
	v_mov_b32_e32 v169, v220
	v_pk_add_f32 v[166:167], v[166:167], v[168:169]
	v_and_b32_sdwa v138, v41, v235 dst_sel:DWORD dst_unused:UNUSED_PAD src0_sel:WORD_1 src1_sel:DWORD
	v_pk_add_f32 v[160:161], v[160:161], v[166:167]
	v_mov_b32_e32 v167, v158
	v_mov_b32_e32 v166, v160
	v_mov_b32_e32 v158, v161
	v_pk_add_f32 v[158:159], v[166:167], v[158:159]
	ds_bpermute_b32 v161, v171, v159
	ds_bpermute_b32 v160, v171, v158
	v_and_b32_sdwa v166, v39, v235 dst_sel:DWORD dst_unused:UNUSED_PAD src0_sel:WORD_1 src1_sel:DWORD
	s_addc_u32 s27, s13, s17
	v_and_b32_sdwa v188, v40, v235 dst_sel:DWORD dst_unused:UNUSED_PAD src0_sel:WORD_1 src1_sel:DWORD
	v_add3_u32 v138, v41, v138, s44
	s_waitcnt lgkmcnt(0)
	v_pk_add_f32 v[158:159], v[158:159], v[160:161]
	ds_bpermute_b32 v161, v226, v159
	ds_bpermute_b32 v160, v226, v158
	v_add3_u32 v166, v39, v166, s44
	s_add_u32 s28, s33, s14
	v_add3_u32 v136, v40, v188, s44
	v_and_b32_e32 v138, 0xffff0000, v138
	s_waitcnt lgkmcnt(0)
	v_pk_add_f32 v[158:159], v[158:159], v[160:161]
	ds_bpermute_b32 v161, v228, v159
	ds_bpermute_b32 v160, v228, v158
	v_and_b32_e32 v166, 0xffff0000, v166
	s_addc_u32 s29, s34, s15
	s_add_i32 s4, s8, -4
	v_or_b32_sdwa v167, v138, v136 dst_sel:DWORD dst_unused:UNUSED_PAD src0_sel:DWORD src1_sel:WORD_1
	s_waitcnt lgkmcnt(0)
	v_pk_add_f32 v[158:159], v[158:159], v[160:161]
	ds_bpermute_b32 v161, v229, v159
	ds_bpermute_b32 v160, v229, v158
	v_or_b32_sdwa v166, v166, v246 dst_sel:DWORD dst_unused:UNUSED_PAD src0_sel:DWORD src1_sel:WORD_1
	s_ashr_i32 s5, s4, 31
	global_store_dwordx2 v234, v[166:167], s[22:23] offset:3584 nt
	s_lshl_b64 s[14:15], s[4:5], 11
	s_waitcnt lgkmcnt(0)
	v_pk_add_f32 v[158:159], v[158:159], v[160:161]
	ds_bpermute_b32 v161, v230, v159
	ds_bpermute_b32 v160, v230, v158
	s_lshl_b64 s[22:23], s[4:5], 12
	s_add_u32 s24, s96, s22
	s_addc_u32 s25, s97, s23
	s_lshl_b64 s[4:5], s[4:5], 13
	s_waitcnt lgkmcnt(0)
	v_pk_add_f32 v[158:159], v[158:159], v[160:161]
	ds_bpermute_b32 v161, v231, v159
	ds_bpermute_b32 v160, v231, v158
	s_add_u32 s30, s6, s4
	s_addc_u32 s31, s7, s5
	v_mov_b32_e32 v168, 0
	v_lshl_add_u64 v[218:219], s[30:31], 0, v[178:179]
	s_waitcnt lgkmcnt(0)
	v_pk_add_f32 v[158:159], v[158:159], v[160:161]
	s_add_u32 s16, s35, s20
	v_pk_fma_f32 v[220:221], v[158:159], s[10:11], v[180:181] op_sel_hi:[1,0,0]
	s_addc_u32 s17, s36, s21
	v_mul_f32_e32 v136, 0x4b800000, v221
	v_cmp_gt_f32_e64 s[4:5], s43, v221
	v_cmp_gt_f32_e32 vcc, s43, v220
	s_nop 0
	v_cndmask_b32_e64 v136, v221, v136, s[4:5]
	v_rsq_f32_e32 v136, v136
	s_nop 0
	v_mul_f32_e32 v138, 0x45800000, v136
	v_cndmask_b32_e64 v136, v136, v138, s[4:5]
	v_pk_mul_f32 v[158:159], v[214:215], v[136:137] op_sel_hi:[1,0]
	v_pk_mul_f32 v[160:161], v[216:217], v[136:137] op_sel_hi:[1,0]
	v_pk_fma_f32 v[158:159], v[26:27], v[158:159], v[30:31]
	v_pk_fma_f32 v[160:161], v[28:29], v[160:161], v[32:33]
	v_bfe_u32 v138, v158, 16, 1
	v_bfe_u32 v166, v159, 16, 1
	v_add3_u32 v138, v158, v138, s44
	v_add3_u32 v166, v159, v166, s44
	v_med3_f32 v158, v158, s45, v236
	v_med3_f32 v159, v159, s45, v236
	v_lshrrev_b32_e32 v138, 16, v138
	v_cvt_pk_fp8_f32 v168, v158, v159
	v_and_or_b32 v166, v166, s42, v138
	v_bfe_u32 v138, v160, 16, 1
	v_add3_u32 v138, v160, v138, s44
	v_bfe_u32 v158, v161, 16, 1
	v_lshrrev_b32_e32 v138, 16, v138
	v_med3_f32 v159, v160, s45, v236
	v_med3_f32 v160, v161, s45, v236
	v_add3_u32 v158, v161, v158, s44
	v_cvt_pk_fp8_f32 v168, v159, v160 op_sel:[0,0,1]
	v_and_or_b32 v167, v158, s42, v138
	v_pk_mul_f32 v[158:159], v[210:211], v[136:137] op_sel_hi:[1,0]
	global_store_dwordx2 v234, v[166:167], s[26:27]
	global_store_dword v237, v168, s[28:29]
	v_pk_fma_f32 v[158:159], v[90:91], v[158:159], v[94:95]
	v_pk_mul_f32 v[160:161], v[212:213], v[136:137] op_sel_hi:[1,0]
	v_bfe_u32 v138, v158, 16, 1
	v_add3_u32 v138, v158, v138, s44
	v_bfe_u32 v166, v159, 16, 1
	v_pk_fma_f32 v[160:161], v[92:93], v[160:161], v[96:97]
	v_lshrrev_b32_e32 v138, 16, v138
	v_add3_u32 v166, v159, v166, s44
	v_med3_f32 v158, v158, s45, v236
	v_med3_f32 v159, v159, s45, v236
	v_mov_b32_e32 v168, 0
	v_and_or_b32 v166, v166, s42, v138
	v_bfe_u32 v138, v160, 16, 1
	v_cvt_pk_fp8_f32 v168, v158, v159
	v_add3_u32 v138, v160, v138, s44
	v_bfe_u32 v158, v161, 16, 1
	v_pk_mul_f32 v[66:67], v[66:67], v[136:137] op_sel_hi:[1,0]
	v_lshrrev_b32_e32 v138, 16, v138
	v_add3_u32 v158, v161, v158, s44
	v_pk_fma_f32 v[66:67], v[82:83], v[66:67], v[86:87]
	v_med3_f32 v159, v160, s45, v236
	v_med3_f32 v160, v161, s45, v236
	v_and_or_b32 v167, v158, s42, v138
	v_bfe_u32 v138, v66, 16, 1
	v_bfe_u32 v158, v67, 16, 1
	v_cvt_pk_fp8_f32 v168, v159, v160 op_sel:[0,0,1]
	v_pk_mul_f32 v[68:69], v[68:69], v[136:137] op_sel_hi:[1,0]
	v_add3_u32 v138, v66, v138, s44
	v_add3_u32 v158, v67, v158, s44
	v_med3_f32 v66, v66, s45, v236
	v_med3_f32 v67, v67, s45, v236
	v_mov_b32_e32 v160, 0
	v_pk_fma_f32 v[68:69], v[84:85], v[68:69], v[88:89]
	v_lshrrev_b32_e32 v138, 16, v138
	v_cvt_pk_fp8_f32 v160, v66, v67
	v_and_or_b32 v158, v158, s42, v138
	v_bfe_u32 v138, v68, 16, 1
	v_add3_u32 v138, v68, v138, s44
	v_bfe_u32 v66, v69, 16, 1
	v_pk_mul_f32 v[58:59], v[58:59], v[136:137] op_sel_hi:[1,0]
	v_lshrrev_b32_e32 v138, 16, v138
	v_med3_f32 v67, v68, s45, v236
	v_med3_f32 v68, v69, s45, v236
	v_add3_u32 v66, v69, v66, s44
	v_pk_fma_f32 v[58:59], v[74:75], v[58:59], v[78:79]
	v_cvt_pk_fp8_f32 v160, v67, v68 op_sel:[0,0,1]
	v_and_or_b32 v159, v66, s42, v138
	v_bfe_u32 v66, v58, 16, 1
	v_bfe_u32 v67, v59, 16, 1
	v_pk_mul_f32 v[60:61], v[60:61], v[136:137] op_sel_hi:[1,0]
	v_add3_u32 v66, v58, v66, s44
	v_add3_u32 v67, v59, v67, s44
	v_med3_f32 v58, v58, s45, v236
	v_med3_f32 v59, v59, s45, v236
	v_mov_b32_e32 v68, 0
	v_pk_fma_f32 v[60:61], v[76:77], v[60:61], v[80:81]
	v_lshrrev_b32_e32 v66, 16, v66
	v_cvt_pk_fp8_f32 v68, v58, v59
	v_and_or_b32 v66, v67, s42, v66
	v_bfe_u32 v67, v60, 16, 1
	v_add3_u32 v67, v60, v67, s44
	v_bfe_u32 v58, v61, 16, 1
	v_pk_mul_f32 v[54:55], v[54:55], v[136:137] op_sel_hi:[1,0]
	v_lshrrev_b32_e32 v67, 16, v67
	v_med3_f32 v59, v60, s45, v236
	v_med3_f32 v60, v61, s45, v236
	v_add3_u32 v58, v61, v58, s44
	v_pk_fma_f32 v[54:55], v[34:35], v[54:55], v[70:71]
	v_cvt_pk_fp8_f32 v68, v59, v60 op_sel:[0,0,1]
	v_and_or_b32 v67, v58, s42, v67
	v_bfe_u32 v58, v54, 16, 1
	v_bfe_u32 v59, v55, 16, 1
	v_pk_mul_f32 v[56:57], v[56:57], v[136:137] op_sel_hi:[1,0]
	v_add3_u32 v58, v54, v58, s44
	v_add3_u32 v59, v55, v59, s44
	v_med3_f32 v54, v54, s45, v236
	v_med3_f32 v55, v55, s45, v236
	v_mov_b32_e32 v60, 0
	v_pk_fma_f32 v[56:57], v[36:37], v[56:57], v[72:73]
	v_lshrrev_b32_e32 v58, 16, v58
	v_cvt_pk_fp8_f32 v60, v54, v55
	v_and_or_b32 v58, v59, s42, v58
	v_bfe_u32 v59, v56, 16, 1
	v_add3_u32 v59, v56, v59, s44
	v_bfe_u32 v54, v57, 16, 1
	v_pk_mul_f32 v[46:47], v[46:47], v[136:137] op_sel_hi:[1,0]
	v_lshrrev_b32_e32 v59, 16, v59
	v_med3_f32 v55, v56, s45, v236
	v_med3_f32 v56, v57, s45, v236
	v_add3_u32 v54, v57, v54, s44
	v_pk_fma_f32 v[46:47], v[18:19], v[46:47], v[22:23]
	v_cvt_pk_fp8_f32 v60, v55, v56 op_sel:[0,0,1]
	v_and_or_b32 v59, v54, s42, v59
	v_bfe_u32 v54, v46, 16, 1
	v_bfe_u32 v55, v47, 16, 1
	v_pk_mul_f32 v[48:49], v[48:49], v[136:137] op_sel_hi:[1,0]
	v_add3_u32 v54, v46, v54, s44
	v_add3_u32 v55, v47, v55, s44
	v_med3_f32 v46, v46, s45, v236
	v_med3_f32 v47, v47, s45, v236
	v_mov_b32_e32 v56, 0
	v_pk_fma_f32 v[48:49], v[20:21], v[48:49], v[24:25]
	v_lshrrev_b32_e32 v54, 16, v54
	v_cvt_pk_fp8_f32 v56, v46, v47
	v_and_or_b32 v54, v55, s42, v54
	v_bfe_u32 v55, v48, 16, 1
	v_add3_u32 v55, v48, v55, s44
	v_bfe_u32 v46, v49, 16, 1
	v_pk_mul_f32 v[42:43], v[42:43], v[136:137] op_sel_hi:[1,0]
	v_lshrrev_b32_e32 v55, 16, v55
	v_med3_f32 v47, v48, s45, v236
	v_med3_f32 v48, v49, s45, v236
	v_add3_u32 v46, v49, v46, s44
	v_pk_fma_f32 v[42:43], v[10:11], v[42:43], v[14:15]
	v_cvt_pk_fp8_f32 v56, v47, v48 op_sel:[0,0,1]
	v_and_or_b32 v55, v46, s42, v55
	v_bfe_u32 v46, v42, 16, 1
	v_bfe_u32 v47, v43, 16, 1
	v_pk_mul_f32 v[44:45], v[44:45], v[136:137] op_sel_hi:[1,0]
	v_add3_u32 v46, v42, v46, s44
	v_add3_u32 v47, v43, v47, s44
	v_med3_f32 v42, v42, s45, v236
	v_med3_f32 v43, v43, s45, v236
	v_mov_b32_e32 v48, 0
	v_pk_fma_f32 v[44:45], v[12:13], v[44:45], v[16:17]
	v_lshrrev_b32_e32 v46, 16, v46
	v_cvt_pk_fp8_f32 v48, v42, v43
	v_and_or_b32 v46, v47, s42, v46
	v_bfe_u32 v47, v44, 16, 1
	v_add3_u32 v47, v44, v47, s44
	v_bfe_u32 v42, v45, 16, 1
	v_pk_mul_f32 v[38:39], v[38:39], v[136:137] op_sel_hi:[1,0]
	v_lshrrev_b32_e32 v47, 16, v47
	v_med3_f32 v43, v44, s45, v236
	v_med3_f32 v44, v45, s45, v236
	v_add3_u32 v42, v45, v42, s44
	v_pk_fma_f32 v[38:39], v[2:3], v[38:39], v[6:7]
	v_cvt_pk_fp8_f32 v48, v43, v44 op_sel:[0,0,1]
	v_and_or_b32 v47, v42, s42, v47
	v_bfe_u32 v42, v38, 16, 1
	v_bfe_u32 v43, v39, 16, 1
	v_add3_u32 v42, v38, v42, s44
	v_add3_u32 v43, v39, v43, s44
	v_med3_f32 v38, v38, s45, v236
	v_med3_f32 v39, v39, s45, v236
	v_mov_b32_e32 v44, 0
	v_pk_mul_f32 v[40:41], v[40:41], v[136:137] op_sel_hi:[1,0]
	v_cvt_pk_fp8_f32 v44, v38, v39
	v_pk_fma_f32 v[40:41], v[4:5], v[40:41], v[8:9]
	v_lshrrev_b32_e32 v42, 16, v42
	v_and_or_b32 v42, v43, s42, v42
	v_bfe_u32 v43, v40, 16, 1
	v_add3_u32 v43, v40, v43, s44
	v_med3_f32 v39, v40, s45, v236
	v_med3_f32 v40, v41, s45, v236
	v_bfe_u32 v38, v41, 16, 1
	v_cvt_pk_fp8_f32 v44, v39, v40 op_sel:[0,0,1]
	v_lshrrev_b32_e32 v43, 16, v43
	v_add3_u32 v38, v41, v38, s44
	v_and_or_b32 v43, v38, s42, v43
	global_store_dwordx2 v234, v[166:167], s[26:27] offset:512
	global_store_dword v237, v168, s[28:29] offset:256
	global_store_dwordx2 v234, v[158:159], s[26:27] offset:1024
	global_store_dword v237, v160, s[28:29] offset:512
	global_store_dwordx2 v234, v[66:67], s[26:27] offset:1536
	global_store_dword v237, v68, s[28:29] offset:768
	global_store_dwordx2 v234, v[58:59], s[26:27] offset:2048
	global_store_dword v237, v60, s[28:29] offset:1024
	global_store_dwordx2 v234, v[54:55], s[26:27] offset:2560
	global_store_dword v237, v56, s[28:29] offset:1280
	global_store_dwordx2 v234, v[46:47], s[26:27] offset:3072
	global_store_dword v237, v48, s[28:29] offset:1536
	global_store_dwordx2 v234, v[42:43], s[26:27] offset:3584
	global_store_dword v237, v44, s[28:29] offset:1792
	global_load_dwordx2 v[222:223], v234, s[24:25]
	global_load_dwordx4 v[166:169], v178, s[30:31]
	global_load_dwordx2 v[224:225], v234, s[24:25] offset:512
	global_load_dwordx4 v[158:161], v178, s[30:31] offset:1024
	global_load_dwordx2 v[238:239], v234, s[24:25] offset:1024
	global_load_dwordx4 v[66:69], v178, s[30:31] offset:2048
	global_load_dwordx2 v[240:241], v234, s[24:25] offset:1536
	global_load_dwordx4 v[58:61], v178, s[30:31] offset:3072
	global_load_dwordx2 v[242:243], v234, s[24:25] offset:2048
	v_add_co_u32_e64 v38, s[4:5], s41, v218
	v_mul_f32_e32 v40, 0x4b800000, v220
	s_nop 0
	v_addc_co_u32_e64 v39, s[4:5], 0, v219, s[4:5]
	v_cndmask_b32_e32 v40, v220, v40, vcc
	global_load_dwordx4 v[54:57], v[38:39], off
	global_load_dwordx2 v[218:219], v234, s[24:25] offset:2560
	global_load_dwordx4 v[46:49], v[38:39], off offset:1024
	global_load_dwordx2 v[216:217], v234, s[24:25] offset:3072
	v_rsq_f32_e32 v136, v40
	global_load_dwordx4 v[42:45], v[38:39], off offset:2048
	global_load_dwordx2 v[220:221], v234, s[24:25] offset:3584
	s_nop 0
	global_load_dwordx4 v[38:41], v[38:39], off offset:3072
	s_add_u32 s26, s11, s20
	s_addc_u32 s27, s13, s21
	v_mul_f32_e32 v138, 0x45800000, v136
	v_cndmask_b32_e32 v138, v136, v138, vcc
	v_pk_mul_f32 v[208:209], v[138:139], v[208:209] op_sel_hi:[0,1]
	v_pk_mul_f32 v[206:207], v[138:139], v[206:207] op_sel_hi:[0,1]
	v_pk_fma_f32 v[162:163], v[98:99], v[206:207], v[162:163]
	v_pk_fma_f32 v[164:165], v[100:101], v[208:209], v[164:165]
	v_and_b32_sdwa v206, v163, v235 dst_sel:DWORD dst_unused:UNUSED_PAD src0_sel:WORD_1 src1_sel:DWORD
	v_and_b32_sdwa v190, v165, v235 dst_sel:DWORD dst_unused:UNUSED_PAD src0_sel:WORD_1 src1_sel:DWORD
	v_and_b32_sdwa v136, v164, v235 dst_sel:DWORD dst_unused:UNUSED_PAD src0_sel:WORD_1 src1_sel:DWORD
	v_and_b32_sdwa v188, v162, v235 dst_sel:DWORD dst_unused:UNUSED_PAD src0_sel:WORD_1 src1_sel:DWORD
	v_add3_u32 v190, v165, v190, s44
	v_add3_u32 v206, v163, v206, s44
	v_add3_u32 v188, v162, v188, s44
	v_add3_u32 v136, v164, v136, s44
	v_and_b32_e32 v190, 0xffff0000, v190
	v_and_b32_e32 v206, 0xffff0000, v206
	v_or_b32_sdwa v207, v190, v136 dst_sel:DWORD dst_unused:UNUSED_PAD src0_sel:DWORD src1_sel:WORD_1
	v_or_b32_sdwa v206, v206, v188 dst_sel:DWORD dst_unused:UNUSED_PAD src0_sel:DWORD src1_sel:WORD_1
	global_store_dwordx2 v234, v[206:207], s[16:17] nt
	v_mov_b32_e32 v206, v203
	v_mov_b32_e32 v203, v204
	v_mov_b32_e32 v207, v205
	v_pk_mul_f32 v[202:203], v[138:139], v[202:203] op_sel_hi:[0,1]
	v_pk_mul_f32 v[206:207], v[138:139], v[206:207] op_sel_hi:[0,1]
	v_pk_fma_f32 v[154:155], v[102:103], v[202:203], v[154:155]
	v_pk_fma_f32 v[156:157], v[104:105], v[206:207], v[156:157]
	v_and_b32_sdwa v202, v155, v235 dst_sel:DWORD dst_unused:UNUSED_PAD src0_sel:WORD_1 src1_sel:DWORD
	v_and_b32_sdwa v188, v154, v235 dst_sel:DWORD dst_unused:UNUSED_PAD src0_sel:WORD_1 src1_sel:DWORD
	v_and_b32_sdwa v190, v157, v235 dst_sel:DWORD dst_unused:UNUSED_PAD src0_sel:WORD_1 src1_sel:DWORD
	v_add3_u32 v202, v155, v202, s44
	v_pk_mul_f32 v[200:201], v[138:139], v[200:201] op_sel_hi:[0,1]
	v_pk_mul_f32 v[198:199], v[138:139], v[198:199] op_sel_hi:[0,1]
	v_and_b32_sdwa v136, v156, v235 dst_sel:DWORD dst_unused:UNUSED_PAD src0_sel:WORD_1 src1_sel:DWORD
	v_add3_u32 v188, v154, v188, s44
	v_add3_u32 v190, v157, v190, s44
	v_and_b32_e32 v202, 0xffff0000, v202
	v_pk_fma_f32 v[210:211], v[106:107], v[198:199], v[150:151]
	v_pk_fma_f32 v[152:153], v[108:109], v[200:201], v[152:153]
	v_add3_u32 v136, v156, v136, s44
	v_and_b32_e32 v190, 0xffff0000, v190
	v_or_b32_sdwa v202, v202, v188 dst_sel:DWORD dst_unused:UNUSED_PAD src0_sel:DWORD src1_sel:WORD_1
	v_and_b32_sdwa v151, v153, v235 dst_sel:DWORD dst_unused:UNUSED_PAD src0_sel:WORD_1 src1_sel:DWORD
	v_and_b32_sdwa v188, v211, v235 dst_sel:DWORD dst_unused:UNUSED_PAD src0_sel:WORD_1 src1_sel:DWORD
	v_or_b32_sdwa v203, v190, v136 dst_sel:DWORD dst_unused:UNUSED_PAD src0_sel:DWORD src1_sel:WORD_1
	v_and_b32_sdwa v136, v152, v235 dst_sel:DWORD dst_unused:UNUSED_PAD src0_sel:WORD_1 src1_sel:DWORD
	v_and_b32_sdwa v150, v210, v235 dst_sel:DWORD dst_unused:UNUSED_PAD src0_sel:WORD_1 src1_sel:DWORD
	v_add3_u32 v151, v153, v151, s44
	v_add3_u32 v188, v211, v188, s44
	v_add3_u32 v150, v210, v150, s44
	v_add3_u32 v136, v152, v136, s44
	v_and_b32_e32 v151, 0xffff0000, v151
	v_and_b32_e32 v188, 0xffff0000, v188
	v_or_b32_sdwa v151, v151, v136 dst_sel:DWORD dst_unused:UNUSED_PAD src0_sel:DWORD src1_sel:WORD_1
	v_or_b32_sdwa v150, v188, v150 dst_sel:DWORD dst_unused:UNUSED_PAD src0_sel:DWORD src1_sel:WORD_1
	global_store_dwordx2 v234, v[150:151], s[16:17] offset:1024 nt
	v_pk_mul_f32 v[150:151], v[152:153], v[152:153]
	v_pk_mul_f32 v[198:199], v[210:211], v[210:211]
	v_mov_b32_e32 v188, v191
	v_pk_mov_b32 v[200:201], v[198:199], v[150:151] op_sel:[1,0]
	v_mov_b32_e32 v199, v151
	v_pk_mul_f32 v[196:197], v[196:197], v[138:139] op_sel_hi:[1,0]
	v_pk_mul_f32 v[188:189], v[188:189], v[138:139] op_sel_hi:[1,0]
	v_pk_add_f32 v[150:151], v[198:199], v[200:201]
	v_pk_fma_f32 v[146:147], v[110:111], v[188:189], v[146:147]
	v_pk_fma_f32 v[148:149], v[112:113], v[196:197], v[148:149]
	v_pk_add_f32 v[150:151], v[150:151], v[150:151] op_sel_hi:[0,1]
	v_and_b32_sdwa v188, v149, v235 dst_sel:DWORD dst_unused:UNUSED_PAD src0_sel:WORD_1 src1_sel:DWORD
	v_and_b32_sdwa v189, v147, v235 dst_sel:DWORD dst_unused:UNUSED_PAD src0_sel:WORD_1 src1_sel:DWORD
	v_and_b32_sdwa v136, v148, v235 dst_sel:DWORD dst_unused:UNUSED_PAD src0_sel:WORD_1 src1_sel:DWORD
	v_and_b32_sdwa v150, v146, v235 dst_sel:DWORD dst_unused:UNUSED_PAD src0_sel:WORD_1 src1_sel:DWORD
	v_add3_u32 v188, v149, v188, s44
	v_add3_u32 v189, v147, v189, s44
	v_mov_b32_e32 v204, v163
	v_mov_b32_e32 v205, v155
	v_add3_u32 v150, v146, v150, s44
	v_add3_u32 v136, v148, v136, s44
	v_and_b32_e32 v188, 0xffff0000, v188
	v_and_b32_e32 v190, 0xffff0000, v189
	global_store_dwordx2 v234, v[202:203], s[16:17] offset:512 nt
	v_mov_b32_e32 v202, v162
	v_mov_b32_e32 v203, v154
	v_pk_mul_f32 v[204:205], v[204:205], v[204:205]
	v_or_b32_sdwa v189, v188, v136 dst_sel:DWORD dst_unused:UNUSED_PAD src0_sel:DWORD src1_sel:WORD_1
	v_or_b32_sdwa v188, v190, v150 dst_sel:DWORD dst_unused:UNUSED_PAD src0_sel:DWORD src1_sel:WORD_1
	v_mul_f32_e32 v136, v146, v146
	v_mov_b32_e32 v196, v192
	v_mov_b32_e32 v197, v194
	v_mov_b32_e32 v194, v193
	v_pk_fma_f32 v[202:203], v[202:203], v[202:203], v[204:205]
	v_mov_b32_e32 v204, v164
	v_mov_b32_e32 v205, v156
	global_store_dwordx2 v234, v[188:189], s[16:17] offset:1536 nt
	v_pk_fma_f32 v[188:189], v[146:147], v[146:147], v[136:137] op_sel_hi:[1,1,0]
	v_mul_f32_e32 v136, v148, v148
	v_pk_mul_f32 v[196:197], v[138:139], v[196:197] op_sel_hi:[0,1]
	v_pk_mul_f32 v[192:193], v[138:139], v[194:195] op_sel_hi:[0,1]
	v_pk_mul_f32 v[204:205], v[204:205], v[204:205]
	v_mov_b32_e32 v206, v165
	v_mov_b32_e32 v207, v157
	v_pk_fma_f32 v[190:191], v[148:149], v[148:149], v[136:137] op_sel_hi:[1,1,0]
	v_pk_fma_f32 v[144:145], v[116:117], v[192:193], v[144:145]
	v_pk_fma_f32 v[142:143], v[114:115], v[196:197], v[142:143]
	v_pk_fma_f32 v[204:205], v[206:207], v[206:207], v[204:205]
	v_and_b32_sdwa v188, v145, v235 dst_sel:DWORD dst_unused:UNUSED_PAD src0_sel:WORD_1 src1_sel:DWORD
	v_and_b32_sdwa v190, v143, v235 dst_sel:DWORD dst_unused:UNUSED_PAD src0_sel:WORD_1 src1_sel:DWORD
	v_pk_add_f32 v[202:203], v[202:203], v[204:205]
	v_and_b32_sdwa v136, v144, v235 dst_sel:DWORD dst_unused:UNUSED_PAD src0_sel:WORD_1 src1_sel:DWORD
	v_and_b32_sdwa v150, v142, v235 dst_sel:DWORD dst_unused:UNUSED_PAD src0_sel:WORD_1 src1_sel:DWORD
	v_add3_u32 v188, v145, v188, s44
	v_add3_u32 v190, v143, v190, s44
	v_pk_add_f32 v[202:203], v[202:203], v[202:203] op_sel_hi:[0,1]
	v_add3_u32 v150, v142, v150, s44
	v_add3_u32 v136, v144, v136, s44
	v_and_b32_e32 v188, 0xffff0000, v188
	v_and_b32_e32 v190, 0xffff0000, v190
	v_or_b32_sdwa v193, v188, v136 dst_sel:DWORD dst_unused:UNUSED_PAD src0_sel:DWORD src1_sel:WORD_1
	v_or_b32_sdwa v192, v190, v150 dst_sel:DWORD dst_unused:UNUSED_PAD src0_sel:DWORD src1_sel:WORD_1
	v_mul_f32_e32 v188, v142, v142
	v_mul_f32_e32 v190, v143, v143
	v_mul_f32_e32 v202, v144, v144
	v_mul_f32_e32 v150, v145, v145
	v_pk_add_f32 v[188:189], v[188:189], v[190:191]
	v_pk_add_f32 v[150:151], v[150:151], v[202:203]
	v_mov_b32_e32 v136, v139
	v_pk_add_f32 v[150:151], v[188:189], v[150:151]
	s_waitcnt vmcnt(19)
	v_and_b32_e32 v207, 0xffff0000, v222
	v_pk_add_f32 v[188:189], v[150:151], v[150:151] op_sel_hi:[0,1]
	v_mov_b32_e32 v150, v185
	v_mov_b32_e32 v185, v186
	v_mov_b32_e32 v151, v187
	v_pk_mul_f32 v[184:185], v[138:139], v[184:185] op_sel_hi:[0,1]
	v_pk_mul_f32 v[150:151], v[138:139], v[150:151] op_sel_hi:[0,1]
	v_pk_fma_f32 v[212:213], v[118:119], v[184:185], v[130:131]
	v_pk_fma_f32 v[214:215], v[120:121], v[150:151], v[132:133]
	v_and_b32_sdwa v131, v212, v235 dst_sel:DWORD dst_unused:UNUSED_PAD src0_sel:WORD_1 src1_sel:DWORD
	v_add3_u32 v132, v212, v131, s44
	v_and_b32_sdwa v131, v215, v235 dst_sel:DWORD dst_unused:UNUSED_PAD src0_sel:WORD_1 src1_sel:DWORD
	v_and_b32_sdwa v133, v213, v235 dst_sel:DWORD dst_unused:UNUSED_PAD src0_sel:WORD_1 src1_sel:DWORD
	v_and_b32_sdwa v130, v214, v235 dst_sel:DWORD dst_unused:UNUSED_PAD src0_sel:WORD_1 src1_sel:DWORD
	v_add3_u32 v131, v215, v131, s44
	v_add3_u32 v133, v213, v133, s44
	v_add3_u32 v130, v214, v130, s44
	v_and_b32_e32 v131, 0xffff0000, v131
	v_and_b32_e32 v133, 0xffff0000, v133
	v_or_b32_sdwa v131, v131, v130 dst_sel:DWORD dst_unused:UNUSED_PAD src0_sel:DWORD src1_sel:WORD_1
	v_or_b32_sdwa v130, v133, v132 dst_sel:DWORD dst_unused:UNUSED_PAD src0_sel:DWORD src1_sel:WORD_1
	global_store_dwordx2 v234, v[130:131], s[16:17] offset:2560 nt
	v_pk_mul_f32 v[130:131], v[214:215], v[214:215]
	v_pk_mul_f32 v[132:133], v[212:213], v[212:213]
	v_and_b32_e32 v209, 0xffff0000, v223
	v_pk_mov_b32 v[150:151], v[132:133], v[130:131] op_sel:[1,0]
	v_mov_b32_e32 v133, v131
	v_pk_add_f32 v[130:131], v[132:133], v[150:151]
	v_pk_mul_f32 v[132:133], v[138:139], v[140:141] op_sel_hi:[0,1]
	v_pk_add_f32 v[184:185], v[130:131], v[130:131] op_sel_hi:[0,1]
	v_pk_mul_f32 v[130:131], v[138:139], v[182:183] op_sel_hi:[0,1]
	v_pk_fma_f32 v[140:141], v[122:123], v[132:133], v[62:63]
	v_pk_fma_f32 v[150:151], v[124:125], v[130:131], v[64:65]
	v_and_b32_sdwa v63, v140, v235 dst_sel:DWORD dst_unused:UNUSED_PAD src0_sel:WORD_1 src1_sel:DWORD
	v_add3_u32 v64, v140, v63, s44
	v_and_b32_sdwa v63, v151, v235 dst_sel:DWORD dst_unused:UNUSED_PAD src0_sel:WORD_1 src1_sel:DWORD
	v_and_b32_sdwa v65, v141, v235 dst_sel:DWORD dst_unused:UNUSED_PAD src0_sel:WORD_1 src1_sel:DWORD
	v_and_b32_sdwa v62, v150, v235 dst_sel:DWORD dst_unused:UNUSED_PAD src0_sel:WORD_1 src1_sel:DWORD
	v_add3_u32 v63, v151, v63, s44
	v_add3_u32 v65, v141, v65, s44
	v_add3_u32 v62, v150, v62, s44
	v_and_b32_e32 v63, 0xffff0000, v63
	v_and_b32_e32 v65, 0xffff0000, v65
	v_or_b32_sdwa v63, v63, v62 dst_sel:DWORD dst_unused:UNUSED_PAD src0_sel:DWORD src1_sel:WORD_1
	v_or_b32_sdwa v62, v65, v64 dst_sel:DWORD dst_unused:UNUSED_PAD src0_sel:DWORD src1_sel:WORD_1
	global_store_dwordx2 v234, v[62:63], s[16:17] offset:3072 nt
	v_mul_f32_e32 v62, v140, v140
	v_pk_fma_f32 v[62:63], v[140:141], v[140:141], v[62:63] op_sel_hi:[1,1,0]
	v_pk_mul_f32 v[132:133], v[136:137], v[138:139] op_sel_hi:[1,0]
	v_mul_f32_e32 v62, v150, v150
	v_pk_mul_f32 v[130:131], v[134:135], v[138:139] op_sel_hi:[1,0]
	v_pk_fma_f32 v[64:65], v[150:151], v[150:151], v[62:63] op_sel_hi:[1,1,0]
	v_pk_fma_f32 v[130:131], v[128:129], v[130:131], v[52:53]
	v_pk_fma_f32 v[132:133], v[126:127], v[132:133], v[50:51]
	v_mul_f32_e32 v188, v130, v130
	v_and_b32_sdwa v50, v132, v235 dst_sel:DWORD dst_unused:UNUSED_PAD src0_sel:WORD_1 src1_sel:DWORD
	v_mul_f32_e32 v62, v132, v132
	v_mul_f32_e32 v64, v133, v133
	v_mul_f32_e32 v184, v131, v131
	v_add3_u32 v245, v132, v50, s44
	v_pk_add_f32 v[50:51], v[62:63], v[64:65]
	v_pk_add_f32 v[52:53], v[184:185], v[188:189]
	v_lshlrev_b32_e32 v206, 16, v222
	v_pk_add_f32 v[134:135], v[50:51], v[52:53]
	v_lshlrev_b32_e32 v208, 16, v223
	v_mul_f32_e32 v50, v209, v209
	s_waitcnt vmcnt(19)
	v_and_b32_e32 v205, 0xffff0000, v225
	v_and_b32_e32 v204, 0xffff0000, v224
	v_mul_f32_e32 v62, v207, v207
	v_pk_fma_f32 v[50:51], v[208:209], v[208:209], v[50:51] op_sel_hi:[1,1,0]
	v_lshlrev_b32_e32 v203, 16, v225
	v_lshlrev_b32_e32 v202, 16, v224
	v_pk_mul_f32 v[52:53], v[204:205], v[204:205]
	s_waitcnt vmcnt(15)
	v_lshlrev_b32_e32 v191, 16, v240
	v_pk_fma_f32 v[62:63], v[206:207], v[206:207], v[62:63] op_sel_hi:[1,1,0]
	v_pk_fma_f32 v[52:53], v[202:203], v[202:203], v[52:53]
	v_and_b32_e32 v189, 0xffff0000, v240
	v_mov_b32_e32 v190, v62
	v_mov_b32_e32 v64, v50
	v_mov_b32_e32 v65, v191
	v_mul_f32_e32 v136, v189, v189
	v_pk_add_f32 v[50:51], v[62:63], v[50:51]
	v_pk_mul_f32 v[62:63], v[190:191], v[64:65]
	v_pk_add_f32 v[52:53], v[52:53], v[52:53] op_sel:[0,1] op_sel_hi:[1,0]
	v_and_b32_e32 v199, 0xffff0000, v238
	v_and_b32_e32 v201, 0xffff0000, v239
	v_mov_b32_e32 v51, v63
	v_mov_b32_e32 v53, v136
	v_lshlrev_b32_e32 v198, 16, v238
	v_lshlrev_b32_e32 v200, 16, v239
	v_lshlrev_b32_e32 v196, 16, v241
	v_and_b32_e32 v197, 0xffff0000, v241
	v_pk_add_f32 v[50:51], v[50:51], v[52:53]
	v_mul_f32_e32 v52, v199, v199
	v_mul_f32_e32 v62, v201, v201
	v_mul_f32_e32 v137, v196, v196
	v_mul_f32_e32 v138, v197, v197
	v_pk_fma_f32 v[52:53], v[198:199], v[198:199], v[52:53] op_sel_hi:[1,1,0]
	v_pk_fma_f32 v[62:63], v[200:201], v[200:201], v[62:63] op_sel_hi:[1,1,0]
	v_mov_b32_e32 v53, v137
	v_mov_b32_e32 v63, v138
	v_pk_add_f32 v[52:53], v[52:53], v[62:63]
	s_waitcnt vmcnt(13)
	v_and_b32_e32 v195, 0xffff0000, v243
	v_and_b32_e32 v194, 0xffff0000, v242
	global_store_dwordx2 v234, v[192:193], s[16:17] offset:2048 nt
	v_pk_add_f32 v[136:137], v[50:51], v[52:53]
	v_lshlrev_b32_e32 v193, 16, v243
	v_lshlrev_b32_e32 v192, 16, v242
	v_pk_mul_f32 v[50:51], v[194:195], v[194:195]
	s_waitcnt vmcnt(12)
	v_and_b32_e32 v187, 0xffff0000, v219
	v_pk_fma_f32 v[50:51], v[192:193], v[192:193], v[50:51]
	v_and_b32_e32 v186, 0xffff0000, v218
	v_pk_add_f32 v[138:139], v[50:51], v[50:51] op_sel:[0,1] op_sel_hi:[1,0]
	s_waitcnt vmcnt(8)
	v_lshlrev_b32_e32 v63, 16, v220
	v_pk_add_f32 v[136:137], v[136:137], v[136:137] op_sel:[0,1] op_sel_hi:[1,0]
	v_lshlrev_b32_e32 v185, 16, v219
	v_lshlrev_b32_e32 v184, 16, v218
	v_pk_mul_f32 v[50:51], v[186:187], v[186:187]
	v_lshlrev_b32_e32 v64, 16, v216
	v_and_b32_e32 v65, 0xffff0000, v216
	v_lshlrev_b32_e32 v182, 16, v217
	v_and_b32_e32 v183, 0xffff0000, v217
	v_mov_b32_e32 v62, v136
	v_mov_b32_e32 v216, v138
	v_mov_b32_e32 v217, v63
	v_pk_fma_f32 v[218:219], v[184:185], v[184:185], v[50:51]
	v_and_b32_e32 v53, 0xffff0000, v220
	v_pk_add_f32 v[136:137], v[136:137], v[138:139]
	v_pk_mul_f32 v[138:139], v[62:63], v[216:217]
	v_mul_f32_e32 v52, v53, v53
	v_mov_b32_e32 v137, v139
	v_pk_add_f32 v[138:139], v[218:219], v[218:219] op_sel:[0,1] op_sel_hi:[1,0]
	v_lshlrev_b32_e32 v50, 16, v221
	v_mov_b32_e32 v139, v52
	v_mul_f32_e32 v52, v65, v65
	v_and_b32_e32 v51, 0xffff0000, v221
	v_pk_add_f32 v[136:137], v[136:137], v[138:139]
	v_pk_fma_f32 v[138:139], v[64:65], v[64:65], v[52:53] op_sel_hi:[1,1,0]
	v_mul_f32_e32 v52, v183, v183
	v_mul_f32_e32 v188, v50, v50
	v_mul_f32_e32 v190, v51, v51
	v_pk_fma_f32 v[216:217], v[182:183], v[182:183], v[52:53] op_sel_hi:[1,1,0]
	v_mov_b32_e32 v139, v188
	v_mov_b32_e32 v217, v190
	v_pk_add_f32 v[138:139], v[138:139], v[216:217]
	v_and_b32_sdwa v62, v131, v235 dst_sel:DWORD dst_unused:UNUSED_PAD src0_sel:WORD_1 src1_sel:DWORD
	v_pk_add_f32 v[136:137], v[136:137], v[138:139]
	v_mov_b32_e32 v139, v134
	v_mov_b32_e32 v138, v136
	v_mov_b32_e32 v134, v137
	v_pk_add_f32 v[134:135], v[138:139], v[134:135]
	ds_bpermute_b32 v137, v171, v135
	ds_bpermute_b32 v136, v171, v134
	v_and_b32_sdwa v138, v133, v235 dst_sel:DWORD dst_unused:UNUSED_PAD src0_sel:WORD_1 src1_sel:DWORD
	v_and_b32_sdwa v244, v130, v235 dst_sel:DWORD dst_unused:UNUSED_PAD src0_sel:WORD_1 src1_sel:DWORD
	v_add3_u32 v62, v131, v62, s44
	v_add3_u32 v138, v133, v138, s44
	s_waitcnt lgkmcnt(0)
	v_pk_add_f32 v[134:135], v[134:135], v[136:137]
	ds_bpermute_b32 v137, v226, v135
	ds_bpermute_b32 v136, v226, v134
	s_add_u32 s28, s33, s18
	v_add3_u32 v52, v130, v244, s44
	v_and_b32_e32 v62, 0xffff0000, v62
	v_and_b32_e32 v138, 0xffff0000, v138
	s_waitcnt lgkmcnt(0)
	v_pk_add_f32 v[134:135], v[134:135], v[136:137]
	ds_bpermute_b32 v137, v228, v135
	ds_bpermute_b32 v136, v228, v134
	s_addc_u32 s29, s34, s19
	s_add_i32 s4, s8, -3
	v_or_b32_sdwa v139, v62, v52 dst_sel:DWORD dst_unused:UNUSED_PAD src0_sel:DWORD src1_sel:WORD_1
	v_or_b32_sdwa v138, v138, v245 dst_sel:DWORD dst_unused:UNUSED_PAD src0_sel:DWORD src1_sel:WORD_1
	s_waitcnt lgkmcnt(0)
	v_pk_add_f32 v[134:135], v[134:135], v[136:137]
	ds_bpermute_b32 v137, v229, v135
	ds_bpermute_b32 v136, v229, v134
	s_ashr_i32 s5, s4, 31
	global_store_dwordx2 v234, v[138:139], s[16:17] offset:3584 nt
	s_lshl_b64 s[16:17], s[4:5], 11
	s_lshl_b64 s[24:25], s[4:5], 12
	s_waitcnt lgkmcnt(0)
	v_pk_add_f32 v[134:135], v[134:135], v[136:137]
	ds_bpermute_b32 v137, v230, v135
	ds_bpermute_b32 v136, v230, v134
	s_add_u32 s20, s96, s24
	s_addc_u32 s21, s97, s25
	s_lshl_b64 s[4:5], s[4:5], 13
	s_add_u32 s30, s6, s4
	s_waitcnt lgkmcnt(0)
	v_pk_add_f32 v[134:135], v[134:135], v[136:137]
	ds_bpermute_b32 v137, v231, v135
	ds_bpermute_b32 v136, v231, v134
	s_addc_u32 s31, s7, s5
	v_lshl_add_u64 v[138:139], s[30:31], 0, v[178:179]
	s_add_u32 s18, s35, s22
	s_addc_u32 s19, s36, s23
	s_waitcnt lgkmcnt(0)
	v_pk_add_f32 v[134:135], v[134:135], v[136:137]
	v_mov_b32_e32 v188, v191
	v_pk_fma_f32 v[134:135], v[134:135], s[10:11], v[180:181] op_sel_hi:[1,0,0]
	s_nop 0
	v_mul_f32_e32 v52, 0x4b800000, v135
	v_cmp_gt_f32_e64 s[4:5], s43, v135
	v_cmp_gt_f32_e32 vcc, s43, v134
	s_nop 0
	v_cndmask_b32_e64 v52, v135, v52, s[4:5]
	v_rsq_f32_e32 v52, v52
	s_nop 0
	v_mul_f32_e32 v62, 0x45800000, v52
	v_cndmask_b32_e64 v52, v52, v62, s[4:5]
	v_pk_mul_f32 v[136:137], v[162:163], v[52:53] op_sel_hi:[1,0]
	v_pk_mul_f32 v[162:163], v[164:165], v[52:53] op_sel_hi:[1,0]
	v_pk_fma_f32 v[136:137], v[26:27], v[136:137], v[30:31]
	v_pk_fma_f32 v[162:163], v[28:29], v[162:163], v[32:33]
	v_bfe_u32 v62, v136, 16, 1
	v_add3_u32 v62, v136, v62, s44
	v_bfe_u32 v135, v137, 16, 1
	v_lshrrev_b32_e32 v62, 16, v62
	v_add3_u32 v135, v137, v135, s44
	v_and_or_b32 v164, v135, s42, v62
	v_med3_f32 v135, v136, s45, v236
	v_med3_f32 v136, v137, s45, v236
	v_mov_b32_e32 v137, 0
	v_cvt_pk_fp8_f32 v137, v135, v136
	v_bfe_u32 v62, v162, 16, 1
	v_add3_u32 v62, v162, v62, s44
	v_med3_f32 v136, v162, s45, v236
	v_med3_f32 v162, v163, s45, v236
	v_bfe_u32 v135, v163, 16, 1
	v_cvt_pk_fp8_f32 v137, v136, v162 op_sel:[0,0,1]
	v_lshrrev_b32_e32 v62, 16, v62
	v_add3_u32 v135, v163, v135, s44
	v_and_or_b32 v165, v135, s42, v62
	global_store_dwordx2 v234, v[164:165], s[26:27]
	global_store_dword v237, v137, s[28:29]
	v_pk_mul_f32 v[136:137], v[154:155], v[52:53] op_sel_hi:[1,0]
	v_pk_mul_f32 v[154:155], v[156:157], v[52:53] op_sel_hi:[1,0]
	v_pk_fma_f32 v[136:137], v[90:91], v[136:137], v[94:95]
	v_pk_fma_f32 v[154:155], v[92:93], v[154:155], v[96:97]
	v_bfe_u32 v62, v136, 16, 1
	v_add3_u32 v62, v136, v62, s44
	v_bfe_u32 v135, v137, 16, 1
	v_lshrrev_b32_e32 v62, 16, v62
	v_add3_u32 v135, v137, v135, s44
	v_and_or_b32 v156, v135, s42, v62
	v_med3_f32 v135, v136, s45, v236
	v_med3_f32 v136, v137, s45, v236
	v_mov_b32_e32 v137, 0
	v_cvt_pk_fp8_f32 v137, v135, v136
	v_bfe_u32 v62, v154, 16, 1
	v_add3_u32 v62, v154, v62, s44
	v_med3_f32 v136, v154, s45, v236
	v_med3_f32 v154, v155, s45, v236
	v_bfe_u32 v135, v155, 16, 1
	v_cvt_pk_fp8_f32 v137, v136, v154 op_sel:[0,0,1]
	v_lshrrev_b32_e32 v62, 16, v62
	v_add3_u32 v135, v155, v135, s44
	v_and_or_b32 v157, v135, s42, v62
	global_store_dwordx2 v234, v[156:157], s[26:27] offset:512
	global_store_dword v237, v137, s[28:29] offset:256
	v_pk_mul_f32 v[136:137], v[210:211], v[52:53] op_sel_hi:[1,0]
	v_pk_mul_f32 v[152:153], v[152:153], v[52:53] op_sel_hi:[1,0]
	v_pk_fma_f32 v[136:137], v[82:83], v[136:137], v[86:87]
	v_pk_fma_f32 v[152:153], v[84:85], v[152:153], v[88:89]
	v_bfe_u32 v62, v136, 16, 1
	v_add3_u32 v62, v136, v62, s44
	v_bfe_u32 v135, v137, 16, 1
	v_lshrrev_b32_e32 v62, 16, v62
	v_add3_u32 v135, v137, v135, s44
	v_and_or_b32 v154, v135, s42, v62
	v_med3_f32 v135, v136, s45, v236
	v_med3_f32 v136, v137, s45, v236
	v_mov_b32_e32 v137, 0
	v_cvt_pk_fp8_f32 v137, v135, v136
	v_bfe_u32 v62, v152, 16, 1
	v_add3_u32 v62, v152, v62, s44
	v_med3_f32 v136, v152, s45, v236
	v_med3_f32 v152, v153, s45, v236
	v_bfe_u32 v135, v153, 16, 1
	v_cvt_pk_fp8_f32 v137, v136, v152 op_sel:[0,0,1]
	v_lshrrev_b32_e32 v62, 16, v62
	v_add3_u32 v135, v153, v135, s44
	v_and_or_b32 v155, v135, s42, v62
	global_store_dwordx2 v234, v[154:155], s[26:27] offset:1024
	global_store_dword v237, v137, s[28:29] offset:512
	v_pk_mul_f32 v[136:137], v[146:147], v[52:53] op_sel_hi:[1,0]
	v_pk_mul_f32 v[146:147], v[148:149], v[52:53] op_sel_hi:[1,0]
	v_pk_fma_f32 v[136:137], v[74:75], v[136:137], v[78:79]
	v_pk_fma_f32 v[146:147], v[76:77], v[146:147], v[80:81]
	v_bfe_u32 v62, v136, 16, 1
	v_add3_u32 v62, v136, v62, s44
	v_bfe_u32 v135, v137, 16, 1
	v_lshrrev_b32_e32 v62, 16, v62
	v_add3_u32 v135, v137, v135, s44
	v_and_or_b32 v148, v135, s42, v62
	v_med3_f32 v135, v136, s45, v236
	v_med3_f32 v136, v137, s45, v236
	v_mov_b32_e32 v137, 0
	v_cvt_pk_fp8_f32 v137, v135, v136
	v_bfe_u32 v62, v146, 16, 1
	v_add3_u32 v62, v146, v62, s44
	v_med3_f32 v136, v146, s45, v236
	v_med3_f32 v146, v147, s45, v236
	v_bfe_u32 v135, v147, 16, 1
	v_cvt_pk_fp8_f32 v137, v136, v146 op_sel:[0,0,1]
	v_lshrrev_b32_e32 v62, 16, v62
	v_add3_u32 v135, v147, v135, s44
	v_and_or_b32 v149, v135, s42, v62
	global_store_dwordx2 v234, v[148:149], s[26:27] offset:1536
	global_store_dword v237, v137, s[28:29] offset:768
	v_pk_mul_f32 v[136:137], v[142:143], v[52:53] op_sel_hi:[1,0]
	v_pk_mul_f32 v[142:143], v[144:145], v[52:53] op_sel_hi:[1,0]
	v_pk_fma_f32 v[136:137], v[34:35], v[136:137], v[70:71]
	v_pk_fma_f32 v[142:143], v[36:37], v[142:143], v[72:73]
	v_bfe_u32 v62, v136, 16, 1
	v_add3_u32 v62, v136, v62, s44
	v_bfe_u32 v135, v137, 16, 1
	v_lshrrev_b32_e32 v62, 16, v62
	v_add3_u32 v135, v137, v135, s44
	v_and_or_b32 v144, v135, s42, v62
	v_med3_f32 v135, v136, s45, v236
	v_med3_f32 v136, v137, s45, v236
	v_mov_b32_e32 v137, 0
	v_cvt_pk_fp8_f32 v137, v135, v136
	v_bfe_u32 v62, v142, 16, 1
	v_add3_u32 v62, v142, v62, s44
	v_med3_f32 v136, v142, s45, v236
	v_med3_f32 v142, v143, s45, v236
	v_bfe_u32 v135, v143, 16, 1
	v_cvt_pk_fp8_f32 v137, v136, v142 op_sel:[0,0,1]
	v_lshrrev_b32_e32 v62, 16, v62
	v_add3_u32 v135, v143, v135, s44
	v_and_or_b32 v145, v135, s42, v62
	global_store_dwordx2 v234, v[144:145], s[26:27] offset:2048
	global_store_dword v237, v137, s[28:29] offset:1024
	v_pk_mul_f32 v[136:137], v[212:213], v[52:53] op_sel_hi:[1,0]
	v_pk_mul_f32 v[142:143], v[214:215], v[52:53] op_sel_hi:[1,0]
	v_pk_fma_f32 v[136:137], v[18:19], v[136:137], v[22:23]
	v_pk_fma_f32 v[142:143], v[20:21], v[142:143], v[24:25]
	v_bfe_u32 v62, v136, 16, 1
	v_add3_u32 v62, v136, v62, s44
	v_bfe_u32 v135, v137, 16, 1
	v_lshrrev_b32_e32 v62, 16, v62
	v_add3_u32 v135, v137, v135, s44
	v_and_or_b32 v144, v135, s42, v62
	v_med3_f32 v135, v136, s45, v236
	v_med3_f32 v136, v137, s45, v236
	v_mov_b32_e32 v137, 0
	v_cvt_pk_fp8_f32 v137, v135, v136
	v_bfe_u32 v62, v142, 16, 1
	v_add3_u32 v62, v142, v62, s44
	v_med3_f32 v136, v142, s45, v236
	v_med3_f32 v142, v143, s45, v236
	v_bfe_u32 v135, v143, 16, 1
	v_cvt_pk_fp8_f32 v137, v136, v142 op_sel:[0,0,1]
	v_lshrrev_b32_e32 v62, 16, v62
	v_add3_u32 v135, v143, v135, s44
	v_and_or_b32 v145, v135, s42, v62
	global_store_dwordx2 v234, v[144:145], s[26:27] offset:2560
	global_store_dword v237, v137, s[28:29] offset:1280
	v_pk_mul_f32 v[136:137], v[140:141], v[52:53] op_sel_hi:[1,0]
	v_pk_mul_f32 v[140:141], v[150:151], v[52:53] op_sel_hi:[1,0]
	v_pk_fma_f32 v[136:137], v[10:11], v[136:137], v[14:15]
	v_pk_fma_f32 v[140:141], v[12:13], v[140:141], v[16:17]
	v_bfe_u32 v62, v136, 16, 1
	v_add3_u32 v62, v136, v62, s44
	v_bfe_u32 v135, v137, 16, 1
	v_lshrrev_b32_e32 v62, 16, v62
	v_add3_u32 v135, v137, v135, s44
	v_and_or_b32 v142, v135, s42, v62
	v_bfe_u32 v62, v140, 16, 1
	v_med3_f32 v135, v136, s45, v236
	v_med3_f32 v136, v137, s45, v236
	v_mov_b32_e32 v137, 0
	v_pk_mul_f32 v[132:133], v[132:133], v[52:53] op_sel_hi:[1,0]
	v_add3_u32 v62, v140, v62, s44
	v_cvt_pk_fp8_f32 v137, v135, v136
	v_bfe_u32 v135, v141, 16, 1
	v_pk_fma_f32 v[132:133], v[2:3], v[132:133], v[6:7]
	v_lshrrev_b32_e32 v62, 16, v62
	v_add3_u32 v135, v141, v135, s44
	v_pk_mul_f32 v[130:131], v[130:131], v[52:53] op_sel_hi:[1,0]
	v_bfe_u32 v52, v132, 16, 1
	v_and_or_b32 v143, v135, s42, v62
	v_add3_u32 v52, v132, v52, s44
	v_bfe_u32 v62, v133, 16, 1
	v_med3_f32 v136, v140, s45, v236
	v_med3_f32 v140, v141, s45, v236
	v_lshrrev_b32_e32 v52, 16, v52
	v_add3_u32 v62, v133, v62, s44
	v_cvt_pk_fp8_f32 v137, v136, v140 op_sel:[0,0,1]
	v_and_or_b32 v136, v62, s42, v52
	v_med3_f32 v62, v132, s45, v236
	v_med3_f32 v132, v133, s45, v236
	v_mov_b32_e32 v133, 0
	v_cvt_pk_fp8_f32 v133, v62, v132
	v_pk_fma_f32 v[130:131], v[4:5], v[130:131], v[8:9]
	global_store_dwordx2 v234, v[142:143], s[26:27] offset:3072
	global_store_dword v237, v137, s[28:29] offset:1536
	v_bfe_u32 v52, v130, 16, 1
	v_add3_u32 v52, v130, v52, s44
	v_med3_f32 v130, v130, s45, v236
	v_med3_f32 v132, v131, s45, v236
	v_bfe_u32 v62, v131, 16, 1
	v_cvt_pk_fp8_f32 v133, v130, v132 op_sel:[0,0,1]
	v_lshrrev_b32_e32 v52, 16, v52
	v_add3_u32 v62, v131, v62, s44
	v_and_or_b32 v137, v62, s42, v52
	global_store_dwordx2 v234, v[136:137], s[26:27] offset:3584
	global_store_dword v237, v133, s[28:29] offset:1792
	global_load_dwordx2 v[220:221], v234, s[20:21]
	global_load_dwordx4 v[162:165], v178, s[30:31]
	global_load_dwordx2 v[222:223], v234, s[20:21] offset:512
	global_load_dwordx4 v[154:157], v178, s[30:31] offset:1024
	global_load_dwordx2 v[224:225], v234, s[20:21] offset:1024
	global_load_dwordx4 v[150:153], v178, s[30:31] offset:2048
	global_load_dwordx2 v[238:239], v234, s[20:21] offset:1536
	global_load_dwordx4 v[146:149], v178, s[30:31] offset:3072
	global_load_dwordx2 v[240:241], v234, s[20:21] offset:2048
	v_add_co_u32_e64 v130, s[4:5], s41, v138
	v_mul_f32_e32 v52, 0x4b800000, v134
	s_nop 0
	v_addc_co_u32_e64 v131, s[4:5], 0, v139, s[4:5]
	global_load_dwordx4 v[142:145], v[130:131], off
	global_load_dwordx2 v[242:243], v234, s[20:21] offset:2560
	global_load_dwordx4 v[138:141], v[130:131], off offset:1024
	global_load_dwordx2 v[218:219], v234, s[20:21] offset:3072
	v_cndmask_b32_e32 v52, v134, v52, vcc
	global_load_dwordx4 v[134:137], v[130:131], off offset:2048
	global_load_dwordx2 v[244:245], v234, s[20:21] offset:3584
	s_nop 0
	global_load_dwordx4 v[130:133], v[130:131], off offset:3072
	v_rsq_f32_e32 v52, v52
	s_add_u32 s26, s11, s22
	s_addc_u32 s27, s13, s23
	s_add_u32 s28, s33, s14
	v_mul_f32_e32 v62, 0x45800000, v52
	v_cndmask_b32_e32 v62, v52, v62, vcc
	v_pk_mul_f32 v[208:209], v[62:63], v[208:209] op_sel_hi:[0,1]
	v_pk_mul_f32 v[206:207], v[62:63], v[206:207] op_sel_hi:[0,1]
	v_pk_fma_f32 v[214:215], v[98:99], v[206:207], v[166:167]
	v_pk_fma_f32 v[216:217], v[100:101], v[208:209], v[168:169]
	v_and_b32_sdwa v168, v215, v235 dst_sel:DWORD dst_unused:UNUSED_PAD src0_sel:WORD_1 src1_sel:DWORD
	v_and_b32_sdwa v167, v217, v235 dst_sel:DWORD dst_unused:UNUSED_PAD src0_sel:WORD_1 src1_sel:DWORD
	v_and_b32_sdwa v52, v216, v235 dst_sel:DWORD dst_unused:UNUSED_PAD src0_sel:WORD_1 src1_sel:DWORD
	v_and_b32_sdwa v166, v214, v235 dst_sel:DWORD dst_unused:UNUSED_PAD src0_sel:WORD_1 src1_sel:DWORD
	v_add3_u32 v167, v217, v167, s44
	v_add3_u32 v168, v215, v168, s44
	v_add3_u32 v166, v214, v166, s44
	v_add3_u32 v52, v216, v52, s44
	v_and_b32_e32 v167, 0xffff0000, v167
	v_and_b32_e32 v168, 0xffff0000, v168
	v_or_b32_sdwa v167, v167, v52 dst_sel:DWORD dst_unused:UNUSED_PAD src0_sel:DWORD src1_sel:WORD_1
	v_or_b32_sdwa v166, v168, v166 dst_sel:DWORD dst_unused:UNUSED_PAD src0_sel:DWORD src1_sel:WORD_1
	global_store_dwordx2 v234, v[166:167], s[18:19] nt
	v_mov_b32_e32 v166, v203
	v_mov_b32_e32 v167, v205
	v_mov_b32_e32 v203, v204
	v_pk_mul_f32 v[166:167], v[62:63], v[166:167] op_sel_hi:[0,1]
	v_pk_mul_f32 v[168:169], v[62:63], v[202:203] op_sel_hi:[0,1]
	v_pk_fma_f32 v[210:211], v[102:103], v[168:169], v[158:159]
	v_pk_fma_f32 v[212:213], v[104:105], v[166:167], v[160:161]
	v_and_b32_sdwa v160, v211, v235 dst_sel:DWORD dst_unused:UNUSED_PAD src0_sel:WORD_1 src1_sel:DWORD
	v_and_b32_sdwa v159, v213, v235 dst_sel:DWORD dst_unused:UNUSED_PAD src0_sel:WORD_1 src1_sel:DWORD
	v_and_b32_sdwa v52, v212, v235 dst_sel:DWORD dst_unused:UNUSED_PAD src0_sel:WORD_1 src1_sel:DWORD
	v_and_b32_sdwa v158, v210, v235 dst_sel:DWORD dst_unused:UNUSED_PAD src0_sel:WORD_1 src1_sel:DWORD
	v_add3_u32 v159, v213, v159, s44
	v_add3_u32 v160, v211, v160, s44
	v_add3_u32 v158, v210, v158, s44
	v_add3_u32 v52, v212, v52, s44
	v_and_b32_e32 v159, 0xffff0000, v159
	v_and_b32_e32 v160, 0xffff0000, v160
	v_or_b32_sdwa v159, v159, v52 dst_sel:DWORD dst_unused:UNUSED_PAD src0_sel:DWORD src1_sel:WORD_1
	v_or_b32_sdwa v158, v160, v158 dst_sel:DWORD dst_unused:UNUSED_PAD src0_sel:DWORD src1_sel:WORD_1
	v_mov_b32_e32 v160, v215
	v_mov_b32_e32 v161, v211
	global_store_dwordx2 v234, v[158:159], s[18:19] offset:512 nt
	v_mov_b32_e32 v158, v214
	v_mov_b32_e32 v159, v210
	v_pk_mul_f32 v[160:161], v[160:161], v[160:161]
	v_mov_b32_e32 v166, v217
	v_pk_fma_f32 v[158:159], v[158:159], v[158:159], v[160:161]
	v_mov_b32_e32 v160, v216
	v_mov_b32_e32 v161, v212
	v_pk_mul_f32 v[160:161], v[160:161], v[160:161]
	v_mov_b32_e32 v167, v213
	v_pk_fma_f32 v[160:161], v[166:167], v[166:167], v[160:161]
	v_pk_mul_f32 v[166:167], v[62:63], v[198:199] op_sel_hi:[0,1]
	v_pk_add_f32 v[158:159], v[158:159], v[160:161]
	v_pk_mul_f32 v[160:161], v[62:63], v[200:201] op_sel_hi:[0,1]
	v_pk_fma_f32 v[66:67], v[106:107], v[166:167], v[66:67]
	v_pk_fma_f32 v[68:69], v[108:109], v[160:161], v[68:69]
	v_pk_add_f32 v[158:159], v[158:159], v[158:159] op_sel_hi:[0,1]
	v_and_b32_sdwa v160, v69, v235 dst_sel:DWORD dst_unused:UNUSED_PAD src0_sel:WORD_1 src1_sel:DWORD
	v_and_b32_sdwa v161, v67, v235 dst_sel:DWORD dst_unused:UNUSED_PAD src0_sel:WORD_1 src1_sel:DWORD
	v_and_b32_sdwa v52, v68, v235 dst_sel:DWORD dst_unused:UNUSED_PAD src0_sel:WORD_1 src1_sel:DWORD
	v_and_b32_sdwa v158, v66, v235 dst_sel:DWORD dst_unused:UNUSED_PAD src0_sel:WORD_1 src1_sel:DWORD
	v_add3_u32 v160, v69, v160, s44
	v_add3_u32 v161, v67, v161, s44
	v_add3_u32 v158, v66, v158, s44
	v_add3_u32 v52, v68, v52, s44
	v_and_b32_e32 v160, 0xffff0000, v160
	v_and_b32_e32 v166, 0xffff0000, v161
	v_or_b32_sdwa v161, v160, v52 dst_sel:DWORD dst_unused:UNUSED_PAD src0_sel:DWORD src1_sel:WORD_1
	v_or_b32_sdwa v160, v166, v158 dst_sel:DWORD dst_unused:UNUSED_PAD src0_sel:DWORD src1_sel:WORD_1
	global_store_dwordx2 v234, v[160:161], s[18:19] offset:1024 nt
	v_pk_mul_f32 v[160:161], v[68:69], v[68:69]
	v_pk_mul_f32 v[166:167], v[66:67], v[66:67]
	v_pk_mul_f32 v[64:65], v[62:63], v[64:65] op_sel_hi:[0,1]
	v_pk_mov_b32 v[168:169], v[166:167], v[160:161] op_sel:[1,0]
	v_mov_b32_e32 v167, v161
	v_pk_add_f32 v[160:161], v[166:167], v[168:169]
	v_pk_mul_f32 v[166:167], v[196:197], v[62:63] op_sel_hi:[1,0]
	v_pk_mul_f32 v[168:169], v[188:189], v[62:63] op_sel_hi:[1,0]
	v_pk_add_f32 v[160:161], v[160:161], v[160:161] op_sel_hi:[0,1]
	v_pk_fma_f32 v[58:59], v[110:111], v[168:169], v[58:59]
	v_pk_fma_f32 v[60:61], v[112:113], v[166:167], v[60:61]
	v_and_b32_sdwa v166, v59, v235 dst_sel:DWORD dst_unused:UNUSED_PAD src0_sel:WORD_1 src1_sel:DWORD
	v_and_b32_sdwa v160, v61, v235 dst_sel:DWORD dst_unused:UNUSED_PAD src0_sel:WORD_1 src1_sel:DWORD
	v_and_b32_sdwa v52, v60, v235 dst_sel:DWORD dst_unused:UNUSED_PAD src0_sel:WORD_1 src1_sel:DWORD
	v_and_b32_sdwa v158, v58, v235 dst_sel:DWORD dst_unused:UNUSED_PAD src0_sel:WORD_1 src1_sel:DWORD
	v_add3_u32 v160, v61, v160, s44
	v_add3_u32 v166, v59, v166, s44
	v_add3_u32 v158, v58, v158, s44
	v_add3_u32 v52, v60, v52, s44
	v_and_b32_e32 v160, 0xffff0000, v160
	v_and_b32_e32 v166, 0xffff0000, v166
	v_mov_b32_e32 v188, v192
	v_mov_b32_e32 v189, v194
	v_mov_b32_e32 v194, v193
	v_or_b32_sdwa v167, v160, v52 dst_sel:DWORD dst_unused:UNUSED_PAD src0_sel:DWORD src1_sel:WORD_1
	v_or_b32_sdwa v166, v166, v158 dst_sel:DWORD dst_unused:UNUSED_PAD src0_sel:DWORD src1_sel:WORD_1
	v_mul_f32_e32 v52, v58, v58
	v_pk_mul_f32 v[188:189], v[62:63], v[188:189] op_sel_hi:[0,1]
	v_pk_mul_f32 v[190:191], v[62:63], v[194:195] op_sel_hi:[0,1]
	global_store_dwordx2 v234, v[166:167], s[18:19] offset:1536 nt
	v_pk_fma_f32 v[166:167], v[58:59], v[58:59], v[52:53] op_sel_hi:[1,1,0]
	v_pk_fma_f32 v[56:57], v[116:117], v[190:191], v[56:57]
	v_pk_fma_f32 v[54:55], v[114:115], v[188:189], v[54:55]
	v_mul_f32_e32 v52, v60, v60
	v_and_b32_sdwa v160, v57, v235 dst_sel:DWORD dst_unused:UNUSED_PAD src0_sel:WORD_1 src1_sel:DWORD
	v_and_b32_sdwa v166, v55, v235 dst_sel:DWORD dst_unused:UNUSED_PAD src0_sel:WORD_1 src1_sel:DWORD
	v_pk_fma_f32 v[168:169], v[60:61], v[60:61], v[52:53] op_sel_hi:[1,1,0]
	v_and_b32_sdwa v52, v56, v235 dst_sel:DWORD dst_unused:UNUSED_PAD src0_sel:WORD_1 src1_sel:DWORD
	v_and_b32_sdwa v158, v54, v235 dst_sel:DWORD dst_unused:UNUSED_PAD src0_sel:WORD_1 src1_sel:DWORD
	v_add3_u32 v160, v57, v160, s44
	v_add3_u32 v166, v55, v166, s44
	v_add3_u32 v158, v54, v158, s44
	v_add3_u32 v52, v56, v52, s44
	v_and_b32_e32 v160, 0xffff0000, v160
	v_and_b32_e32 v166, 0xffff0000, v166
	v_or_b32_sdwa v189, v160, v52 dst_sel:DWORD dst_unused:UNUSED_PAD src0_sel:DWORD src1_sel:WORD_1
	v_or_b32_sdwa v188, v166, v158 dst_sel:DWORD dst_unused:UNUSED_PAD src0_sel:DWORD src1_sel:WORD_1
	v_mul_f32_e32 v166, v54, v54
	v_mul_f32_e32 v168, v55, v55
	v_mul_f32_e32 v158, v56, v56
	v_mul_f32_e32 v160, v57, v57
	v_pk_add_f32 v[166:167], v[166:167], v[168:169]
	v_pk_add_f32 v[158:159], v[160:161], v[158:159]
	v_mov_b32_e32 v160, v185
	v_mov_b32_e32 v161, v187
	v_mov_b32_e32 v185, v186
	v_pk_add_f32 v[158:159], v[166:167], v[158:159]
	v_pk_mul_f32 v[160:161], v[62:63], v[160:161] op_sel_hi:[0,1]
	v_pk_mul_f32 v[166:167], v[62:63], v[184:185] op_sel_hi:[0,1]
	v_pk_fma_f32 v[46:47], v[118:119], v[166:167], v[46:47]
	v_pk_fma_f32 v[48:49], v[120:121], v[160:161], v[48:49]
	v_pk_add_f32 v[158:159], v[158:159], v[158:159] op_sel_hi:[0,1]
	v_and_b32_sdwa v160, v49, v235 dst_sel:DWORD dst_unused:UNUSED_PAD src0_sel:WORD_1 src1_sel:DWORD
	v_and_b32_sdwa v161, v47, v235 dst_sel:DWORD dst_unused:UNUSED_PAD src0_sel:WORD_1 src1_sel:DWORD
	v_and_b32_sdwa v52, v48, v235 dst_sel:DWORD dst_unused:UNUSED_PAD src0_sel:WORD_1 src1_sel:DWORD
	v_and_b32_sdwa v158, v46, v235 dst_sel:DWORD dst_unused:UNUSED_PAD src0_sel:WORD_1 src1_sel:DWORD
	v_add3_u32 v160, v49, v160, s44
	v_add3_u32 v161, v47, v161, s44
	v_add3_u32 v158, v46, v158, s44
	v_add3_u32 v52, v48, v52, s44
	v_and_b32_e32 v160, 0xffff0000, v160
	v_and_b32_e32 v166, 0xffff0000, v161
	v_or_b32_sdwa v161, v160, v52 dst_sel:DWORD dst_unused:UNUSED_PAD src0_sel:DWORD src1_sel:WORD_1
	v_or_b32_sdwa v160, v166, v158 dst_sel:DWORD dst_unused:UNUSED_PAD src0_sel:DWORD src1_sel:WORD_1
	global_store_dwordx2 v234, v[160:161], s[18:19] offset:2560 nt
	v_pk_mul_f32 v[160:161], v[48:49], v[48:49]
	v_pk_mul_f32 v[166:167], v[46:47], v[46:47]
	v_pk_fma_f32 v[42:43], v[122:123], v[64:65], v[42:43]
	v_pk_mov_b32 v[168:169], v[166:167], v[160:161] op_sel:[1,0]
	v_mov_b32_e32 v167, v161
	v_pk_add_f32 v[160:161], v[166:167], v[168:169]
	v_pk_mul_f32 v[166:167], v[62:63], v[182:183] op_sel_hi:[0,1]
	v_pk_fma_f32 v[44:45], v[124:125], v[166:167], v[44:45]
	v_and_b32_sdwa v158, v43, v235 dst_sel:DWORD dst_unused:UNUSED_PAD src0_sel:WORD_1 src1_sel:DWORD
	v_and_b32_sdwa v65, v45, v235 dst_sel:DWORD dst_unused:UNUSED_PAD src0_sel:WORD_1 src1_sel:DWORD
	v_and_b32_sdwa v52, v44, v235 dst_sel:DWORD dst_unused:UNUSED_PAD src0_sel:WORD_1 src1_sel:DWORD
	v_and_b32_sdwa v64, v42, v235 dst_sel:DWORD dst_unused:UNUSED_PAD src0_sel:WORD_1 src1_sel:DWORD
	v_add3_u32 v65, v45, v65, s44
	v_add3_u32 v158, v43, v158, s44
	v_add3_u32 v64, v42, v64, s44
	v_add3_u32 v52, v44, v52, s44
	v_and_b32_e32 v65, 0xffff0000, v65
	v_and_b32_e32 v158, 0xffff0000, v158
	v_or_b32_sdwa v65, v65, v52 dst_sel:DWORD dst_unused:UNUSED_PAD src0_sel:DWORD src1_sel:WORD_1
	v_or_b32_sdwa v64, v158, v64 dst_sel:DWORD dst_unused:UNUSED_PAD src0_sel:DWORD src1_sel:WORD_1
	v_mul_f32_e32 v52, v42, v42
	global_store_dwordx2 v234, v[64:65], s[18:19] offset:3072 nt
	v_pk_fma_f32 v[64:65], v[42:43], v[42:43], v[52:53] op_sel_hi:[1,1,0]
	v_mul_f32_e32 v52, v44, v44
	v_pk_fma_f32 v[166:167], v[44:45], v[44:45], v[52:53] op_sel_hi:[1,1,0]
	v_mov_b32_e32 v52, v63
	v_pk_mul_f32 v[52:53], v[52:53], v[62:63] op_sel_hi:[1,0]
	v_pk_mul_f32 v[50:51], v[50:51], v[62:63] op_sel_hi:[1,0]
	v_pk_add_f32 v[160:161], v[160:161], v[160:161] op_sel_hi:[0,1]
	s_waitcnt vmcnt(46)
	v_pk_fma_f32 v[40:41], v[128:129], v[50:51], v[40:41]
	v_pk_fma_f32 v[38:39], v[126:127], v[52:53], v[38:39]
	v_mul_f32_e32 v158, v40, v40
	v_and_b32_sdwa v50, v38, v235 dst_sel:DWORD dst_unused:UNUSED_PAD src0_sel:WORD_1 src1_sel:DWORD
	v_mul_f32_e32 v64, v38, v38
	v_mul_f32_e32 v166, v39, v39
	v_mul_f32_e32 v160, v41, v41
	v_add3_u32 v246, v38, v50, s44
	v_pk_add_f32 v[50:51], v[64:65], v[166:167]
	v_pk_add_f32 v[52:53], v[160:161], v[158:159]
	s_waitcnt vmcnt(21)
	v_and_b32_e32 v207, 0xffff0000, v220
	v_and_b32_e32 v209, 0xffff0000, v221
	v_pk_add_f32 v[50:51], v[50:51], v[52:53]
	v_lshlrev_b32_e32 v206, 16, v220
	v_lshlrev_b32_e32 v208, 16, v221
	v_mul_f32_e32 v52, v209, v209
	s_waitcnt vmcnt(19)
	v_and_b32_e32 v205, 0xffff0000, v223
	v_and_b32_e32 v204, 0xffff0000, v222
	v_mul_f32_e32 v64, v207, v207
	v_pk_fma_f32 v[52:53], v[208:209], v[208:209], v[52:53] op_sel_hi:[1,1,0]
	v_lshlrev_b32_e32 v203, 16, v223
	v_lshlrev_b32_e32 v202, 16, v222
	v_pk_mul_f32 v[62:63], v[204:205], v[204:205]
	s_waitcnt vmcnt(15)
	v_lshlrev_b32_e32 v191, 16, v238
	v_pk_fma_f32 v[64:65], v[206:207], v[206:207], v[64:65] op_sel_hi:[1,1,0]
	global_store_dwordx2 v234, v[188:189], s[18:19] offset:2048 nt
	v_pk_fma_f32 v[62:63], v[202:203], v[202:203], v[62:63]
	v_and_b32_e32 v189, 0xffff0000, v238
	v_mov_b32_e32 v190, v64
	v_mov_b32_e32 v158, v52
	v_mov_b32_e32 v159, v191
	v_mul_f32_e32 v160, v189, v189
	v_pk_add_f32 v[52:53], v[64:65], v[52:53]
	v_pk_mul_f32 v[64:65], v[190:191], v[158:159]
	v_pk_add_f32 v[62:63], v[62:63], v[62:63] op_sel:[0,1] op_sel_hi:[1,0]
	v_and_b32_e32 v199, 0xffff0000, v224
	v_and_b32_e32 v201, 0xffff0000, v225
	v_mov_b32_e32 v53, v65
	v_mov_b32_e32 v63, v160
	v_lshlrev_b32_e32 v198, 16, v224
	v_lshlrev_b32_e32 v200, 16, v225
	v_lshlrev_b32_e32 v196, 16, v239
	v_and_b32_e32 v197, 0xffff0000, v239
	v_pk_add_f32 v[52:53], v[52:53], v[62:63]
	v_mul_f32_e32 v62, v199, v199
	v_mul_f32_e32 v64, v201, v201
	v_mul_f32_e32 v161, v196, v196
	v_mul_f32_e32 v166, v197, v197
	v_pk_fma_f32 v[62:63], v[198:199], v[198:199], v[62:63] op_sel_hi:[1,1,0]
	v_pk_fma_f32 v[64:65], v[200:201], v[200:201], v[64:65] op_sel_hi:[1,1,0]
	v_mov_b32_e32 v63, v161
	v_mov_b32_e32 v65, v166
	v_pk_add_f32 v[62:63], v[62:63], v[64:65]
	s_waitcnt vmcnt(14)
	v_and_b32_e32 v195, 0xffff0000, v241
	v_and_b32_e32 v194, 0xffff0000, v240
	v_pk_add_f32 v[52:53], v[52:53], v[62:63]
	v_lshlrev_b32_e32 v193, 16, v241
	v_lshlrev_b32_e32 v192, 16, v240
	v_pk_mul_f32 v[62:63], v[194:195], v[194:195]
	s_waitcnt vmcnt(12)
	v_and_b32_e32 v187, 0xffff0000, v243
	v_pk_fma_f32 v[62:63], v[192:193], v[192:193], v[62:63]
	v_and_b32_e32 v186, 0xffff0000, v242
	v_pk_add_f32 v[62:63], v[62:63], v[62:63] op_sel:[0,1] op_sel_hi:[1,0]
	s_waitcnt vmcnt(8)
	v_lshlrev_b32_e32 v167, 16, v244
	v_pk_add_f32 v[52:53], v[52:53], v[52:53] op_sel:[0,1] op_sel_hi:[1,0]
	v_lshlrev_b32_e32 v185, 16, v243
	v_lshlrev_b32_e32 v184, 16, v242
	v_pk_mul_f32 v[64:65], v[186:187], v[186:187]
	v_lshlrev_b32_e32 v168, 16, v218
	v_and_b32_e32 v169, 0xffff0000, v218
	v_lshlrev_b32_e32 v182, 16, v219
	v_and_b32_e32 v183, 0xffff0000, v219
	v_mov_b32_e32 v166, v52
	v_mov_b32_e32 v218, v62
	v_mov_b32_e32 v219, v167
	v_pk_fma_f32 v[64:65], v[184:185], v[184:185], v[64:65]
	v_and_b32_e32 v161, 0xffff0000, v244
	v_pk_add_f32 v[52:53], v[52:53], v[62:63]
	v_pk_mul_f32 v[62:63], v[166:167], v[218:219]
	v_mul_f32_e32 v160, v161, v161
	v_mov_b32_e32 v53, v63
	v_pk_add_f32 v[62:63], v[64:65], v[64:65] op_sel:[0,1] op_sel_hi:[1,0]
	v_lshlrev_b32_e32 v158, 16, v245
	v_mov_b32_e32 v63, v160
	v_and_b32_e32 v159, 0xffff0000, v245
	v_pk_add_f32 v[52:53], v[52:53], v[62:63]
	v_mul_f32_e32 v62, v169, v169
	v_mul_f32_e32 v64, v183, v183
	v_mul_f32_e32 v190, v158, v158
	v_mul_f32_e32 v220, v159, v159
	v_pk_fma_f32 v[62:63], v[168:169], v[168:169], v[62:63] op_sel_hi:[1,1,0]
	v_pk_fma_f32 v[64:65], v[182:183], v[182:183], v[64:65] op_sel_hi:[1,1,0]
	v_mov_b32_e32 v63, v190
	v_mov_b32_e32 v65, v220
	v_pk_add_f32 v[62:63], v[62:63], v[64:65]
	v_and_b32_sdwa v64, v39, v235 dst_sel:DWORD dst_unused:UNUSED_PAD src0_sel:WORD_1 src1_sel:DWORD
	v_pk_add_f32 v[52:53], v[52:53], v[62:63]
	v_mov_b32_e32 v63, v50
	v_mov_b32_e32 v62, v52
	v_mov_b32_e32 v50, v53
	v_pk_add_f32 v[50:51], v[62:63], v[50:51]
	ds_bpermute_b32 v53, v171, v51
	ds_bpermute_b32 v52, v171, v50
	v_and_b32_sdwa v63, v41, v235 dst_sel:DWORD dst_unused:UNUSED_PAD src0_sel:WORD_1 src1_sel:DWORD
	v_and_b32_sdwa v188, v40, v235 dst_sel:DWORD dst_unused:UNUSED_PAD src0_sel:WORD_1 src1_sel:DWORD
	v_add3_u32 v63, v41, v63, s44
	v_add3_u32 v64, v39, v64, s44
	s_waitcnt lgkmcnt(0)
	v_pk_add_f32 v[50:51], v[50:51], v[52:53]
	ds_bpermute_b32 v53, v226, v51
	ds_bpermute_b32 v52, v226, v50
	v_add3_u32 v62, v40, v188, s44
	v_and_b32_e32 v63, 0xffff0000, v63
	v_and_b32_e32 v64, 0xffff0000, v64
	s_addc_u32 s29, s34, s15
	s_waitcnt lgkmcnt(0)
	v_pk_add_f32 v[50:51], v[50:51], v[52:53]
	ds_bpermute_b32 v53, v228, v51
	ds_bpermute_b32 v52, v228, v50
	s_add_i32 s4, s8, -2
	v_or_b32_sdwa v63, v63, v62 dst_sel:DWORD dst_unused:UNUSED_PAD src0_sel:DWORD src1_sel:WORD_1
	v_or_b32_sdwa v62, v64, v246 dst_sel:DWORD dst_unused:UNUSED_PAD src0_sel:DWORD src1_sel:WORD_1
	s_ashr_i32 s5, s4, 31
	s_waitcnt lgkmcnt(0)
	v_pk_add_f32 v[50:51], v[50:51], v[52:53]
	ds_bpermute_b32 v53, v229, v51
	ds_bpermute_b32 v52, v229, v50
	global_store_dwordx2 v234, v[62:63], s[18:19] offset:3584 nt
	s_lshl_b64 s[18:19], s[4:5], 11
	s_lshl_b64 s[20:21], s[4:5], 12
	s_add_u32 s22, s96, s20
	s_waitcnt lgkmcnt(0)
	v_pk_add_f32 v[50:51], v[50:51], v[52:53]
	ds_bpermute_b32 v53, v230, v51
	ds_bpermute_b32 v52, v230, v50
	s_addc_u32 s23, s97, s21
	s_lshl_b64 s[4:5], s[4:5], 13
	s_add_u32 s30, s6, s4
	s_addc_u32 s31, s7, s5
	s_waitcnt lgkmcnt(0)
	v_pk_add_f32 v[50:51], v[50:51], v[52:53]
	ds_bpermute_b32 v53, v231, v51
	ds_bpermute_b32 v52, v231, v50
	v_lshl_add_u64 v[62:63], s[30:31], 0, v[178:179]
	s_add_u32 s14, s35, s24
	s_addc_u32 s15, s36, s25
	v_mov_b32_e32 v188, v191
	s_waitcnt lgkmcnt(0)
	v_pk_add_f32 v[50:51], v[50:51], v[52:53]
	s_nop 0
	v_pk_fma_f32 v[50:51], v[50:51], s[10:11], v[180:181] op_sel_hi:[1,0,0]
	s_nop 0
	v_mul_f32_e32 v52, 0x4b800000, v51
	v_cmp_gt_f32_e64 s[4:5], s43, v51
	v_cmp_gt_f32_e32 vcc, s43, v50
	s_nop 0
	v_cndmask_b32_e64 v51, v51, v52, s[4:5]
	v_rsq_f32_e32 v51, v51
	s_nop 0
	v_mul_f32_e32 v52, 0x45800000, v51
	v_cndmask_b32_e64 v52, v51, v52, s[4:5]
	v_pk_mul_f32 v[64:65], v[214:215], v[52:53] op_sel_hi:[1,0]
	v_pk_mul_f32 v[214:215], v[216:217], v[52:53] op_sel_hi:[1,0]
	v_pk_fma_f32 v[64:65], v[26:27], v[64:65], v[30:31]
	v_pk_fma_f32 v[214:215], v[28:29], v[214:215], v[32:33]
	v_bfe_u32 v51, v64, 16, 1
	v_add3_u32 v51, v64, v51, s44
	v_bfe_u32 v53, v65, 16, 1
	v_lshrrev_b32_e32 v51, 16, v51
	v_add3_u32 v53, v65, v53, s44
	v_and_or_b32 v216, v53, s42, v51
	v_med3_f32 v53, v64, s45, v236
	v_med3_f32 v64, v65, s45, v236
	v_mov_b32_e32 v65, 0
	v_cvt_pk_fp8_f32 v65, v53, v64
	v_bfe_u32 v51, v214, 16, 1
	v_med3_f32 v64, v214, s45, v236
	v_med3_f32 v160, v215, s45, v236
	v_add3_u32 v51, v214, v51, s44
	v_bfe_u32 v53, v215, 16, 1
	v_cvt_pk_fp8_f32 v65, v64, v160 op_sel:[0,0,1]
	v_lshrrev_b32_e32 v51, 16, v51
	v_add3_u32 v53, v215, v53, s44
	v_and_or_b32 v217, v53, s42, v51
	global_store_dwordx2 v234, v[216:217], s[26:27]
	global_store_dword v237, v65, s[28:29]
	v_pk_mul_f32 v[64:65], v[210:211], v[52:53] op_sel_hi:[1,0]
	v_pk_mul_f32 v[210:211], v[212:213], v[52:53] op_sel_hi:[1,0]
	v_pk_fma_f32 v[64:65], v[90:91], v[64:65], v[94:95]
	v_pk_fma_f32 v[210:211], v[92:93], v[210:211], v[96:97]
	v_bfe_u32 v51, v64, 16, 1
	v_add3_u32 v51, v64, v51, s44
	v_bfe_u32 v53, v65, 16, 1
	v_lshrrev_b32_e32 v51, 16, v51
	v_add3_u32 v53, v65, v53, s44
	v_and_or_b32 v212, v53, s42, v51
	v_med3_f32 v53, v64, s45, v236
	v_med3_f32 v64, v65, s45, v236
	v_mov_b32_e32 v65, 0
	v_cvt_pk_fp8_f32 v65, v53, v64
	v_bfe_u32 v51, v210, 16, 1
	v_med3_f32 v64, v210, s45, v236
	v_med3_f32 v160, v211, s45, v236
	v_add3_u32 v51, v210, v51, s44
	v_bfe_u32 v53, v211, 16, 1
	v_cvt_pk_fp8_f32 v65, v64, v160 op_sel:[0,0,1]
	v_lshrrev_b32_e32 v51, 16, v51
	v_add3_u32 v53, v211, v53, s44
	v_and_or_b32 v213, v53, s42, v51
	global_store_dwordx2 v234, v[212:213], s[26:27] offset:512
	global_store_dword v237, v65, s[28:29] offset:256
	v_pk_mul_f32 v[64:65], v[66:67], v[52:53] op_sel_hi:[1,0]
	v_pk_mul_f32 v[66:67], v[68:69], v[52:53] op_sel_hi:[1,0]
	v_pk_fma_f32 v[64:65], v[82:83], v[64:65], v[86:87]
	v_pk_fma_f32 v[66:67], v[84:85], v[66:67], v[88:89]
	v_bfe_u32 v51, v64, 16, 1
	v_add3_u32 v51, v64, v51, s44
	v_bfe_u32 v53, v65, 16, 1
	v_lshrrev_b32_e32 v51, 16, v51
	v_add3_u32 v53, v65, v53, s44
	v_and_or_b32 v68, v53, s42, v51
	v_med3_f32 v53, v64, s45, v236
	v_med3_f32 v64, v65, s45, v236
	v_mov_b32_e32 v65, 0
	v_cvt_pk_fp8_f32 v65, v53, v64
	v_bfe_u32 v53, v67, 16, 1
	v_bfe_u32 v51, v66, 16, 1
	v_add3_u32 v53, v67, v53, s44
	v_add3_u32 v51, v66, v51, s44
	v_pk_mul_f32 v[58:59], v[58:59], v[52:53] op_sel_hi:[1,0]
	v_lshrrev_b32_e32 v51, 16, v51
	v_pk_fma_f32 v[58:59], v[74:75], v[58:59], v[78:79]
	v_and_or_b32 v69, v53, s42, v51
	v_bfe_u32 v51, v58, 16, 1
	v_pk_mul_f32 v[60:61], v[60:61], v[52:53] op_sel_hi:[1,0]
	v_add3_u32 v51, v58, v51, s44
	v_bfe_u32 v53, v59, 16, 1
	v_med3_f32 v64, v66, s45, v236
	v_med3_f32 v66, v67, s45, v236
	v_lshrrev_b32_e32 v51, 16, v51
	v_add3_u32 v53, v59, v53, s44
	v_cvt_pk_fp8_f32 v65, v64, v66 op_sel:[0,0,1]
	v_pk_fma_f32 v[60:61], v[76:77], v[60:61], v[80:81]
	v_and_or_b32 v64, v53, s42, v51
	v_med3_f32 v53, v58, s45, v236
	v_med3_f32 v58, v59, s45, v236
	v_mov_b32_e32 v59, 0
	v_cvt_pk_fp8_f32 v59, v53, v58
	v_bfe_u32 v53, v61, 16, 1
	v_bfe_u32 v51, v60, 16, 1
	v_add3_u32 v53, v61, v53, s44
	v_add3_u32 v51, v60, v51, s44
	v_pk_mul_f32 v[54:55], v[54:55], v[52:53] op_sel_hi:[1,0]
	v_lshrrev_b32_e32 v51, 16, v51
	v_pk_fma_f32 v[54:55], v[34:35], v[54:55], v[70:71]
	global_store_dwordx2 v234, v[68:69], s[26:27] offset:1024
	global_store_dword v237, v65, s[28:29] offset:512
	v_and_or_b32 v65, v53, s42, v51
	v_bfe_u32 v51, v54, 16, 1
	v_pk_mul_f32 v[56:57], v[56:57], v[52:53] op_sel_hi:[1,0]
	v_add3_u32 v51, v54, v51, s44
	v_bfe_u32 v53, v55, 16, 1
	v_med3_f32 v58, v60, s45, v236
	v_med3_f32 v60, v61, s45, v236
	v_lshrrev_b32_e32 v51, 16, v51
	v_add3_u32 v53, v55, v53, s44
	v_cvt_pk_fp8_f32 v59, v58, v60 op_sel:[0,0,1]
	v_pk_fma_f32 v[56:57], v[36:37], v[56:57], v[72:73]
	v_and_or_b32 v58, v53, s42, v51
	v_med3_f32 v53, v54, s45, v236
	v_med3_f32 v54, v55, s45, v236
	v_mov_b32_e32 v55, 0
	v_cvt_pk_fp8_f32 v55, v53, v54
	v_bfe_u32 v53, v57, 16, 1
	v_bfe_u32 v51, v56, 16, 1
	v_add3_u32 v53, v57, v53, s44
	v_add3_u32 v51, v56, v51, s44
	v_pk_mul_f32 v[46:47], v[46:47], v[52:53] op_sel_hi:[1,0]
	v_lshrrev_b32_e32 v51, 16, v51
	v_pk_fma_f32 v[46:47], v[18:19], v[46:47], v[22:23]
	global_store_dwordx2 v234, v[64:65], s[26:27] offset:1536
	global_store_dword v237, v59, s[28:29] offset:768
	v_and_or_b32 v59, v53, s42, v51
	v_bfe_u32 v51, v46, 16, 1
	v_pk_mul_f32 v[48:49], v[48:49], v[52:53] op_sel_hi:[1,0]
	v_add3_u32 v51, v46, v51, s44
	v_bfe_u32 v53, v47, 16, 1
	v_med3_f32 v54, v56, s45, v236
	v_med3_f32 v56, v57, s45, v236
	v_lshrrev_b32_e32 v51, 16, v51
	v_add3_u32 v53, v47, v53, s44
	v_cvt_pk_fp8_f32 v55, v54, v56 op_sel:[0,0,1]
	v_and_or_b32 v54, v53, s42, v51
	v_med3_f32 v46, v46, s45, v236
	v_med3_f32 v47, v47, s45, v236
	v_mov_b32_e32 v53, 0
	v_cvt_pk_fp8_f32 v53, v46, v47
	v_pk_fma_f32 v[48:49], v[20:21], v[48:49], v[24:25]
	global_store_dwordx2 v234, v[58:59], s[26:27] offset:2048
	global_store_dword v237, v55, s[28:29] offset:1024
	v_bfe_u32 v51, v48, 16, 1
	v_add3_u32 v51, v48, v51, s44
	v_med3_f32 v47, v48, s45, v236
	v_med3_f32 v48, v49, s45, v236
	v_cvt_pk_fp8_f32 v53, v47, v48 op_sel:[0,0,1]
	v_bfe_u32 v46, v49, 16, 1
	v_lshrrev_b32_e32 v51, 16, v51
	v_add3_u32 v46, v49, v46, s44
	v_pk_mul_f32 v[42:43], v[42:43], v[52:53] op_sel_hi:[1,0]
	v_and_or_b32 v55, v46, s42, v51
	v_pk_fma_f32 v[42:43], v[10:11], v[42:43], v[14:15]
	v_pk_mul_f32 v[44:45], v[44:45], v[52:53] op_sel_hi:[1,0]
	v_bfe_u32 v46, v42, 16, 1
	v_bfe_u32 v47, v43, 16, 1
	v_add3_u32 v46, v42, v46, s44
	v_add3_u32 v47, v43, v47, s44
	v_med3_f32 v42, v42, s45, v236
	v_med3_f32 v43, v43, s45, v236
	v_mov_b32_e32 v48, 0
	v_pk_fma_f32 v[44:45], v[12:13], v[44:45], v[16:17]
	v_lshrrev_b32_e32 v46, 16, v46
	v_cvt_pk_fp8_f32 v48, v42, v43
	v_and_or_b32 v46, v47, s42, v46
	v_bfe_u32 v47, v44, 16, 1
	v_add3_u32 v47, v44, v47, s44
	v_bfe_u32 v42, v45, 16, 1
	v_pk_mul_f32 v[38:39], v[38:39], v[52:53] op_sel_hi:[1,0]
	v_lshrrev_b32_e32 v47, 16, v47
	v_med3_f32 v43, v44, s45, v236
	v_med3_f32 v44, v45, s45, v236
	v_add3_u32 v42, v45, v42, s44
	v_pk_fma_f32 v[38:39], v[2:3], v[38:39], v[6:7]
	v_cvt_pk_fp8_f32 v48, v43, v44 op_sel:[0,0,1]
	v_and_or_b32 v47, v42, s42, v47
	v_bfe_u32 v42, v38, 16, 1
	v_bfe_u32 v43, v39, 16, 1
	v_add3_u32 v42, v38, v42, s44
	v_add3_u32 v43, v39, v43, s44
	v_med3_f32 v38, v38, s45, v236
	v_med3_f32 v39, v39, s45, v236
	v_mov_b32_e32 v44, 0
	v_pk_mul_f32 v[40:41], v[40:41], v[52:53] op_sel_hi:[1,0]
	v_cvt_pk_fp8_f32 v44, v38, v39
	v_pk_fma_f32 v[40:41], v[4:5], v[40:41], v[8:9]
	v_lshrrev_b32_e32 v42, 16, v42
	v_and_or_b32 v42, v43, s42, v42
	v_bfe_u32 v43, v40, 16, 1
	v_add3_u32 v43, v40, v43, s44
	v_med3_f32 v39, v40, s45, v236
	v_med3_f32 v40, v41, s45, v236
	v_bfe_u32 v38, v41, 16, 1
	v_cvt_pk_fp8_f32 v44, v39, v40 op_sel:[0,0,1]
	v_lshrrev_b32_e32 v43, 16, v43
	v_add3_u32 v38, v41, v38, s44
	v_and_or_b32 v43, v38, s42, v43
	global_store_dwordx2 v234, v[54:55], s[26:27] offset:2560
	global_store_dword v237, v53, s[28:29] offset:1280
	global_store_dwordx2 v234, v[46:47], s[26:27] offset:3072
	global_store_dword v237, v48, s[28:29] offset:1536
	global_store_dwordx2 v234, v[42:43], s[26:27] offset:3584
	global_store_dword v237, v44, s[28:29] offset:1792
	global_load_dwordx2 v[212:213], v234, s[22:23]
	global_load_dwordx4 v[38:41], v178, s[30:31]
	global_load_dwordx2 v[214:215], v234, s[22:23] offset:512
	global_load_dwordx4 v[46:49], v178, s[30:31] offset:1024
	global_load_dwordx2 v[216:217], v234, s[22:23] offset:1024
	global_load_dwordx4 v[54:57], v178, s[30:31] offset:2048
	global_load_dwordx2 v[218:219], v234, s[22:23] offset:1536
	global_load_dwordx4 v[58:61], v178, s[30:31] offset:3072
	global_load_dwordx2 v[220:221], v234, s[22:23] offset:2048
	v_add_co_u32_e64 v42, s[4:5], s41, v62
	v_mul_f32_e32 v44, 0x4b800000, v50
	s_nop 0
	v_addc_co_u32_e64 v43, s[4:5], 0, v63, s[4:5]
	v_cndmask_b32_e32 v44, v50, v44, vcc
	global_load_dwordx4 v[66:69], v[42:43], off
	global_load_dwordx2 v[222:223], v234, s[22:23] offset:2560
	global_load_dwordx4 v[62:65], v[42:43], off offset:1024
	global_load_dwordx2 v[210:211], v234, s[22:23] offset:3072
	v_rsq_f32_e32 v160, v44
	global_load_dwordx4 v[50:53], v[42:43], off offset:2048
	global_load_dwordx2 v[224:225], v234, s[22:23] offset:3584
	s_nop 0
	global_load_dwordx4 v[42:45], v[42:43], off offset:3072
	s_add_u32 s26, s11, s24
	s_addc_u32 s27, s13, s25
	v_mul_f32_e32 v166, 0x45800000, v160
	v_cndmask_b32_e32 v166, v160, v166, vcc
	v_pk_mul_f32 v[206:207], v[166:167], v[206:207] op_sel_hi:[0,1]
	v_pk_mul_f32 v[208:209], v[166:167], v[208:209] op_sel_hi:[0,1]
	v_pk_fma_f32 v[162:163], v[98:99], v[206:207], v[162:163]
	v_pk_fma_f32 v[164:165], v[100:101], v[208:209], v[164:165]
	v_and_b32_sdwa v99, v162, v235 dst_sel:DWORD dst_unused:UNUSED_PAD src0_sel:WORD_1 src1_sel:DWORD
	v_add3_u32 v100, v162, v99, s44
	v_and_b32_sdwa v99, v165, v235 dst_sel:DWORD dst_unused:UNUSED_PAD src0_sel:WORD_1 src1_sel:DWORD
	v_and_b32_sdwa v101, v163, v235 dst_sel:DWORD dst_unused:UNUSED_PAD src0_sel:WORD_1 src1_sel:DWORD
	v_and_b32_sdwa v98, v164, v235 dst_sel:DWORD dst_unused:UNUSED_PAD src0_sel:WORD_1 src1_sel:DWORD
	v_add3_u32 v99, v165, v99, s44
	v_add3_u32 v101, v163, v101, s44
	v_add3_u32 v98, v164, v98, s44
	v_and_b32_e32 v99, 0xffff0000, v99
	v_and_b32_e32 v101, 0xffff0000, v101
	v_or_b32_sdwa v99, v99, v98 dst_sel:DWORD dst_unused:UNUSED_PAD src0_sel:DWORD src1_sel:WORD_1
	v_or_b32_sdwa v98, v101, v100 dst_sel:DWORD dst_unused:UNUSED_PAD src0_sel:DWORD src1_sel:WORD_1
	global_store_dwordx2 v234, v[98:99], s[14:15] nt
	v_mov_b32_e32 v98, v203
	v_mov_b32_e32 v203, v204
	v_mov_b32_e32 v99, v205
	v_pk_mul_f32 v[100:101], v[166:167], v[202:203] op_sel_hi:[0,1]
	v_pk_mul_f32 v[98:99], v[166:167], v[98:99] op_sel_hi:[0,1]
	v_pk_fma_f32 v[154:155], v[102:103], v[100:101], v[154:155]
	v_pk_fma_f32 v[156:157], v[104:105], v[98:99], v[156:157]
	v_and_b32_sdwa v99, v154, v235 dst_sel:DWORD dst_unused:UNUSED_PAD src0_sel:WORD_1 src1_sel:DWORD
	v_add3_u32 v100, v154, v99, s44
	v_and_b32_sdwa v99, v157, v235 dst_sel:DWORD dst_unused:UNUSED_PAD src0_sel:WORD_1 src1_sel:DWORD
	v_and_b32_sdwa v101, v155, v235 dst_sel:DWORD dst_unused:UNUSED_PAD src0_sel:WORD_1 src1_sel:DWORD
	v_and_b32_sdwa v98, v156, v235 dst_sel:DWORD dst_unused:UNUSED_PAD src0_sel:WORD_1 src1_sel:DWORD
	v_add3_u32 v99, v157, v99, s44
	v_add3_u32 v101, v155, v101, s44
	v_add3_u32 v98, v156, v98, s44
	v_and_b32_e32 v99, 0xffff0000, v99
	v_and_b32_e32 v101, 0xffff0000, v101
	v_or_b32_sdwa v99, v99, v98 dst_sel:DWORD dst_unused:UNUSED_PAD src0_sel:DWORD src1_sel:WORD_1
	v_or_b32_sdwa v98, v101, v100 dst_sel:DWORD dst_unused:UNUSED_PAD src0_sel:DWORD src1_sel:WORD_1
	v_mov_b32_e32 v100, v163
	v_mov_b32_e32 v101, v155
	global_store_dwordx2 v234, v[98:99], s[14:15] offset:512 nt
	v_mov_b32_e32 v98, v162
	v_mov_b32_e32 v99, v154
	v_pk_mul_f32 v[100:101], v[100:101], v[100:101]
	v_mov_b32_e32 v102, v165
	v_pk_fma_f32 v[98:99], v[98:99], v[98:99], v[100:101]
	v_mov_b32_e32 v100, v164
	v_mov_b32_e32 v101, v156
	v_pk_mul_f32 v[100:101], v[100:101], v[100:101]
	v_mov_b32_e32 v103, v157
	v_pk_fma_f32 v[100:101], v[102:103], v[102:103], v[100:101]
	v_pk_mul_f32 v[102:103], v[166:167], v[198:199] op_sel_hi:[0,1]
	v_pk_add_f32 v[98:99], v[98:99], v[100:101]
	v_pk_mul_f32 v[100:101], v[166:167], v[200:201] op_sel_hi:[0,1]
	v_pk_fma_f32 v[150:151], v[106:107], v[102:103], v[150:151]
	v_pk_fma_f32 v[152:153], v[108:109], v[100:101], v[152:153]
	v_pk_add_f32 v[98:99], v[98:99], v[98:99] op_sel_hi:[0,1]
	v_and_b32_sdwa v101, v153, v235 dst_sel:DWORD dst_unused:UNUSED_PAD src0_sel:WORD_1 src1_sel:DWORD
	v_and_b32_sdwa v102, v151, v235 dst_sel:DWORD dst_unused:UNUSED_PAD src0_sel:WORD_1 src1_sel:DWORD
	v_and_b32_sdwa v98, v152, v235 dst_sel:DWORD dst_unused:UNUSED_PAD src0_sel:WORD_1 src1_sel:DWORD
	v_and_b32_sdwa v100, v150, v235 dst_sel:DWORD dst_unused:UNUSED_PAD src0_sel:WORD_1 src1_sel:DWORD
	v_add3_u32 v101, v153, v101, s44
	v_add3_u32 v102, v151, v102, s44
	v_add3_u32 v100, v150, v100, s44
	v_add3_u32 v98, v152, v98, s44
	v_and_b32_e32 v101, 0xffff0000, v101
	v_and_b32_e32 v102, 0xffff0000, v102
	v_or_b32_sdwa v101, v101, v98 dst_sel:DWORD dst_unused:UNUSED_PAD src0_sel:DWORD src1_sel:WORD_1
	v_or_b32_sdwa v100, v102, v100 dst_sel:DWORD dst_unused:UNUSED_PAD src0_sel:DWORD src1_sel:WORD_1
	global_store_dwordx2 v234, v[100:101], s[14:15] offset:1024 nt
	v_pk_mul_f32 v[100:101], v[152:153], v[152:153]
	v_pk_mul_f32 v[102:103], v[150:151], v[150:151]
	v_mov_b32_e32 v106, v192
	v_pk_mov_b32 v[104:105], v[102:103], v[100:101] op_sel:[1,0]
	v_mov_b32_e32 v103, v101
	v_pk_add_f32 v[100:101], v[102:103], v[104:105]
	v_pk_mul_f32 v[102:103], v[196:197], v[166:167] op_sel_hi:[1,0]
	v_pk_mul_f32 v[104:105], v[188:189], v[166:167] op_sel_hi:[1,0]
	v_pk_fma_f32 v[148:149], v[112:113], v[102:103], v[148:149]
	v_pk_fma_f32 v[146:147], v[110:111], v[104:105], v[146:147]
	v_pk_add_f32 v[100:101], v[100:101], v[100:101] op_sel_hi:[0,1]
	v_and_b32_sdwa v102, v149, v235 dst_sel:DWORD dst_unused:UNUSED_PAD src0_sel:WORD_1 src1_sel:DWORD
	v_and_b32_sdwa v103, v147, v235 dst_sel:DWORD dst_unused:UNUSED_PAD src0_sel:WORD_1 src1_sel:DWORD
	v_and_b32_sdwa v98, v148, v235 dst_sel:DWORD dst_unused:UNUSED_PAD src0_sel:WORD_1 src1_sel:DWORD
	v_and_b32_sdwa v100, v146, v235 dst_sel:DWORD dst_unused:UNUSED_PAD src0_sel:WORD_1 src1_sel:DWORD
	v_add3_u32 v102, v149, v102, s44
	v_add3_u32 v103, v147, v103, s44
	v_add3_u32 v100, v146, v100, s44
	v_add3_u32 v98, v148, v98, s44
	v_and_b32_e32 v102, 0xffff0000, v102
	v_and_b32_e32 v104, 0xffff0000, v103
	v_or_b32_sdwa v103, v102, v98 dst_sel:DWORD dst_unused:UNUSED_PAD src0_sel:DWORD src1_sel:WORD_1
	v_or_b32_sdwa v102, v104, v100 dst_sel:DWORD dst_unused:UNUSED_PAD src0_sel:DWORD src1_sel:WORD_1
	v_mul_f32_e32 v98, v146, v146
	v_mov_b32_e32 v107, v194
	v_mov_b32_e32 v194, v193
	global_store_dwordx2 v234, v[102:103], s[14:15] offset:1536 nt
	v_pk_fma_f32 v[102:103], v[146:147], v[146:147], v[98:99] op_sel_hi:[1,1,0]
	v_mul_f32_e32 v98, v148, v148
	v_pk_mul_f32 v[106:107], v[166:167], v[106:107] op_sel_hi:[0,1]
	v_pk_mul_f32 v[108:109], v[166:167], v[194:195] op_sel_hi:[0,1]
	v_pk_fma_f32 v[104:105], v[148:149], v[148:149], v[98:99] op_sel_hi:[1,1,0]
	v_pk_fma_f32 v[144:145], v[116:117], v[108:109], v[144:145]
	v_pk_fma_f32 v[142:143], v[114:115], v[106:107], v[142:143]
	v_and_b32_sdwa v102, v145, v235 dst_sel:DWORD dst_unused:UNUSED_PAD src0_sel:WORD_1 src1_sel:DWORD
	v_and_b32_sdwa v104, v143, v235 dst_sel:DWORD dst_unused:UNUSED_PAD src0_sel:WORD_1 src1_sel:DWORD
	v_and_b32_sdwa v98, v144, v235 dst_sel:DWORD dst_unused:UNUSED_PAD src0_sel:WORD_1 src1_sel:DWORD
	v_and_b32_sdwa v100, v142, v235 dst_sel:DWORD dst_unused:UNUSED_PAD src0_sel:WORD_1 src1_sel:DWORD
	v_add3_u32 v102, v145, v102, s44
	v_add3_u32 v104, v143, v104, s44
	v_add3_u32 v100, v142, v100, s44
	v_add3_u32 v98, v144, v98, s44
	v_and_b32_e32 v102, 0xffff0000, v102
	v_and_b32_e32 v104, 0xffff0000, v104
	v_or_b32_sdwa v107, v102, v98 dst_sel:DWORD dst_unused:UNUSED_PAD src0_sel:DWORD src1_sel:WORD_1
	v_or_b32_sdwa v106, v104, v100 dst_sel:DWORD dst_unused:UNUSED_PAD src0_sel:DWORD src1_sel:WORD_1
	v_mul_f32_e32 v102, v142, v142
	v_mul_f32_e32 v104, v143, v143
	v_mul_f32_e32 v98, v144, v144
	v_mul_f32_e32 v100, v145, v145
	v_pk_add_f32 v[102:103], v[102:103], v[104:105]
	v_pk_add_f32 v[98:99], v[100:101], v[98:99]
	v_mov_b32_e32 v100, v185
	v_mov_b32_e32 v101, v187
	v_mov_b32_e32 v185, v186
	v_pk_add_f32 v[98:99], v[102:103], v[98:99]
	v_pk_mul_f32 v[100:101], v[166:167], v[100:101] op_sel_hi:[0,1]
	v_pk_mul_f32 v[102:103], v[166:167], v[184:185] op_sel_hi:[0,1]
	v_pk_fma_f32 v[184:185], v[118:119], v[102:103], v[138:139]
	v_pk_fma_f32 v[186:187], v[120:121], v[100:101], v[140:141]
	v_pk_add_f32 v[98:99], v[98:99], v[98:99] op_sel_hi:[0,1]
	v_and_b32_sdwa v101, v187, v235 dst_sel:DWORD dst_unused:UNUSED_PAD src0_sel:WORD_1 src1_sel:DWORD
	v_and_b32_sdwa v102, v185, v235 dst_sel:DWORD dst_unused:UNUSED_PAD src0_sel:WORD_1 src1_sel:DWORD
	v_and_b32_sdwa v98, v186, v235 dst_sel:DWORD dst_unused:UNUSED_PAD src0_sel:WORD_1 src1_sel:DWORD
	v_and_b32_sdwa v100, v184, v235 dst_sel:DWORD dst_unused:UNUSED_PAD src0_sel:WORD_1 src1_sel:DWORD
	v_add3_u32 v101, v187, v101, s44
	v_add3_u32 v102, v185, v102, s44
	v_add3_u32 v100, v184, v100, s44
	v_add3_u32 v98, v186, v98, s44
	v_and_b32_e32 v101, 0xffff0000, v101
	v_and_b32_e32 v102, 0xffff0000, v102
	v_or_b32_sdwa v101, v101, v98 dst_sel:DWORD dst_unused:UNUSED_PAD src0_sel:DWORD src1_sel:WORD_1
	v_or_b32_sdwa v100, v102, v100 dst_sel:DWORD dst_unused:UNUSED_PAD src0_sel:DWORD src1_sel:WORD_1
	global_store_dwordx2 v234, v[100:101], s[14:15] offset:2560 nt
	v_pk_mul_f32 v[100:101], v[186:187], v[186:187]
	v_pk_mul_f32 v[102:103], v[184:185], v[184:185]
	v_mov_b32_e32 v160, v167
	v_pk_mov_b32 v[104:105], v[102:103], v[100:101] op_sel:[1,0]
	v_mov_b32_e32 v103, v101
	v_pk_add_f32 v[100:101], v[102:103], v[104:105]
	v_pk_mul_f32 v[102:103], v[166:167], v[182:183] op_sel_hi:[0,1]
	v_pk_mul_f32 v[104:105], v[166:167], v[168:169] op_sel_hi:[0,1]
	v_pk_fma_f32 v[138:139], v[122:123], v[104:105], v[134:135]
	v_pk_fma_f32 v[140:141], v[124:125], v[102:103], v[136:137]
	v_pk_add_f32 v[100:101], v[100:101], v[100:101] op_sel_hi:[0,1]
	v_and_b32_sdwa v102, v141, v235 dst_sel:DWORD dst_unused:UNUSED_PAD src0_sel:WORD_1 src1_sel:DWORD
	v_and_b32_sdwa v103, v139, v235 dst_sel:DWORD dst_unused:UNUSED_PAD src0_sel:WORD_1 src1_sel:DWORD
	v_and_b32_sdwa v98, v140, v235 dst_sel:DWORD dst_unused:UNUSED_PAD src0_sel:WORD_1 src1_sel:DWORD
	v_and_b32_sdwa v100, v138, v235 dst_sel:DWORD dst_unused:UNUSED_PAD src0_sel:WORD_1 src1_sel:DWORD
	v_add3_u32 v102, v141, v102, s44
	v_add3_u32 v103, v139, v103, s44
	v_add3_u32 v100, v138, v100, s44
	v_add3_u32 v98, v140, v98, s44
	v_and_b32_e32 v102, 0xffff0000, v102
	v_and_b32_e32 v104, 0xffff0000, v103
	global_store_dwordx2 v234, v[106:107], s[14:15] offset:2048 nt
	v_or_b32_sdwa v103, v102, v98 dst_sel:DWORD dst_unused:UNUSED_PAD src0_sel:DWORD src1_sel:WORD_1
	v_or_b32_sdwa v102, v104, v100 dst_sel:DWORD dst_unused:UNUSED_PAD src0_sel:DWORD src1_sel:WORD_1
	v_mul_f32_e32 v98, v138, v138
	v_pk_mul_f32 v[106:107], v[160:161], v[166:167] op_sel_hi:[1,0]
	global_store_dwordx2 v234, v[102:103], s[14:15] offset:3072 nt
	v_pk_fma_f32 v[102:103], v[138:139], v[138:139], v[98:99] op_sel_hi:[1,1,0]
	v_mul_f32_e32 v98, v140, v140
	v_pk_mul_f32 v[108:109], v[158:159], v[166:167] op_sel_hi:[1,0]
	s_waitcnt vmcnt(47)
	v_pk_fma_f32 v[136:137], v[126:127], v[106:107], v[130:131]
	v_pk_fma_f32 v[104:105], v[140:141], v[140:141], v[98:99] op_sel_hi:[1,1,0]
	v_pk_fma_f32 v[134:135], v[128:129], v[108:109], v[132:133]
	v_and_b32_sdwa v98, v136, v235 dst_sel:DWORD dst_unused:UNUSED_PAD src0_sel:WORD_1 src1_sel:DWORD
	v_add3_u32 v188, v136, v98, s44
	v_mul_f32_e32 v102, v136, v136
	v_mul_f32_e32 v104, v137, v137
	v_mul_f32_e32 v98, v134, v134
	v_mul_f32_e32 v100, v135, v135
	v_pk_add_f32 v[102:103], v[102:103], v[104:105]
	v_pk_add_f32 v[98:99], v[100:101], v[98:99]
	s_waitcnt vmcnt(22)
	v_and_b32_e32 v131, 0xffff0000, v212
	v_and_b32_e32 v133, 0xffff0000, v213
	v_pk_add_f32 v[158:159], v[102:103], v[98:99]
	v_lshlrev_b32_e32 v130, 16, v212
	v_lshlrev_b32_e32 v132, 16, v213
	v_mul_f32_e32 v98, v133, v133
	s_waitcnt vmcnt(20)
	v_and_b32_e32 v129, 0xffff0000, v215
	v_and_b32_e32 v128, 0xffff0000, v214
	v_mul_f32_e32 v102, v131, v131
	v_pk_fma_f32 v[98:99], v[132:133], v[132:133], v[98:99] op_sel_hi:[1,1,0]
	v_lshlrev_b32_e32 v127, 16, v215
	v_lshlrev_b32_e32 v126, 16, v214
	v_pk_mul_f32 v[100:101], v[128:129], v[128:129]
	s_waitcnt vmcnt(16)
	v_lshlrev_b32_e32 v121, 16, v218
	v_pk_fma_f32 v[102:103], v[130:131], v[130:131], v[102:103] op_sel_hi:[1,1,0]
	v_pk_fma_f32 v[100:101], v[126:127], v[126:127], v[100:101]
	v_and_b32_e32 v119, 0xffff0000, v218
	v_mov_b32_e32 v120, v102
	v_mov_b32_e32 v104, v98
	v_mov_b32_e32 v105, v121
	v_mul_f32_e32 v106, v119, v119
	v_pk_add_f32 v[98:99], v[102:103], v[98:99]
	v_pk_mul_f32 v[102:103], v[120:121], v[104:105]
	v_pk_add_f32 v[100:101], v[100:101], v[100:101] op_sel:[0,1] op_sel_hi:[1,0]
	v_and_b32_e32 v123, 0xffff0000, v216
	v_and_b32_e32 v125, 0xffff0000, v217
	v_mov_b32_e32 v99, v103
	v_mov_b32_e32 v101, v106
	v_lshlrev_b32_e32 v122, 16, v216
	v_lshlrev_b32_e32 v124, 16, v217
	v_lshlrev_b32_e32 v116, 16, v219
	v_and_b32_e32 v117, 0xffff0000, v219
	v_pk_add_f32 v[98:99], v[98:99], v[100:101]
	v_mul_f32_e32 v100, v123, v123
	v_mul_f32_e32 v102, v125, v125
	v_mul_f32_e32 v107, v116, v116
	v_mul_f32_e32 v108, v117, v117
	v_pk_fma_f32 v[100:101], v[122:123], v[122:123], v[100:101] op_sel_hi:[1,1,0]
	v_pk_fma_f32 v[102:103], v[124:125], v[124:125], v[102:103] op_sel_hi:[1,1,0]
	v_mov_b32_e32 v101, v107
	v_mov_b32_e32 v103, v108
	v_pk_add_f32 v[100:101], v[100:101], v[102:103]
	s_waitcnt vmcnt(14)
	v_and_b32_e32 v115, 0xffff0000, v221
	v_and_b32_e32 v114, 0xffff0000, v220
	v_pk_add_f32 v[160:161], v[98:99], v[100:101]
	v_lshlrev_b32_e32 v113, 16, v221
	v_lshlrev_b32_e32 v112, 16, v220
	v_pk_mul_f32 v[98:99], v[114:115], v[114:115]
	s_waitcnt vmcnt(12)
	v_and_b32_e32 v111, 0xffff0000, v223
	v_pk_fma_f32 v[98:99], v[112:113], v[112:113], v[98:99]
	v_and_b32_e32 v110, 0xffff0000, v222
	v_pk_add_f32 v[166:167], v[98:99], v[98:99] op_sel:[0,1] op_sel_hi:[1,0]
	s_waitcnt vmcnt(8)
	v_lshlrev_b32_e32 v103, 16, v224
	v_pk_add_f32 v[160:161], v[160:161], v[160:161] op_sel:[0,1] op_sel_hi:[1,0]
	v_lshlrev_b32_e32 v109, 16, v223
	v_lshlrev_b32_e32 v108, 16, v222
	v_pk_mul_f32 v[98:99], v[110:111], v[110:111]
	v_mov_b32_e32 v102, v160
	v_mov_b32_e32 v182, v166
	v_mov_b32_e32 v183, v103
	v_pk_fma_f32 v[168:169], v[108:109], v[108:109], v[98:99]
	v_and_b32_e32 v101, 0xffff0000, v224
	v_pk_add_f32 v[160:161], v[160:161], v[166:167]
	v_pk_mul_f32 v[166:167], v[102:103], v[182:183]
	v_and_b32_e32 v105, 0xffff0000, v210
	v_mul_f32_e32 v100, v101, v101
	v_mov_b32_e32 v161, v167
	v_pk_add_f32 v[166:167], v[168:169], v[168:169] op_sel:[0,1] op_sel_hi:[1,0]
	v_lshlrev_b32_e32 v104, 16, v210
	v_and_b32_e32 v107, 0xffff0000, v211
	v_mov_b32_e32 v167, v100
	v_mul_f32_e32 v100, v105, v105
	v_lshlrev_b32_e32 v106, 16, v211
	v_lshlrev_b32_e32 v98, 16, v225
	v_and_b32_e32 v99, 0xffff0000, v225
	v_pk_add_f32 v[160:161], v[160:161], v[166:167]
	v_pk_fma_f32 v[166:167], v[104:105], v[104:105], v[100:101] op_sel_hi:[1,1,0]
	v_mul_f32_e32 v100, v107, v107
	v_mul_f32_e32 v120, v98, v98
	v_mul_f32_e32 v189, v99, v99
	v_pk_fma_f32 v[168:169], v[106:107], v[106:107], v[100:101] op_sel_hi:[1,1,0]
	v_mov_b32_e32 v167, v120
	v_mov_b32_e32 v169, v189
	v_pk_add_f32 v[166:167], v[166:167], v[168:169]
	v_and_b32_sdwa v118, v134, v235 dst_sel:DWORD dst_unused:UNUSED_PAD src0_sel:WORD_1 src1_sel:DWORD
	v_pk_add_f32 v[160:161], v[160:161], v[166:167]
	v_mov_b32_e32 v167, v158
	v_mov_b32_e32 v166, v160
	v_mov_b32_e32 v158, v161
	v_pk_add_f32 v[158:159], v[166:167], v[158:159]
	ds_bpermute_b32 v161, v171, v159
	ds_bpermute_b32 v160, v171, v158
	v_add3_u32 v100, v134, v118, s44
	v_and_b32_sdwa v102, v135, v235 dst_sel:DWORD dst_unused:UNUSED_PAD src0_sel:WORD_1 src1_sel:DWORD
	v_and_b32_sdwa v118, v137, v235 dst_sel:DWORD dst_unused:UNUSED_PAD src0_sel:WORD_1 src1_sel:DWORD
	v_add3_u32 v102, v135, v102, s44
	s_waitcnt lgkmcnt(0)
	v_pk_add_f32 v[158:159], v[158:159], v[160:161]
	ds_bpermute_b32 v161, v226, v159
	ds_bpermute_b32 v160, v226, v158
	v_add3_u32 v118, v137, v118, s44
	s_add_u32 s28, s33, s16
	v_and_b32_e32 v102, 0xffff0000, v102
	v_and_b32_e32 v118, 0xffff0000, v118
	s_waitcnt lgkmcnt(0)
	v_pk_add_f32 v[158:159], v[158:159], v[160:161]
	ds_bpermute_b32 v161, v228, v159
	ds_bpermute_b32 v160, v228, v158
	s_addc_u32 s29, s34, s17
	s_add_i32 s4, s8, -1
	v_or_b32_sdwa v167, v102, v100 dst_sel:DWORD dst_unused:UNUSED_PAD src0_sel:DWORD src1_sel:WORD_1
	v_or_b32_sdwa v166, v118, v188 dst_sel:DWORD dst_unused:UNUSED_PAD src0_sel:DWORD src1_sel:WORD_1
	s_waitcnt lgkmcnt(0)
	v_pk_add_f32 v[158:159], v[158:159], v[160:161]
	ds_bpermute_b32 v161, v229, v159
	ds_bpermute_b32 v160, v229, v158
	s_ashr_i32 s5, s4, 31
	global_store_dwordx2 v234, v[166:167], s[14:15] offset:3584 nt
	s_lshl_b64 s[14:15], s[4:5], 11
	s_lshl_b64 s[16:17], s[4:5], 12
	s_waitcnt lgkmcnt(0)
	v_pk_add_f32 v[158:159], v[158:159], v[160:161]
	ds_bpermute_b32 v161, v230, v159
	ds_bpermute_b32 v160, v230, v158
	s_add_u32 s24, s96, s16
	s_addc_u32 s25, s97, s17
	s_lshl_b64 s[4:5], s[4:5], 13
	s_add_u32 s30, s6, s4
	s_waitcnt lgkmcnt(0)
	v_pk_add_f32 v[158:159], v[158:159], v[160:161]
	ds_bpermute_b32 v161, v231, v159
	ds_bpermute_b32 v160, v231, v158
	s_addc_u32 s31, s7, s5
	v_lshl_add_u64 v[166:167], s[30:31], 0, v[178:179]
	s_add_u32 s22, s35, s20
	s_addc_u32 s23, s36, s21
	s_waitcnt lgkmcnt(0)
	v_pk_add_f32 v[158:159], v[158:159], v[160:161]
	v_mov_b32_e32 v118, v121
	v_pk_fma_f32 v[158:159], v[158:159], s[10:11], v[180:181] op_sel_hi:[1,0,0]
	s_add_u32 s20, s11, s20
	v_mul_f32_e32 v100, 0x4b800000, v159
	v_cmp_gt_f32_e64 s[4:5], s43, v159
	v_cmp_gt_f32_e32 vcc, s43, v158
	s_addc_u32 s21, s13, s21
	v_cndmask_b32_e64 v100, v159, v100, s[4:5]
	v_rsq_f32_e32 v100, v100
	s_add_u32 s18, s33, s18
	s_addc_u32 s19, s34, s19
	s_ashr_i32 s9, s8, 31
	v_mul_f32_e32 v102, 0x45800000, v100
	v_cndmask_b32_e64 v100, v100, v102, s[4:5]
	v_pk_mul_f32 v[160:161], v[162:163], v[100:101] op_sel_hi:[1,0]
	v_pk_mul_f32 v[162:163], v[164:165], v[100:101] op_sel_hi:[1,0]
	v_pk_fma_f32 v[26:27], v[26:27], v[160:161], v[30:31]
	v_pk_fma_f32 v[28:29], v[28:29], v[162:163], v[32:33]
	v_bfe_u32 v30, v26, 16, 1
	v_bfe_u32 v31, v27, 16, 1
	v_add3_u32 v30, v26, v30, s44
	v_add3_u32 v31, v27, v31, s44
	v_med3_f32 v26, v26, s45, v236
	v_med3_f32 v27, v27, s45, v236
	v_mov_b32_e32 v32, 0
	v_cvt_pk_fp8_f32 v32, v26, v27
	v_lshrrev_b32_e32 v30, 16, v30
	v_and_or_b32 v30, v31, s42, v30
	v_bfe_u32 v31, v28, 16, 1
	v_add3_u32 v31, v28, v31, s44
	v_bfe_u32 v26, v29, 16, 1
	v_med3_f32 v27, v28, s45, v236
	v_med3_f32 v28, v29, s45, v236
	v_lshrrev_b32_e32 v31, 16, v31
	v_cvt_pk_fp8_f32 v32, v27, v28 op_sel:[0,0,1]
	v_add3_u32 v26, v29, v26, s44
	v_and_or_b32 v31, v26, s42, v31
	v_pk_mul_f32 v[26:27], v[154:155], v[100:101] op_sel_hi:[1,0]
	global_store_dwordx2 v234, v[30:31], s[26:27]
	global_store_dword v237, v32, s[28:29]
	v_pk_fma_f32 v[26:27], v[90:91], v[26:27], v[94:95]
	v_mov_b32_e32 v32, 0
	v_bfe_u32 v30, v26, 16, 1
	v_bfe_u32 v31, v27, 16, 1
	v_add3_u32 v30, v26, v30, s44
	v_add3_u32 v31, v27, v31, s44
	v_med3_f32 v26, v26, s45, v236
	v_med3_f32 v27, v27, s45, v236
	v_pk_mul_f32 v[28:29], v[156:157], v[100:101] op_sel_hi:[1,0]
	v_cvt_pk_fp8_f32 v32, v26, v27
	v_pk_fma_f32 v[28:29], v[92:93], v[28:29], v[96:97]
	v_lshrrev_b32_e32 v30, 16, v30
	v_and_or_b32 v30, v31, s42, v30
	v_bfe_u32 v31, v28, 16, 1
	v_add3_u32 v31, v28, v31, s44
	v_bfe_u32 v26, v29, 16, 1
	v_med3_f32 v27, v28, s45, v236
	v_med3_f32 v28, v29, s45, v236
	v_lshrrev_b32_e32 v31, 16, v31
	v_cvt_pk_fp8_f32 v32, v27, v28 op_sel:[0,0,1]
	v_add3_u32 v26, v29, v26, s44
	v_and_or_b32 v31, v26, s42, v31
	v_pk_mul_f32 v[26:27], v[150:151], v[100:101] op_sel_hi:[1,0]
	global_store_dwordx2 v234, v[30:31], s[26:27] offset:512
	global_store_dword v237, v32, s[28:29] offset:256
	v_pk_fma_f32 v[26:27], v[82:83], v[26:27], v[86:87]
	v_mov_b32_e32 v32, 0
	v_bfe_u32 v30, v26, 16, 1
	v_bfe_u32 v31, v27, 16, 1
	v_add3_u32 v30, v26, v30, s44
	v_add3_u32 v31, v27, v31, s44
	v_med3_f32 v26, v26, s45, v236
	v_med3_f32 v27, v27, s45, v236
	v_pk_mul_f32 v[28:29], v[152:153], v[100:101] op_sel_hi:[1,0]
	v_cvt_pk_fp8_f32 v32, v26, v27
	v_pk_fma_f32 v[28:29], v[84:85], v[28:29], v[88:89]
	v_lshrrev_b32_e32 v30, 16, v30
	v_and_or_b32 v30, v31, s42, v30
	v_bfe_u32 v31, v28, 16, 1
	v_add3_u32 v31, v28, v31, s44
	v_bfe_u32 v26, v29, 16, 1
	v_med3_f32 v27, v28, s45, v236
	v_med3_f32 v28, v29, s45, v236
	v_lshrrev_b32_e32 v31, 16, v31
	v_cvt_pk_fp8_f32 v32, v27, v28 op_sel:[0,0,1]
	v_add3_u32 v26, v29, v26, s44
	v_and_or_b32 v31, v26, s42, v31
	v_pk_mul_f32 v[26:27], v[146:147], v[100:101] op_sel_hi:[1,0]
	global_store_dwordx2 v234, v[30:31], s[26:27] offset:1024
	global_store_dword v237, v32, s[28:29] offset:512
	v_pk_fma_f32 v[26:27], v[74:75], v[26:27], v[78:79]
	v_mov_b32_e32 v32, 0
	v_bfe_u32 v30, v26, 16, 1
	v_bfe_u32 v31, v27, 16, 1
	v_add3_u32 v30, v26, v30, s44
	v_add3_u32 v31, v27, v31, s44
	v_med3_f32 v26, v26, s45, v236
	v_med3_f32 v27, v27, s45, v236
	v_pk_mul_f32 v[28:29], v[148:149], v[100:101] op_sel_hi:[1,0]
	v_cvt_pk_fp8_f32 v32, v26, v27
	v_pk_fma_f32 v[28:29], v[76:77], v[28:29], v[80:81]
	v_lshrrev_b32_e32 v30, 16, v30
	v_and_or_b32 v30, v31, s42, v30
	v_bfe_u32 v31, v28, 16, 1
	v_add3_u32 v31, v28, v31, s44
	v_bfe_u32 v26, v29, 16, 1
	v_med3_f32 v27, v28, s45, v236
	v_med3_f32 v28, v29, s45, v236
	v_lshrrev_b32_e32 v31, 16, v31
	v_cvt_pk_fp8_f32 v32, v27, v28 op_sel:[0,0,1]
	v_add3_u32 v26, v29, v26, s44
	v_and_or_b32 v31, v26, s42, v31
	v_pk_mul_f32 v[26:27], v[142:143], v[100:101] op_sel_hi:[1,0]
	global_store_dwordx2 v234, v[30:31], s[26:27] offset:1536
	global_store_dword v237, v32, s[28:29] offset:768
	v_pk_fma_f32 v[26:27], v[34:35], v[26:27], v[70:71]
	v_pk_mul_f32 v[28:29], v[144:145], v[100:101] op_sel_hi:[1,0]
	v_bfe_u32 v30, v26, 16, 1
	v_bfe_u32 v31, v27, 16, 1
	v_add3_u32 v30, v26, v30, s44
	v_add3_u32 v31, v27, v31, s44
	v_med3_f32 v26, v26, s45, v236
	v_med3_f32 v27, v27, s45, v236
	v_mov_b32_e32 v32, 0
	v_pk_fma_f32 v[28:29], v[36:37], v[28:29], v[72:73]
	v_lshrrev_b32_e32 v30, 16, v30
	v_cvt_pk_fp8_f32 v32, v26, v27
	v_and_or_b32 v30, v31, s42, v30
	v_bfe_u32 v31, v28, 16, 1
	v_add3_u32 v31, v28, v31, s44
	v_bfe_u32 v26, v29, 16, 1
	v_lshrrev_b32_e32 v31, 16, v31
	v_med3_f32 v27, v28, s45, v236
	v_med3_f32 v28, v29, s45, v236
	v_add3_u32 v26, v29, v26, s44
	v_cvt_pk_fp8_f32 v32, v27, v28 op_sel:[0,0,1]
	v_and_or_b32 v31, v26, s42, v31
	v_pk_mul_f32 v[26:27], v[184:185], v[100:101] op_sel_hi:[1,0]
	v_pk_mul_f32 v[28:29], v[186:187], v[100:101] op_sel_hi:[1,0]
	v_pk_fma_f32 v[18:19], v[18:19], v[26:27], v[22:23]
	v_pk_fma_f32 v[20:21], v[20:21], v[28:29], v[24:25]
	v_bfe_u32 v22, v18, 16, 1
	v_bfe_u32 v23, v19, 16, 1
	v_add3_u32 v22, v18, v22, s44
	v_add3_u32 v23, v19, v23, s44
	v_med3_f32 v18, v18, s45, v236
	v_med3_f32 v19, v19, s45, v236
	v_mov_b32_e32 v24, 0
	v_lshrrev_b32_e32 v22, 16, v22
	v_cvt_pk_fp8_f32 v24, v18, v19
	v_and_or_b32 v22, v23, s42, v22
	v_bfe_u32 v23, v20, 16, 1
	v_add3_u32 v23, v20, v23, s44
	v_bfe_u32 v18, v21, 16, 1
	v_lshrrev_b32_e32 v23, 16, v23
	v_med3_f32 v19, v20, s45, v236
	v_med3_f32 v20, v21, s45, v236
	v_add3_u32 v18, v21, v18, s44
	v_cvt_pk_fp8_f32 v24, v19, v20 op_sel:[0,0,1]
	v_and_or_b32 v23, v18, s42, v23
	v_pk_mul_f32 v[18:19], v[138:139], v[100:101] op_sel_hi:[1,0]
	v_pk_mul_f32 v[20:21], v[140:141], v[100:101] op_sel_hi:[1,0]
	v_pk_fma_f32 v[10:11], v[10:11], v[18:19], v[14:15]
	v_pk_fma_f32 v[12:13], v[12:13], v[20:21], v[16:17]
	v_bfe_u32 v14, v10, 16, 1
	v_bfe_u32 v15, v11, 16, 1
	v_add3_u32 v14, v10, v14, s44
	v_add3_u32 v15, v11, v15, s44
	v_med3_f32 v10, v10, s45, v236
	v_med3_f32 v11, v11, s45, v236
	v_mov_b32_e32 v16, 0
	v_lshrrev_b32_e32 v14, 16, v14
	v_cvt_pk_fp8_f32 v16, v10, v11
	v_and_or_b32 v14, v15, s42, v14
	v_bfe_u32 v15, v12, 16, 1
	v_add3_u32 v15, v12, v15, s44
	v_bfe_u32 v10, v13, 16, 1
	v_lshrrev_b32_e32 v15, 16, v15
	v_med3_f32 v11, v12, s45, v236
	v_med3_f32 v12, v13, s45, v236
	v_add3_u32 v10, v13, v10, s44
	v_cvt_pk_fp8_f32 v16, v11, v12 op_sel:[0,0,1]
	v_and_or_b32 v15, v10, s42, v15
	v_pk_mul_f32 v[10:11], v[136:137], v[100:101] op_sel_hi:[1,0]
	v_pk_mul_f32 v[12:13], v[134:135], v[100:101] op_sel_hi:[1,0]
	v_pk_fma_f32 v[2:3], v[2:3], v[10:11], v[6:7]
	v_pk_fma_f32 v[4:5], v[4:5], v[12:13], v[8:9]
	v_bfe_u32 v6, v2, 16, 1
	v_bfe_u32 v7, v3, 16, 1
	v_add3_u32 v6, v2, v6, s44
	v_add3_u32 v7, v3, v7, s44
	v_med3_f32 v2, v2, s45, v236
	v_med3_f32 v3, v3, s45, v236
	v_mov_b32_e32 v8, 0
	v_cvt_pk_fp8_f32 v8, v2, v3
	v_lshrrev_b32_e32 v6, 16, v6
	v_and_or_b32 v6, v7, s42, v6
	v_bfe_u32 v7, v4, 16, 1
	v_add3_u32 v7, v4, v7, s44
	v_med3_f32 v3, v4, s45, v236
	v_med3_f32 v4, v5, s45, v236
	v_bfe_u32 v2, v5, 16, 1
	v_cvt_pk_fp8_f32 v8, v3, v4 op_sel:[0,0,1]
	v_mul_f32_e32 v4, 0x4b800000, v158
	v_lshrrev_b32_e32 v7, 16, v7
	v_add3_u32 v2, v5, v2, s44
	v_cndmask_b32_e32 v4, v158, v4, vcc
	v_and_or_b32 v7, v2, s42, v7
	v_add_co_u32_e64 v2, s[4:5], s41, v166
	v_rsq_f32_e32 v86, v4
	global_store_dwordx2 v234, v[30:31], s[26:27] offset:2048
	global_store_dword v237, v32, s[28:29] offset:1024
	global_store_dwordx2 v234, v[22:23], s[26:27] offset:2560
	global_store_dword v237, v24, s[28:29] offset:1280
	global_store_dwordx2 v234, v[14:15], s[26:27] offset:3072
	global_store_dword v237, v16, s[28:29] offset:1536
	global_store_dwordx2 v234, v[6:7], s[26:27] offset:3584
	global_store_dword v237, v8, s[28:29] offset:1792
	v_addc_co_u32_e64 v3, s[4:5], 0, v167, s[4:5]
	global_load_dwordx2 v[84:85], v234, s[24:25]
	global_load_dwordx4 v[30:33], v178, s[30:31]
	global_load_dwordx2 v[82:83], v234, s[24:25] offset:512
	global_load_dwordx4 v[26:29], v178, s[30:31] offset:1024
	global_load_dwordx2 v[80:81], v234, s[24:25] offset:1024
	global_load_dwordx4 v[22:25], v178, s[30:31] offset:2048
	global_load_dwordx2 v[78:79], v234, s[24:25] offset:1536
	global_load_dwordx4 v[18:21], v178, s[30:31] offset:3072
	global_load_dwordx2 v[76:77], v234, s[24:25] offset:2048
	global_load_dwordx4 v[14:17], v[2:3], off
	global_load_dwordx2 v[74:75], v234, s[24:25] offset:2560
	global_load_dwordx4 v[10:13], v[2:3], off offset:1024
	global_load_dwordx2 v[70:71], v234, s[24:25] offset:3072
	global_load_dwordx4 v[6:9], v[2:3], off offset:2048
	global_load_dwordx2 v[72:73], v234, s[24:25] offset:3584
	s_nop 0
	global_load_dwordx4 v[2:5], v[2:3], off offset:3072
	ds_read_b128 v[34:37], v233
	v_mul_f32_e32 v87, 0x45800000, v86
	v_cndmask_b32_e32 v86, v86, v87, vcc
	v_pk_mul_f32 v[88:89], v[86:87], v[130:131] op_sel_hi:[0,1]
	v_pk_mul_f32 v[90:91], v[86:87], v[132:133] op_sel_hi:[0,1]
	s_waitcnt lgkmcnt(0)
	v_pk_fma_f32 v[132:133], v[34:35], v[88:89], v[38:39]
	v_pk_fma_f32 v[130:131], v[36:37], v[90:91], v[40:41]
	v_and_b32_sdwa v39, v132, v235 dst_sel:DWORD dst_unused:UNUSED_PAD src0_sel:WORD_1 src1_sel:DWORD
	v_add3_u32 v40, v132, v39, s44
	v_and_b32_sdwa v39, v131, v235 dst_sel:DWORD dst_unused:UNUSED_PAD src0_sel:WORD_1 src1_sel:DWORD
	v_and_b32_sdwa v41, v133, v235 dst_sel:DWORD dst_unused:UNUSED_PAD src0_sel:WORD_1 src1_sel:DWORD
	v_and_b32_sdwa v38, v130, v235 dst_sel:DWORD dst_unused:UNUSED_PAD src0_sel:WORD_1 src1_sel:DWORD
	v_add3_u32 v39, v131, v39, s44
	v_add3_u32 v41, v133, v41, s44
	v_add3_u32 v38, v130, v38, s44
	v_and_b32_e32 v39, 0xffff0000, v39
	v_and_b32_e32 v41, 0xffff0000, v41
	v_or_b32_sdwa v39, v39, v38 dst_sel:DWORD dst_unused:UNUSED_PAD src0_sel:DWORD src1_sel:WORD_1
	v_or_b32_sdwa v38, v41, v40 dst_sel:DWORD dst_unused:UNUSED_PAD src0_sel:DWORD src1_sel:WORD_1
	global_store_dwordx2 v234, v[38:39], s[22:23] nt
	ds_read_b128 v[38:41], v233 offset:1024
	v_mov_b32_e32 v88, v126
	v_mov_b32_e32 v89, v128
	v_pk_mul_f32 v[88:89], v[86:87], v[88:89] op_sel_hi:[0,1]
	v_mov_b32_e32 v128, v127
	v_pk_mul_f32 v[90:91], v[86:87], v[128:129] op_sel_hi:[0,1]
	s_waitcnt lgkmcnt(0)
	v_pk_fma_f32 v[136:137], v[38:39], v[88:89], v[46:47]
	v_pk_fma_f32 v[134:135], v[40:41], v[90:91], v[48:49]
	v_and_b32_sdwa v47, v136, v235 dst_sel:DWORD dst_unused:UNUSED_PAD src0_sel:WORD_1 src1_sel:DWORD
	v_add3_u32 v48, v136, v47, s44
	v_and_b32_sdwa v47, v135, v235 dst_sel:DWORD dst_unused:UNUSED_PAD src0_sel:WORD_1 src1_sel:DWORD
	v_and_b32_sdwa v49, v137, v235 dst_sel:DWORD dst_unused:UNUSED_PAD src0_sel:WORD_1 src1_sel:DWORD
	v_and_b32_sdwa v46, v134, v235 dst_sel:DWORD dst_unused:UNUSED_PAD src0_sel:WORD_1 src1_sel:DWORD
	v_add3_u32 v47, v135, v47, s44
	v_add3_u32 v49, v137, v49, s44
	v_add3_u32 v46, v134, v46, s44
	v_and_b32_e32 v47, 0xffff0000, v47
	v_and_b32_e32 v49, 0xffff0000, v49
	v_or_b32_sdwa v47, v47, v46 dst_sel:DWORD dst_unused:UNUSED_PAD src0_sel:DWORD src1_sel:WORD_1
	v_or_b32_sdwa v46, v49, v48 dst_sel:DWORD dst_unused:UNUSED_PAD src0_sel:DWORD src1_sel:WORD_1
	v_mov_b32_e32 v48, v133
	v_mov_b32_e32 v49, v137
	global_store_dwordx2 v234, v[46:47], s[22:23] offset:512 nt
	v_mov_b32_e32 v46, v132
	v_mov_b32_e32 v47, v136
	v_pk_mul_f32 v[48:49], v[48:49], v[48:49]
	v_pk_mul_f32 v[92:93], v[86:87], v[124:125] op_sel_hi:[0,1]
	v_pk_fma_f32 v[88:89], v[46:47], v[46:47], v[48:49]
	v_mov_b32_e32 v46, v130
	v_mov_b32_e32 v47, v134
	v_pk_mul_f32 v[46:47], v[46:47], v[46:47]
	v_mov_b32_e32 v48, v131
	v_mov_b32_e32 v49, v135
	v_pk_fma_f32 v[90:91], v[48:49], v[48:49], v[46:47]
	ds_read_b128 v[46:49], v233 offset:2048
	v_pk_add_f32 v[88:89], v[88:89], v[90:91]
	v_pk_mul_f32 v[90:91], v[86:87], v[122:123] op_sel_hi:[0,1]
	v_pk_mul_f32 v[94:95], v[116:117], v[86:87] op_sel_hi:[1,0]
	v_mov_b32_e32 v96, v112
	s_waitcnt lgkmcnt(0)
	v_pk_fma_f32 v[140:141], v[46:47], v[90:91], v[54:55]
	v_pk_fma_f32 v[138:139], v[48:49], v[92:93], v[56:57]
	v_and_b32_sdwa v55, v140, v235 dst_sel:DWORD dst_unused:UNUSED_PAD src0_sel:WORD_1 src1_sel:DWORD
	v_add3_u32 v56, v140, v55, s44
	v_and_b32_sdwa v55, v139, v235 dst_sel:DWORD dst_unused:UNUSED_PAD src0_sel:WORD_1 src1_sel:DWORD
	v_and_b32_sdwa v57, v141, v235 dst_sel:DWORD dst_unused:UNUSED_PAD src0_sel:WORD_1 src1_sel:DWORD
	v_and_b32_sdwa v54, v138, v235 dst_sel:DWORD dst_unused:UNUSED_PAD src0_sel:WORD_1 src1_sel:DWORD
	v_add3_u32 v55, v139, v55, s44
	v_add3_u32 v57, v141, v57, s44
	v_add3_u32 v54, v138, v54, s44
	v_and_b32_e32 v55, 0xffff0000, v55
	v_and_b32_e32 v57, 0xffff0000, v57
	v_or_b32_sdwa v55, v55, v54 dst_sel:DWORD dst_unused:UNUSED_PAD src0_sel:DWORD src1_sel:WORD_1
	v_or_b32_sdwa v54, v57, v56 dst_sel:DWORD dst_unused:UNUSED_PAD src0_sel:DWORD src1_sel:WORD_1
	global_store_dwordx2 v234, v[54:55], s[22:23] offset:1024 nt
	v_pk_mul_f32 v[54:55], v[140:141], v[140:141]
	v_pk_mul_f32 v[56:57], v[138:139], v[138:139]
	v_pk_mul_f32 v[92:93], v[118:119], v[86:87] op_sel_hi:[1,0]
	v_pk_mov_b32 v[90:91], v[54:55], v[56:57] op_sel:[1,0]
	v_mov_b32_e32 v55, v57
	v_pk_add_f32 v[90:91], v[54:55], v[90:91]
	ds_read_b128 v[54:57], v233 offset:3072
	v_mov_b32_e32 v97, v114
	v_pk_mul_f32 v[96:97], v[86:87], v[96:97] op_sel_hi:[0,1]
	v_mov_b32_e32 v114, v113
	v_pk_mul_f32 v[112:113], v[86:87], v[114:115] op_sel_hi:[0,1]
	s_waitcnt lgkmcnt(0)
	v_pk_fma_f32 v[144:145], v[54:55], v[92:93], v[58:59]
	v_pk_fma_f32 v[142:143], v[56:57], v[94:95], v[60:61]
	v_and_b32_sdwa v59, v144, v235 dst_sel:DWORD dst_unused:UNUSED_PAD src0_sel:WORD_1 src1_sel:DWORD
	v_add3_u32 v60, v144, v59, s44
	v_and_b32_sdwa v59, v143, v235 dst_sel:DWORD dst_unused:UNUSED_PAD src0_sel:WORD_1 src1_sel:DWORD
	v_and_b32_sdwa v61, v145, v235 dst_sel:DWORD dst_unused:UNUSED_PAD src0_sel:WORD_1 src1_sel:DWORD
	v_and_b32_sdwa v58, v142, v235 dst_sel:DWORD dst_unused:UNUSED_PAD src0_sel:WORD_1 src1_sel:DWORD
	v_add3_u32 v59, v143, v59, s44
	v_add3_u32 v61, v145, v61, s44
	v_add3_u32 v58, v142, v58, s44
	v_and_b32_e32 v59, 0xffff0000, v59
	v_and_b32_e32 v61, 0xffff0000, v61
	v_or_b32_sdwa v59, v59, v58 dst_sel:DWORD dst_unused:UNUSED_PAD src0_sel:DWORD src1_sel:WORD_1
	v_or_b32_sdwa v58, v61, v60 dst_sel:DWORD dst_unused:UNUSED_PAD src0_sel:DWORD src1_sel:WORD_1
	global_store_dwordx2 v234, v[58:59], s[22:23] offset:1536 nt
	v_mul_f32_e32 v58, v144, v144
	v_pk_fma_f32 v[92:93], v[144:145], v[144:145], v[58:59] op_sel_hi:[1,1,0]
	v_mul_f32_e32 v58, v142, v142
	v_pk_fma_f32 v[94:95], v[142:143], v[142:143], v[58:59] op_sel_hi:[1,1,0]
	ds_read_b128 v[58:61], v233 offset:4096
	v_pk_add_f32 v[88:89], v[88:89], v[88:89] op_sel_hi:[0,1]
	v_pk_add_f32 v[90:91], v[90:91], v[90:91] op_sel_hi:[0,1]
	v_mov_b32_e32 v100, v103
	s_waitcnt vmcnt(19)
	v_and_b32_e32 v207, 0xffff0000, v84
	s_waitcnt lgkmcnt(0)
	v_pk_fma_f32 v[148:149], v[58:59], v[96:97], v[66:67]
	v_pk_fma_f32 v[146:147], v[60:61], v[112:113], v[68:69]
	v_and_b32_sdwa v67, v148, v235 dst_sel:DWORD dst_unused:UNUSED_PAD src0_sel:WORD_1 src1_sel:DWORD
	v_add3_u32 v68, v148, v67, s44
	v_and_b32_sdwa v67, v147, v235 dst_sel:DWORD dst_unused:UNUSED_PAD src0_sel:WORD_1 src1_sel:DWORD
	v_and_b32_sdwa v69, v149, v235 dst_sel:DWORD dst_unused:UNUSED_PAD src0_sel:WORD_1 src1_sel:DWORD
	v_and_b32_sdwa v66, v146, v235 dst_sel:DWORD dst_unused:UNUSED_PAD src0_sel:WORD_1 src1_sel:DWORD
	v_add3_u32 v67, v147, v67, s44
	v_add3_u32 v69, v149, v69, s44
	v_add3_u32 v66, v146, v66, s44
	v_and_b32_e32 v67, 0xffff0000, v67
	v_and_b32_e32 v69, 0xffff0000, v69
	v_or_b32_sdwa v67, v67, v66 dst_sel:DWORD dst_unused:UNUSED_PAD src0_sel:DWORD src1_sel:WORD_1
	v_or_b32_sdwa v66, v69, v68 dst_sel:DWORD dst_unused:UNUSED_PAD src0_sel:DWORD src1_sel:WORD_1
	v_mul_f32_e32 v92, v148, v148
	v_mul_f32_e32 v94, v149, v149
	v_mul_f32_e32 v88, v146, v146
	v_mul_f32_e32 v90, v147, v147
	global_store_dwordx2 v234, v[66:67], s[22:23] offset:2048 nt
	v_pk_add_f32 v[66:67], v[92:93], v[94:95]
	v_pk_add_f32 v[68:69], v[90:91], v[88:89]
	v_mov_b32_e32 v90, v108
	v_pk_add_f32 v[66:67], v[66:67], v[68:69]
	v_mov_b32_e32 v91, v110
	v_pk_add_f32 v[88:89], v[66:67], v[66:67] op_sel_hi:[0,1]
	ds_read_b128 v[66:69], v233 offset:5120
	v_pk_mul_f32 v[90:91], v[86:87], v[90:91] op_sel_hi:[0,1]
	v_mov_b32_e32 v110, v109
	v_pk_mul_f32 v[92:93], v[86:87], v[110:111] op_sel_hi:[0,1]
	v_pk_mul_f32 v[94:95], v[86:87], v[106:107] op_sel_hi:[0,1]
	s_waitcnt lgkmcnt(0)
	v_pk_fma_f32 v[152:153], v[66:67], v[90:91], v[62:63]
	v_pk_fma_f32 v[150:151], v[68:69], v[92:93], v[64:65]
	v_and_b32_sdwa v63, v152, v235 dst_sel:DWORD dst_unused:UNUSED_PAD src0_sel:WORD_1 src1_sel:DWORD
	v_add3_u32 v64, v152, v63, s44
	v_and_b32_sdwa v63, v151, v235 dst_sel:DWORD dst_unused:UNUSED_PAD src0_sel:WORD_1 src1_sel:DWORD
	v_and_b32_sdwa v65, v153, v235 dst_sel:DWORD dst_unused:UNUSED_PAD src0_sel:WORD_1 src1_sel:DWORD
	v_and_b32_sdwa v62, v150, v235 dst_sel:DWORD dst_unused:UNUSED_PAD src0_sel:WORD_1 src1_sel:DWORD
	v_add3_u32 v63, v151, v63, s44
	v_add3_u32 v65, v153, v65, s44
	v_add3_u32 v62, v150, v62, s44
	v_and_b32_e32 v63, 0xffff0000, v63
	v_and_b32_e32 v65, 0xffff0000, v65
	v_or_b32_sdwa v63, v63, v62 dst_sel:DWORD dst_unused:UNUSED_PAD src0_sel:DWORD src1_sel:WORD_1
	v_or_b32_sdwa v62, v65, v64 dst_sel:DWORD dst_unused:UNUSED_PAD src0_sel:DWORD src1_sel:WORD_1
	global_store_dwordx2 v234, v[62:63], s[22:23] offset:2560 nt
	v_pk_mul_f32 v[90:91], v[152:153], v[152:153]
	v_pk_mul_f32 v[62:63], v[150:151], v[150:151]
	v_pk_mul_f32 v[96:97], v[100:101], v[86:87] op_sel_hi:[1,0]
	v_pk_mov_b32 v[92:93], v[90:91], v[62:63] op_sel:[1,0]
	v_mov_b32_e32 v91, v63
	ds_read_b128 v[62:65], v233 offset:6144
	v_pk_add_f32 v[90:91], v[90:91], v[92:93]
	v_pk_mul_f32 v[92:93], v[86:87], v[104:105] op_sel_hi:[0,1]
	v_pk_mul_f32 v[86:87], v[98:99], v[86:87] op_sel_hi:[1,0]
	v_and_b32_e32 v209, 0xffff0000, v85
	s_waitcnt lgkmcnt(0)
	v_pk_fma_f32 v[156:157], v[92:93], v[62:63], v[50:51]
	v_pk_fma_f32 v[154:155], v[94:95], v[64:65], v[52:53]
	v_and_b32_sdwa v51, v156, v235 dst_sel:DWORD dst_unused:UNUSED_PAD src0_sel:WORD_1 src1_sel:DWORD
	v_add3_u32 v52, v156, v51, s44
	v_and_b32_sdwa v51, v155, v235 dst_sel:DWORD dst_unused:UNUSED_PAD src0_sel:WORD_1 src1_sel:DWORD
	v_and_b32_sdwa v53, v157, v235 dst_sel:DWORD dst_unused:UNUSED_PAD src0_sel:WORD_1 src1_sel:DWORD
	v_and_b32_sdwa v50, v154, v235 dst_sel:DWORD dst_unused:UNUSED_PAD src0_sel:WORD_1 src1_sel:DWORD
	v_add3_u32 v51, v155, v51, s44
	v_add3_u32 v53, v157, v53, s44
	v_add3_u32 v50, v154, v50, s44
	v_and_b32_e32 v51, 0xffff0000, v51
	v_and_b32_e32 v53, 0xffff0000, v53
	v_or_b32_sdwa v51, v51, v50 dst_sel:DWORD dst_unused:UNUSED_PAD src0_sel:DWORD src1_sel:WORD_1
	v_or_b32_sdwa v50, v53, v52 dst_sel:DWORD dst_unused:UNUSED_PAD src0_sel:DWORD src1_sel:WORD_1
	global_store_dwordx2 v234, v[50:51], s[22:23] offset:3072 nt
	v_mul_f32_e32 v50, v156, v156
	v_pk_fma_f32 v[92:93], v[156:157], v[156:157], v[50:51] op_sel_hi:[1,1,0]
	ds_read_b128 v[50:53], v233 offset:7168
	v_lshlrev_b32_e32 v206, 16, v84
	v_lshlrev_b32_e32 v208, 16, v85
	v_mul_f32_e32 v84, v209, v209
	s_waitcnt vmcnt(16)
	v_lshlrev_b32_e32 v195, 16, v78
	s_waitcnt lgkmcnt(0)
	v_pk_fma_f32 v[160:161], v[96:97], v[50:51], v[42:43]
	v_pk_fma_f32 v[158:159], v[86:87], v[52:53], v[44:45]
	v_and_b32_sdwa v43, v160, v235 dst_sel:DWORD dst_unused:UNUSED_PAD src0_sel:WORD_1 src1_sel:DWORD
	v_and_b32_e32 v193, 0xffff0000, v78
	v_mul_f32_e32 v78, v207, v207
	v_add3_u32 v44, v160, v43, s44
	v_and_b32_sdwa v43, v159, v235 dst_sel:DWORD dst_unused:UNUSED_PAD src0_sel:WORD_1 src1_sel:DWORD
	v_and_b32_sdwa v45, v161, v235 dst_sel:DWORD dst_unused:UNUSED_PAD src0_sel:WORD_1 src1_sel:DWORD
	v_pk_fma_f32 v[84:85], v[208:209], v[208:209], v[84:85] op_sel_hi:[1,1,0]
	v_and_b32_e32 v205, 0xffff0000, v83
	v_and_b32_e32 v204, 0xffff0000, v82
	v_lshlrev_b32_e32 v196, 16, v79
	v_and_b32_e32 v197, 0xffff0000, v79
	v_pk_fma_f32 v[78:79], v[206:207], v[206:207], v[78:79] op_sel_hi:[1,1,0]
	v_pk_add_f32 v[90:91], v[90:91], v[90:91] op_sel_hi:[0,1]
	v_mul_f32_e32 v88, v154, v154
	v_and_b32_sdwa v42, v158, v235 dst_sel:DWORD dst_unused:UNUSED_PAD src0_sel:WORD_1 src1_sel:DWORD
	v_add3_u32 v43, v159, v43, s44
	v_add3_u32 v45, v161, v45, s44
	v_lshlrev_b32_e32 v203, 16, v83
	v_lshlrev_b32_e32 v202, 16, v82
	v_pk_mul_f32 v[82:83], v[204:205], v[204:205]
	v_lshlrev_b32_e32 v198, 16, v80
	v_and_b32_e32 v199, 0xffff0000, v80
	v_lshlrev_b32_e32 v200, 16, v81
	v_and_b32_e32 v201, 0xffff0000, v81
	v_mov_b32_e32 v194, v78
	v_mov_b32_e32 v80, v84
	v_mov_b32_e32 v81, v195
	v_pk_fma_f32 v[94:95], v[154:155], v[154:155], v[88:89] op_sel_hi:[1,1,0]
	v_add3_u32 v42, v158, v42, s44
	v_and_b32_e32 v43, 0xffff0000, v43
	v_and_b32_e32 v45, 0xffff0000, v45
	v_mul_f32_e32 v88, v158, v158
	v_mul_f32_e32 v90, v159, v159
	v_pk_fma_f32 v[82:83], v[202:203], v[202:203], v[82:83]
	v_pk_add_f32 v[78:79], v[78:79], v[84:85]
	v_pk_mul_f32 v[80:81], v[194:195], v[80:81]
	v_or_b32_sdwa v43, v43, v42 dst_sel:DWORD dst_unused:UNUSED_PAD src0_sel:DWORD src1_sel:WORD_1
	v_or_b32_sdwa v42, v45, v44 dst_sel:DWORD dst_unused:UNUSED_PAD src0_sel:DWORD src1_sel:WORD_1
	v_pk_add_f32 v[44:45], v[90:91], v[88:89]
	v_mul_f32_e32 v88, v193, v193
	v_mov_b32_e32 v79, v81
	v_pk_add_f32 v[80:81], v[82:83], v[82:83] op_sel:[0,1] op_sel_hi:[1,0]
	v_mul_f32_e32 v82, v201, v201
	v_mov_b32_e32 v81, v88
	v_pk_add_f32 v[78:79], v[78:79], v[80:81]
	v_mul_f32_e32 v80, v199, v199
	v_mul_f32_e32 v89, v196, v196
	v_mul_f32_e32 v90, v197, v197
	v_pk_fma_f32 v[80:81], v[198:199], v[198:199], v[80:81] op_sel_hi:[1,1,0]
	v_pk_fma_f32 v[82:83], v[200:201], v[200:201], v[82:83] op_sel_hi:[1,1,0]
	v_mov_b32_e32 v81, v89
	v_mov_b32_e32 v83, v90
	s_waitcnt vmcnt(14)
	v_and_b32_e32 v189, 0xffff0000, v77
	v_and_b32_e32 v188, 0xffff0000, v76
	v_pk_add_f32 v[80:81], v[80:81], v[82:83]
	v_lshlrev_b32_e32 v191, 16, v77
	v_lshlrev_b32_e32 v190, 16, v76
	v_pk_mul_f32 v[76:77], v[188:189], v[188:189]
	v_pk_add_f32 v[78:79], v[78:79], v[80:81]
	v_pk_fma_f32 v[76:77], v[190:191], v[190:191], v[76:77]
	s_waitcnt vmcnt(12)
	v_and_b32_e32 v187, 0xffff0000, v75
	v_pk_add_f32 v[76:77], v[76:77], v[76:77] op_sel:[0,1] op_sel_hi:[1,0]
	v_and_b32_e32 v186, 0xffff0000, v74
	s_waitcnt vmcnt(10)
	v_lshlrev_b32_e32 v168, 16, v70
	v_and_b32_e32 v169, 0xffff0000, v70
	v_lshlrev_b32_e32 v182, 16, v71
	v_and_b32_e32 v183, 0xffff0000, v71
	s_waitcnt vmcnt(8)
	v_lshlrev_b32_e32 v167, 16, v72
	v_pk_add_f32 v[70:71], v[78:79], v[78:79] op_sel:[0,1] op_sel_hi:[1,0]
	v_lshlrev_b32_e32 v185, 16, v75
	v_lshlrev_b32_e32 v184, 16, v74
	v_pk_mul_f32 v[74:75], v[186:187], v[186:187]
	v_and_b32_e32 v165, 0xffff0000, v72
	v_lshlrev_b32_e32 v162, 16, v73
	v_and_b32_e32 v163, 0xffff0000, v73
	v_mov_b32_e32 v166, v70
	v_mov_b32_e32 v72, v76
	v_mov_b32_e32 v73, v167
	v_pk_fma_f32 v[74:75], v[184:185], v[184:185], v[74:75]
	v_pk_add_f32 v[70:71], v[70:71], v[76:77]
	v_pk_mul_f32 v[72:73], v[166:167], v[72:73]
	v_mul_f32_e32 v80, v165, v165
	v_mov_b32_e32 v71, v73
	v_pk_add_f32 v[72:73], v[74:75], v[74:75] op_sel:[0,1] op_sel_hi:[1,0]
	v_mul_f32_e32 v74, v183, v183
	v_mov_b32_e32 v73, v80
	v_pk_add_f32 v[70:71], v[70:71], v[72:73]
	v_mul_f32_e32 v72, v169, v169
	v_mul_f32_e32 v81, v162, v162
	v_mul_f32_e32 v82, v163, v163
	v_pk_fma_f32 v[72:73], v[168:169], v[168:169], v[72:73] op_sel_hi:[1,1,0]
	v_pk_fma_f32 v[74:75], v[182:183], v[182:183], v[74:75] op_sel_hi:[1,1,0]
	v_mul_f32_e32 v92, v160, v160
	v_mul_f32_e32 v94, v161, v161
	v_mov_b32_e32 v73, v81
	v_mov_b32_e32 v75, v82
	global_store_dwordx2 v234, v[42:43], s[22:23] offset:3584 nt
	v_pk_add_f32 v[42:43], v[92:93], v[94:95]
	v_pk_add_f32 v[72:73], v[72:73], v[74:75]
	v_pk_add_f32 v[86:87], v[42:43], v[44:45]
	v_pk_add_f32 v[70:71], v[70:71], v[72:73]
	v_mov_b32_e32 v73, v86
	v_mov_b32_e32 v72, v70
	v_mov_b32_e32 v86, v71
	v_pk_add_f32 v[70:71], v[72:73], v[86:87]
	ds_bpermute_b32 v73, v171, v71
	ds_bpermute_b32 v72, v171, v70
	s_lshl_b64 s[22:23], s[8:9], 11
	s_lshl_b64 s[24:25], s[8:9], 12
	s_add_u32 s28, s96, s24
	s_addc_u32 s29, s97, s25
	s_waitcnt lgkmcnt(0)
	v_pk_add_f32 v[74:75], v[70:71], v[72:73]
	ds_bpermute_b32 v77, v226, v75
	ds_bpermute_b32 v76, v226, v74
	s_lshl_b64 s[4:5], s[8:9], 13
	s_add_u32 s30, s6, s4
	s_addc_u32 s31, s7, s5
	ds_read_b128 v[42:45], v233 offset:8192
	s_waitcnt lgkmcnt(1)
	v_pk_add_f32 v[114:115], v[74:75], v[76:77]
	ds_bpermute_b32 v117, v228, v115
	ds_bpermute_b32 v116, v228, v114
	ds_read_b128 v[126:129], v233 offset:16384
	ds_read_b128 v[106:109], v233 offset:9216
	ds_read_b128 v[110:113], v233 offset:17408
	ds_read_b128 v[86:89], v233 offset:10240
	ds_read_b128 v[102:105], v233 offset:18432
	ds_read_b128 v[78:81], v233 offset:11264
	ds_read_b128 v[82:85], v233 offset:19456
	ds_read_b128 v[70:73], v233 offset:12288
	ds_read_b128 v[74:77], v233 offset:20480
	ds_read_b128 v[90:93], v233 offset:13312
	ds_read_b128 v[98:101], v233 offset:21504
	ds_read_b128 v[94:97], v233 offset:14336
	s_add_u32 s26, s35, s16
	s_waitcnt lgkmcnt(12)
	v_pk_add_f32 v[210:211], v[114:115], v[116:117]
	ds_bpermute_b32 v213, v229, v211
	ds_bpermute_b32 v212, v229, v210
	ds_read_b128 v[118:121], v233 offset:22528
	ds_read_b128 v[114:117], v233 offset:15360
	ds_read_b128 v[122:125], v233 offset:23552
	s_addc_u32 s27, s36, s17
	s_add_u32 s16, s11, s16
	s_addc_u32 s17, s13, s17
	s_waitcnt lgkmcnt(3)
	v_pk_add_f32 v[210:211], v[210:211], v[212:213]
	ds_bpermute_b32 v213, v230, v211
	ds_bpermute_b32 v212, v230, v210
	s_waitcnt lgkmcnt(0)
	v_pk_add_f32 v[212:213], v[210:211], v[212:213]
	ds_bpermute_b32 v215, v231, v213
	ds_bpermute_b32 v214, v231, v212
	v_lshl_add_u64 v[210:211], s[30:31], 0, v[178:179]
	s_waitcnt lgkmcnt(0)
	v_pk_add_f32 v[212:213], v[212:213], v[214:215]
	s_nop 0
	v_pk_fma_f32 v[214:215], v[212:213], s[10:11], v[180:181] op_sel_hi:[1,0,0]
	s_nop 0
	v_mul_f32_e32 v164, 0x4b800000, v215
	v_cmp_gt_f32_e64 s[4:5], s43, v215
	v_cmp_gt_f32_e32 vcc, s43, v214
	s_nop 0
	v_cndmask_b32_e64 v164, v215, v164, s[4:5]
	v_rsq_f32_e32 v164, v164
	s_nop 0
	v_mul_f32_e32 v166, 0x45800000, v164
	v_cndmask_b32_e64 v164, v164, v166, s[4:5]
	v_pk_mul_f32 v[132:133], v[132:133], v[164:165] op_sel_hi:[1,0]
	v_pk_mul_f32 v[130:131], v[130:131], v[164:165] op_sel_hi:[1,0]
	v_pk_fma_f32 v[132:133], v[42:43], v[132:133], v[126:127]
	v_pk_fma_f32 v[130:131], v[44:45], v[130:131], v[128:129]
	v_bfe_u32 v166, v132, 16, 1
	v_add3_u32 v166, v132, v166, s44
	v_bfe_u32 v192, v133, 16, 1
	v_lshrrev_b32_e32 v166, 16, v166
	v_add3_u32 v192, v133, v192, s44
	v_and_or_b32 v212, v192, s42, v166
	v_med3_f32 v132, v132, s45, v236
	v_med3_f32 v133, v133, s45, v236
	v_mov_b32_e32 v192, 0
	v_cvt_pk_fp8_f32 v192, v132, v133
	v_bfe_u32 v166, v130, 16, 1
	v_add3_u32 v166, v130, v166, s44
	v_bfe_u32 v132, v131, 16, 1
	v_med3_f32 v130, v130, s45, v236
	v_med3_f32 v133, v131, s45, v236
	v_lshrrev_b32_e32 v166, 16, v166
	v_cvt_pk_fp8_f32 v192, v130, v133 op_sel:[0,0,1]
	v_add3_u32 v130, v131, v132, s44
	v_and_or_b32 v213, v130, s42, v166
	v_pk_mul_f32 v[130:131], v[136:137], v[164:165] op_sel_hi:[1,0]
	v_pk_mul_f32 v[132:133], v[134:135], v[164:165] op_sel_hi:[1,0]
	v_pk_fma_f32 v[130:131], v[106:107], v[130:131], v[110:111]
	v_mov_b32_e32 v136, 0
	v_bfe_u32 v134, v130, 16, 1
	v_bfe_u32 v135, v131, 16, 1
	v_add3_u32 v134, v130, v134, s44
	v_add3_u32 v135, v131, v135, s44
	v_med3_f32 v130, v130, s45, v236
	v_med3_f32 v131, v131, s45, v236
	v_cvt_pk_fp8_f32 v136, v130, v131
	v_pk_fma_f32 v[132:133], v[108:109], v[132:133], v[112:113]
	v_lshrrev_b32_e32 v134, 16, v134
	v_and_or_b32 v134, v135, s42, v134
	v_bfe_u32 v135, v132, 16, 1
	v_add3_u32 v135, v132, v135, s44
	v_bfe_u32 v130, v133, 16, 1
	v_med3_f32 v131, v132, s45, v236
	v_med3_f32 v132, v133, s45, v236
	v_lshrrev_b32_e32 v135, 16, v135
	v_cvt_pk_fp8_f32 v136, v131, v132 op_sel:[0,0,1]
	v_add3_u32 v130, v133, v130, s44
	v_and_or_b32 v135, v130, s42, v135
	v_pk_mul_f32 v[130:131], v[140:141], v[164:165] op_sel_hi:[1,0]
	global_store_dwordx2 v234, v[212:213], s[20:21]
	global_store_dword v237, v192, s[18:19]
	v_pk_fma_f32 v[130:131], v[86:87], v[130:131], v[102:103]
	global_store_dwordx2 v234, v[134:135], s[20:21] offset:512
	global_store_dword v237, v136, s[18:19] offset:256
	v_bfe_u32 v134, v130, 16, 1
	v_bfe_u32 v135, v131, 16, 1
	v_add3_u32 v134, v130, v134, s44
	v_add3_u32 v135, v131, v135, s44
	v_med3_f32 v130, v130, s45, v236
	v_med3_f32 v131, v131, s45, v236
	v_mov_b32_e32 v136, 0
	v_pk_mul_f32 v[132:133], v[138:139], v[164:165] op_sel_hi:[1,0]
	v_cvt_pk_fp8_f32 v136, v130, v131
	v_pk_fma_f32 v[132:133], v[88:89], v[132:133], v[104:105]
	v_lshrrev_b32_e32 v134, 16, v134
	v_and_or_b32 v134, v135, s42, v134
	v_bfe_u32 v135, v132, 16, 1
	v_add3_u32 v135, v132, v135, s44
	v_bfe_u32 v130, v133, 16, 1
	v_med3_f32 v131, v132, s45, v236
	v_med3_f32 v132, v133, s45, v236
	v_lshrrev_b32_e32 v135, 16, v135
	v_cvt_pk_fp8_f32 v136, v131, v132 op_sel:[0,0,1]
	v_add3_u32 v130, v133, v130, s44
	v_and_or_b32 v135, v130, s42, v135
	v_pk_mul_f32 v[130:131], v[144:145], v[164:165] op_sel_hi:[1,0]
	global_store_dwordx2 v234, v[134:135], s[20:21] offset:1024
	global_store_dword v237, v136, s[18:19] offset:512
	v_pk_fma_f32 v[130:131], v[130:131], v[78:79], v[82:83]
	v_mov_b32_e32 v136, 0
	v_bfe_u32 v134, v130, 16, 1
	v_bfe_u32 v135, v131, 16, 1
	v_add3_u32 v134, v130, v134, s44
	v_add3_u32 v135, v131, v135, s44
	v_med3_f32 v130, v130, s45, v236
	v_med3_f32 v131, v131, s45, v236
	v_pk_mul_f32 v[132:133], v[142:143], v[164:165] op_sel_hi:[1,0]
	v_cvt_pk_fp8_f32 v136, v130, v131
	v_pk_fma_f32 v[132:133], v[132:133], v[80:81], v[84:85]
	v_lshrrev_b32_e32 v134, 16, v134
	v_and_or_b32 v134, v135, s42, v134
	v_bfe_u32 v135, v132, 16, 1
	v_add3_u32 v135, v132, v135, s44
	v_bfe_u32 v130, v133, 16, 1
	v_med3_f32 v131, v132, s45, v236
	v_med3_f32 v132, v133, s45, v236
	v_lshrrev_b32_e32 v135, 16, v135
	v_cvt_pk_fp8_f32 v136, v131, v132 op_sel:[0,0,1]
	v_add3_u32 v130, v133, v130, s44
	v_and_or_b32 v135, v130, s42, v135
	v_pk_mul_f32 v[130:131], v[148:149], v[164:165] op_sel_hi:[1,0]
	global_store_dwordx2 v234, v[134:135], s[20:21] offset:1536
	global_store_dword v237, v136, s[18:19] offset:768
	v_pk_fma_f32 v[130:131], v[130:131], v[70:71], v[74:75]
	v_mov_b32_e32 v136, 0
	v_bfe_u32 v134, v130, 16, 1
	v_bfe_u32 v135, v131, 16, 1
	v_add3_u32 v134, v130, v134, s44
	v_add3_u32 v135, v131, v135, s44
	v_med3_f32 v130, v130, s45, v236
	v_med3_f32 v131, v131, s45, v236
	v_pk_mul_f32 v[132:133], v[146:147], v[164:165] op_sel_hi:[1,0]
	v_cvt_pk_fp8_f32 v136, v130, v131
	v_pk_fma_f32 v[132:133], v[132:133], v[72:73], v[76:77]
	v_lshrrev_b32_e32 v134, 16, v134
	v_and_or_b32 v134, v135, s42, v134
	v_bfe_u32 v135, v132, 16, 1
	v_add3_u32 v135, v132, v135, s44
	v_bfe_u32 v130, v133, 16, 1
	v_med3_f32 v131, v132, s45, v236
	v_med3_f32 v132, v133, s45, v236
	v_lshrrev_b32_e32 v135, 16, v135
	v_cvt_pk_fp8_f32 v136, v131, v132 op_sel:[0,0,1]
	v_add3_u32 v130, v133, v130, s44
	v_and_or_b32 v135, v130, s42, v135
	v_pk_mul_f32 v[130:131], v[152:153], v[164:165] op_sel_hi:[1,0]
	global_store_dwordx2 v234, v[134:135], s[20:21] offset:2048
	global_store_dword v237, v136, s[18:19] offset:1024
	v_pk_fma_f32 v[130:131], v[130:131], v[90:91], v[98:99]
	v_mov_b32_e32 v136, 0
	v_bfe_u32 v134, v130, 16, 1
	v_bfe_u32 v135, v131, 16, 1
	v_add3_u32 v134, v130, v134, s44
	v_add3_u32 v135, v131, v135, s44
	v_med3_f32 v130, v130, s45, v236
	v_med3_f32 v131, v131, s45, v236
	v_pk_mul_f32 v[132:133], v[150:151], v[164:165] op_sel_hi:[1,0]
	v_cvt_pk_fp8_f32 v136, v130, v131
	v_pk_fma_f32 v[132:133], v[132:133], v[92:93], v[100:101]
	v_lshrrev_b32_e32 v134, 16, v134
	v_and_or_b32 v134, v135, s42, v134
	v_bfe_u32 v135, v132, 16, 1
	v_add3_u32 v135, v132, v135, s44
	v_bfe_u32 v130, v133, 16, 1
	v_med3_f32 v131, v132, s45, v236
	v_med3_f32 v132, v133, s45, v236
	v_lshrrev_b32_e32 v135, 16, v135
	v_cvt_pk_fp8_f32 v136, v131, v132 op_sel:[0,0,1]
	v_add3_u32 v130, v133, v130, s44
	v_and_or_b32 v135, v130, s42, v135
	v_pk_mul_f32 v[130:131], v[156:157], v[164:165] op_sel_hi:[1,0]
	global_store_dwordx2 v234, v[134:135], s[20:21] offset:2560
	global_store_dword v237, v136, s[18:19] offset:1280
	v_pk_fma_f32 v[130:131], v[130:131], v[94:95], v[118:119]
	v_mov_b32_e32 v136, 0
	v_bfe_u32 v134, v130, 16, 1
	v_bfe_u32 v135, v131, 16, 1
	v_add3_u32 v134, v130, v134, s44
	v_add3_u32 v135, v131, v135, s44
	v_med3_f32 v130, v130, s45, v236
	v_med3_f32 v131, v131, s45, v236
	v_pk_mul_f32 v[132:133], v[154:155], v[164:165] op_sel_hi:[1,0]
	v_cvt_pk_fp8_f32 v136, v130, v131
	v_pk_fma_f32 v[132:133], v[132:133], v[96:97], v[120:121]
	v_lshrrev_b32_e32 v134, 16, v134
	v_and_or_b32 v134, v135, s42, v134
	v_bfe_u32 v135, v132, 16, 1
	v_add3_u32 v135, v132, v135, s44
	v_bfe_u32 v130, v133, 16, 1
	v_med3_f32 v131, v132, s45, v236
	v_med3_f32 v132, v133, s45, v236
	v_lshrrev_b32_e32 v135, 16, v135
	v_cvt_pk_fp8_f32 v136, v131, v132 op_sel:[0,0,1]
	v_add3_u32 v130, v133, v130, s44
	v_and_or_b32 v135, v130, s42, v135
	v_pk_mul_f32 v[130:131], v[160:161], v[164:165] op_sel_hi:[1,0]
	global_store_dwordx2 v234, v[134:135], s[20:21] offset:3072
	global_store_dword v237, v136, s[18:19] offset:1536
	v_pk_fma_f32 v[130:131], v[130:131], v[114:115], v[122:123]
	v_mov_b32_e32 v136, 0
	v_bfe_u32 v134, v130, 16, 1
	v_bfe_u32 v135, v131, 16, 1
	v_add3_u32 v134, v130, v134, s44
	v_add3_u32 v135, v131, v135, s44
	v_med3_f32 v130, v130, s45, v236
	v_med3_f32 v131, v131, s45, v236
	v_pk_mul_f32 v[132:133], v[158:159], v[164:165] op_sel_hi:[1,0]
	v_cvt_pk_fp8_f32 v136, v130, v131
	v_pk_fma_f32 v[132:133], v[132:133], v[116:117], v[124:125]
	v_lshrrev_b32_e32 v134, 16, v134
	v_and_or_b32 v134, v135, s42, v134
	v_bfe_u32 v135, v132, 16, 1
	v_add3_u32 v135, v132, v135, s44
	v_med3_f32 v131, v132, s45, v236
	v_med3_f32 v132, v133, s45, v236
	v_bfe_u32 v130, v133, 16, 1
	v_cvt_pk_fp8_f32 v136, v131, v132 op_sel:[0,0,1]
	v_lshrrev_b32_e32 v135, 16, v135
	v_add3_u32 v130, v133, v130, s44
	v_and_or_b32 v135, v130, s42, v135
	global_store_dwordx2 v234, v[134:135], s[20:21] offset:3584
	global_store_dword v237, v136, s[18:19] offset:1792
	global_load_dwordx2 v[224:225], v234, s[28:29]
	global_load_dwordx4 v[158:161], v178, s[30:31]
	global_load_dwordx2 v[222:223], v234, s[28:29] offset:512
	global_load_dwordx4 v[154:157], v178, s[30:31] offset:1024
	global_load_dwordx2 v[220:221], v234, s[28:29] offset:1024
	global_load_dwordx4 v[150:153], v178, s[30:31] offset:2048
	global_load_dwordx2 v[218:219], v234, s[28:29] offset:1536
	global_load_dwordx4 v[146:149], v178, s[30:31] offset:3072
	global_load_dwordx2 v[216:217], v234, s[28:29] offset:2048
	v_add_co_u32_e64 v130, s[4:5], s41, v210
	v_mul_f32_e32 v132, 0x4b800000, v214
	s_nop 0
	v_addc_co_u32_e64 v131, s[4:5], 0, v211, s[4:5]
	global_load_dwordx4 v[142:145], v[130:131], off
	global_load_dwordx2 v[212:213], v234, s[28:29] offset:2560
	global_load_dwordx4 v[138:141], v[130:131], off offset:1024
	global_load_dwordx2 v[210:211], v234, s[28:29] offset:3072
	v_cndmask_b32_e32 v132, v214, v132, vcc
	v_rsq_f32_e32 v164, v132
	global_load_dwordx4 v[134:137], v[130:131], off offset:2048
	global_load_dwordx2 v[214:215], v234, s[28:29] offset:3584
	s_nop 0
	global_load_dwordx4 v[130:133], v[130:131], off offset:3072
	v_mov_b32_e32 v192, v195
	s_add_u32 s18, s33, s14
	v_mul_f32_e32 v166, 0x45800000, v164
	v_cndmask_b32_e32 v166, v164, v166, vcc
	v_pk_mul_f32 v[206:207], v[166:167], v[206:207] op_sel_hi:[0,1]
	v_pk_mul_f32 v[208:209], v[166:167], v[208:209] op_sel_hi:[0,1]
	v_pk_fma_f32 v[206:207], v[34:35], v[206:207], v[30:31]
	v_pk_fma_f32 v[208:209], v[36:37], v[208:209], v[32:33]
	v_and_b32_sdwa v31, v206, v235 dst_sel:DWORD dst_unused:UNUSED_PAD src0_sel:WORD_1 src1_sel:DWORD
	v_add3_u32 v32, v206, v31, s44
	v_and_b32_sdwa v31, v209, v235 dst_sel:DWORD dst_unused:UNUSED_PAD src0_sel:WORD_1 src1_sel:DWORD
	v_and_b32_sdwa v33, v207, v235 dst_sel:DWORD dst_unused:UNUSED_PAD src0_sel:WORD_1 src1_sel:DWORD
	v_and_b32_sdwa v30, v208, v235 dst_sel:DWORD dst_unused:UNUSED_PAD src0_sel:WORD_1 src1_sel:DWORD
	v_add3_u32 v31, v209, v31, s44
	v_add3_u32 v33, v207, v33, s44
	v_add3_u32 v30, v208, v30, s44
	v_and_b32_e32 v31, 0xffff0000, v31
	v_and_b32_e32 v33, 0xffff0000, v33
	v_or_b32_sdwa v31, v31, v30 dst_sel:DWORD dst_unused:UNUSED_PAD src0_sel:DWORD src1_sel:WORD_1
	v_or_b32_sdwa v30, v33, v32 dst_sel:DWORD dst_unused:UNUSED_PAD src0_sel:DWORD src1_sel:WORD_1
	global_store_dwordx2 v234, v[30:31], s[26:27] nt
	v_mov_b32_e32 v30, v203
	v_mov_b32_e32 v203, v204
	v_mov_b32_e32 v31, v205
	v_pk_mul_f32 v[32:33], v[166:167], v[202:203] op_sel_hi:[0,1]
	v_pk_mul_f32 v[30:31], v[166:167], v[30:31] op_sel_hi:[0,1]
	v_pk_fma_f32 v[202:203], v[38:39], v[32:33], v[26:27]
	v_pk_fma_f32 v[204:205], v[40:41], v[30:31], v[28:29]
	v_and_b32_sdwa v27, v202, v235 dst_sel:DWORD dst_unused:UNUSED_PAD src0_sel:WORD_1 src1_sel:DWORD
	v_add3_u32 v28, v202, v27, s44
	v_and_b32_sdwa v27, v205, v235 dst_sel:DWORD dst_unused:UNUSED_PAD src0_sel:WORD_1 src1_sel:DWORD
	v_and_b32_sdwa v29, v203, v235 dst_sel:DWORD dst_unused:UNUSED_PAD src0_sel:WORD_1 src1_sel:DWORD
	v_and_b32_sdwa v26, v204, v235 dst_sel:DWORD dst_unused:UNUSED_PAD src0_sel:WORD_1 src1_sel:DWORD
	v_add3_u32 v27, v205, v27, s44
	v_add3_u32 v29, v203, v29, s44
	v_add3_u32 v26, v204, v26, s44
	v_and_b32_e32 v27, 0xffff0000, v27
	v_and_b32_e32 v29, 0xffff0000, v29
	v_or_b32_sdwa v27, v27, v26 dst_sel:DWORD dst_unused:UNUSED_PAD src0_sel:DWORD src1_sel:WORD_1
	v_or_b32_sdwa v26, v29, v28 dst_sel:DWORD dst_unused:UNUSED_PAD src0_sel:DWORD src1_sel:WORD_1
	v_mov_b32_e32 v28, v207
	v_mov_b32_e32 v29, v203
	global_store_dwordx2 v234, v[26:27], s[26:27] offset:512 nt
	v_mov_b32_e32 v26, v206
	v_mov_b32_e32 v27, v202
	v_pk_mul_f32 v[28:29], v[28:29], v[28:29]
	v_mov_b32_e32 v30, v209
	v_pk_fma_f32 v[26:27], v[26:27], v[26:27], v[28:29]
	v_mov_b32_e32 v28, v208
	v_mov_b32_e32 v29, v204
	v_pk_mul_f32 v[28:29], v[28:29], v[28:29]
	v_mov_b32_e32 v31, v205
	v_pk_fma_f32 v[28:29], v[30:31], v[30:31], v[28:29]
	v_pk_mul_f32 v[30:31], v[166:167], v[198:199] op_sel_hi:[0,1]
	v_pk_add_f32 v[26:27], v[26:27], v[28:29]
	v_pk_mul_f32 v[28:29], v[166:167], v[200:201] op_sel_hi:[0,1]
	v_pk_fma_f32 v[198:199], v[46:47], v[30:31], v[22:23]
	v_pk_fma_f32 v[200:201], v[48:49], v[28:29], v[24:25]
	v_and_b32_sdwa v23, v198, v235 dst_sel:DWORD dst_unused:UNUSED_PAD src0_sel:WORD_1 src1_sel:DWORD
	v_add3_u32 v24, v198, v23, s44
	v_and_b32_sdwa v23, v201, v235 dst_sel:DWORD dst_unused:UNUSED_PAD src0_sel:WORD_1 src1_sel:DWORD
	v_and_b32_sdwa v25, v199, v235 dst_sel:DWORD dst_unused:UNUSED_PAD src0_sel:WORD_1 src1_sel:DWORD
	v_and_b32_sdwa v22, v200, v235 dst_sel:DWORD dst_unused:UNUSED_PAD src0_sel:WORD_1 src1_sel:DWORD
	v_add3_u32 v23, v201, v23, s44
	v_add3_u32 v25, v199, v25, s44
	v_add3_u32 v22, v200, v22, s44
	v_and_b32_e32 v23, 0xffff0000, v23
	v_and_b32_e32 v25, 0xffff0000, v25
	v_or_b32_sdwa v23, v23, v22 dst_sel:DWORD dst_unused:UNUSED_PAD src0_sel:DWORD src1_sel:WORD_1
	v_or_b32_sdwa v22, v25, v24 dst_sel:DWORD dst_unused:UNUSED_PAD src0_sel:DWORD src1_sel:WORD_1
	global_store_dwordx2 v234, v[22:23], s[26:27] offset:1024 nt
	v_pk_mul_f32 v[22:23], v[200:201], v[200:201]
	v_pk_mul_f32 v[24:25], v[198:199], v[198:199]
	v_pk_add_f32 v[26:27], v[26:27], v[26:27] op_sel_hi:[0,1]
	v_pk_mov_b32 v[28:29], v[24:25], v[22:23] op_sel:[1,0]
	v_mov_b32_e32 v25, v23
	v_pk_add_f32 v[22:23], v[24:25], v[28:29]
	v_pk_mul_f32 v[28:29], v[192:193], v[166:167] op_sel_hi:[1,0]
	v_pk_mul_f32 v[24:25], v[196:197], v[166:167] op_sel_hi:[1,0]
	v_pk_fma_f32 v[192:193], v[54:55], v[28:29], v[18:19]
	v_pk_fma_f32 v[196:197], v[56:57], v[24:25], v[20:21]
	v_and_b32_sdwa v19, v192, v235 dst_sel:DWORD dst_unused:UNUSED_PAD src0_sel:WORD_1 src1_sel:DWORD
	v_add3_u32 v20, v192, v19, s44
	v_and_b32_sdwa v19, v197, v235 dst_sel:DWORD dst_unused:UNUSED_PAD src0_sel:WORD_1 src1_sel:DWORD
	v_and_b32_sdwa v21, v193, v235 dst_sel:DWORD dst_unused:UNUSED_PAD src0_sel:WORD_1 src1_sel:DWORD
	v_and_b32_sdwa v18, v196, v235 dst_sel:DWORD dst_unused:UNUSED_PAD src0_sel:WORD_1 src1_sel:DWORD
	v_add3_u32 v19, v197, v19, s44
	v_add3_u32 v21, v193, v21, s44
	v_mov_b32_e32 v24, v190
	v_mov_b32_e32 v25, v188
	v_add3_u32 v18, v196, v18, s44
	v_and_b32_e32 v19, 0xffff0000, v19
	v_and_b32_e32 v21, 0xffff0000, v21
	v_pk_mul_f32 v[24:25], v[166:167], v[24:25] op_sel_hi:[0,1]
	v_mov_b32_e32 v188, v191
	v_or_b32_sdwa v19, v19, v18 dst_sel:DWORD dst_unused:UNUSED_PAD src0_sel:DWORD src1_sel:WORD_1
	v_or_b32_sdwa v18, v21, v20 dst_sel:DWORD dst_unused:UNUSED_PAD src0_sel:DWORD src1_sel:WORD_1
	v_pk_mul_f32 v[28:29], v[166:167], v[188:189] op_sel_hi:[0,1]
	v_pk_fma_f32 v[190:191], v[58:59], v[24:25], v[14:15]
	global_store_dwordx2 v234, v[18:19], s[26:27] offset:1536 nt
	v_mul_f32_e32 v18, v192, v192
	v_pk_fma_f32 v[188:189], v[60:61], v[28:29], v[16:17]
	v_and_b32_sdwa v15, v190, v235 dst_sel:DWORD dst_unused:UNUSED_PAD src0_sel:WORD_1 src1_sel:DWORD
	v_pk_fma_f32 v[18:19], v[192:193], v[192:193], v[18:19] op_sel_hi:[1,1,0]
	v_add3_u32 v16, v190, v15, s44
	v_and_b32_sdwa v15, v189, v235 dst_sel:DWORD dst_unused:UNUSED_PAD src0_sel:WORD_1 src1_sel:DWORD
	v_and_b32_sdwa v17, v191, v235 dst_sel:DWORD dst_unused:UNUSED_PAD src0_sel:WORD_1 src1_sel:DWORD
	v_mul_f32_e32 v18, v196, v196
	v_and_b32_sdwa v14, v188, v235 dst_sel:DWORD dst_unused:UNUSED_PAD src0_sel:WORD_1 src1_sel:DWORD
	v_add3_u32 v15, v189, v15, s44
	v_add3_u32 v17, v191, v17, s44
	v_pk_add_f32 v[22:23], v[22:23], v[22:23] op_sel_hi:[0,1]
	v_pk_fma_f32 v[20:21], v[196:197], v[196:197], v[18:19] op_sel_hi:[1,1,0]
	v_add3_u32 v14, v188, v14, s44
	v_and_b32_e32 v15, 0xffff0000, v15
	v_and_b32_e32 v17, 0xffff0000, v17
	v_or_b32_sdwa v15, v15, v14 dst_sel:DWORD dst_unused:UNUSED_PAD src0_sel:DWORD src1_sel:WORD_1
	v_or_b32_sdwa v14, v17, v16 dst_sel:DWORD dst_unused:UNUSED_PAD src0_sel:DWORD src1_sel:WORD_1
	v_mul_f32_e32 v18, v190, v190
	v_mul_f32_e32 v20, v191, v191
	v_mul_f32_e32 v26, v188, v188
	v_mul_f32_e32 v22, v189, v189
	global_store_dwordx2 v234, v[14:15], s[26:27] offset:2048 nt
	v_pk_add_f32 v[14:15], v[18:19], v[20:21]
	v_pk_add_f32 v[16:17], v[22:23], v[26:27]
	v_mov_b32_e32 v164, v167
	v_pk_add_f32 v[14:15], v[14:15], v[16:17]
	v_mov_b32_e32 v16, v185
	v_mov_b32_e32 v185, v186
	v_mov_b32_e32 v17, v187
	v_pk_mul_f32 v[18:19], v[166:167], v[184:185] op_sel_hi:[0,1]
	v_pk_mul_f32 v[16:17], v[166:167], v[16:17] op_sel_hi:[0,1]
	v_pk_fma_f32 v[184:185], v[66:67], v[18:19], v[10:11]
	v_pk_fma_f32 v[186:187], v[68:69], v[16:17], v[12:13]
	v_and_b32_sdwa v11, v184, v235 dst_sel:DWORD dst_unused:UNUSED_PAD src0_sel:WORD_1 src1_sel:DWORD
	v_add3_u32 v12, v184, v11, s44
	v_and_b32_sdwa v11, v187, v235 dst_sel:DWORD dst_unused:UNUSED_PAD src0_sel:WORD_1 src1_sel:DWORD
	v_and_b32_sdwa v13, v185, v235 dst_sel:DWORD dst_unused:UNUSED_PAD src0_sel:WORD_1 src1_sel:DWORD
	v_and_b32_sdwa v10, v186, v235 dst_sel:DWORD dst_unused:UNUSED_PAD src0_sel:WORD_1 src1_sel:DWORD
	v_add3_u32 v11, v187, v11, s44
	v_add3_u32 v13, v185, v13, s44
	v_add3_u32 v10, v186, v10, s44
	v_and_b32_e32 v11, 0xffff0000, v11
	v_and_b32_e32 v13, 0xffff0000, v13
	v_or_b32_sdwa v11, v11, v10 dst_sel:DWORD dst_unused:UNUSED_PAD src0_sel:DWORD src1_sel:WORD_1
	v_or_b32_sdwa v10, v13, v12 dst_sel:DWORD dst_unused:UNUSED_PAD src0_sel:DWORD src1_sel:WORD_1
	global_store_dwordx2 v234, v[10:11], s[26:27] offset:2560 nt
	v_pk_mul_f32 v[10:11], v[186:187], v[186:187]
	v_pk_mul_f32 v[12:13], v[184:185], v[184:185]
	v_pk_add_f32 v[14:15], v[14:15], v[14:15] op_sel_hi:[0,1]
	v_pk_mov_b32 v[16:17], v[12:13], v[10:11] op_sel:[1,0]
	v_mov_b32_e32 v13, v11
	v_pk_add_f32 v[10:11], v[12:13], v[16:17]
	v_pk_mul_f32 v[12:13], v[166:167], v[182:183] op_sel_hi:[0,1]
	v_pk_mul_f32 v[16:17], v[166:167], v[168:169] op_sel_hi:[0,1]
	v_pk_fma_f32 v[168:169], v[64:65], v[12:13], v[8:9]
	v_pk_fma_f32 v[30:31], v[62:63], v[16:17], v[6:7]
	v_and_b32_sdwa v6, v168, v235 dst_sel:DWORD dst_unused:UNUSED_PAD src0_sel:WORD_1 src1_sel:DWORD
	v_and_b32_sdwa v7, v30, v235 dst_sel:DWORD dst_unused:UNUSED_PAD src0_sel:WORD_1 src1_sel:DWORD
	v_add3_u32 v241, v168, v6, s44
	v_mul_f32_e32 v6, v30, v30
	v_add3_u32 v240, v30, v7, s44
	v_pk_fma_f32 v[6:7], v[30:31], v[30:31], v[6:7] op_sel_hi:[1,1,0]
	v_pk_mul_f32 v[12:13], v[164:165], v[166:167] op_sel_hi:[1,0]
	v_mul_f32_e32 v6, v168, v168
	v_pk_mul_f32 v[16:17], v[162:163], v[166:167] op_sel_hi:[1,0]
	v_pk_add_f32 v[10:11], v[10:11], v[10:11] op_sel_hi:[0,1]
	v_pk_fma_f32 v[8:9], v[168:169], v[168:169], v[6:7] op_sel_hi:[1,1,0]
	s_waitcnt vmcnt(46)
	v_pk_fma_f32 v[162:163], v[52:53], v[16:17], v[4:5]
	v_pk_fma_f32 v[164:165], v[50:51], v[12:13], v[2:3]
	v_mul_f32_e32 v14, v162, v162
	v_mul_f32_e32 v6, v164, v164
	v_mul_f32_e32 v8, v165, v165
	v_mul_f32_e32 v10, v163, v163
	v_pk_add_f32 v[2:3], v[6:7], v[8:9]
	v_pk_add_f32 v[4:5], v[10:11], v[14:15]
	s_waitcnt vmcnt(21)
	v_and_b32_e32 v183, 0xffff0000, v224
	v_and_b32_e32 v195, 0xffff0000, v225
	v_pk_add_f32 v[238:239], v[2:3], v[4:5]
	v_lshlrev_b32_e32 v182, 16, v224
	v_lshlrev_b32_e32 v194, 16, v225
	v_mul_f32_e32 v2, v195, v195
	s_waitcnt vmcnt(19)
	v_and_b32_e32 v167, 0xffff0000, v223
	v_and_b32_e32 v166, 0xffff0000, v222
	v_mul_f32_e32 v6, v183, v183
	v_pk_fma_f32 v[2:3], v[194:195], v[194:195], v[2:3] op_sel_hi:[1,1,0]
	v_lshlrev_b32_e32 v33, 16, v223
	v_lshlrev_b32_e32 v32, 16, v222
	v_pk_mul_f32 v[4:5], v[166:167], v[166:167]
	s_waitcnt vmcnt(15)
	v_lshlrev_b32_e32 v19, 16, v218
	v_pk_fma_f32 v[6:7], v[182:183], v[182:183], v[6:7] op_sel_hi:[1,1,0]
	v_pk_fma_f32 v[4:5], v[32:33], v[32:33], v[4:5]
	v_and_b32_e32 v17, 0xffff0000, v218
	v_mov_b32_e32 v18, v6
	v_mov_b32_e32 v8, v2
	v_mov_b32_e32 v9, v19
	v_mul_f32_e32 v10, v17, v17
	v_pk_add_f32 v[2:3], v[6:7], v[2:3]
	v_pk_mul_f32 v[6:7], v[18:19], v[8:9]
	v_pk_add_f32 v[4:5], v[4:5], v[4:5] op_sel:[0,1] op_sel_hi:[1,0]
	v_and_b32_e32 v27, 0xffff0000, v220
	v_and_b32_e32 v29, 0xffff0000, v221
	v_mov_b32_e32 v3, v7
	v_mov_b32_e32 v5, v10
	v_lshlrev_b32_e32 v26, 16, v220
	v_lshlrev_b32_e32 v28, 16, v221
	v_lshlrev_b32_e32 v20, 16, v219
	v_and_b32_e32 v21, 0xffff0000, v219
	v_pk_add_f32 v[2:3], v[2:3], v[4:5]
	v_mul_f32_e32 v4, v27, v27
	v_mul_f32_e32 v6, v29, v29
	v_mul_f32_e32 v11, v20, v20
	v_mul_f32_e32 v12, v21, v21
	v_pk_fma_f32 v[4:5], v[26:27], v[26:27], v[4:5] op_sel_hi:[1,1,0]
	v_pk_fma_f32 v[6:7], v[28:29], v[28:29], v[6:7] op_sel_hi:[1,1,0]
	v_mov_b32_e32 v5, v11
	v_mov_b32_e32 v7, v12
	v_pk_add_f32 v[4:5], v[4:5], v[6:7]
	s_waitcnt vmcnt(13)
	v_and_b32_e32 v25, 0xffff0000, v217
	v_and_b32_e32 v24, 0xffff0000, v216
	v_pk_add_f32 v[218:219], v[2:3], v[4:5]
	v_lshlrev_b32_e32 v23, 16, v217
	v_lshlrev_b32_e32 v22, 16, v216
	v_pk_mul_f32 v[2:3], v[24:25], v[24:25]
	s_waitcnt vmcnt(11)
	v_and_b32_e32 v15, 0xffff0000, v213
	v_pk_fma_f32 v[2:3], v[22:23], v[22:23], v[2:3]
	v_and_b32_e32 v14, 0xffff0000, v212
	v_pk_add_f32 v[216:217], v[2:3], v[2:3] op_sel:[0,1] op_sel_hi:[1,0]
	v_lshlrev_b32_e32 v13, 16, v213
	v_lshlrev_b32_e32 v12, 16, v212
	v_pk_mul_f32 v[2:3], v[14:15], v[14:15]
	s_waitcnt vmcnt(9)
	v_lshlrev_b32_e32 v8, 16, v210
	v_and_b32_e32 v9, 0xffff0000, v210
	v_lshlrev_b32_e32 v10, 16, v211
	v_and_b32_e32 v11, 0xffff0000, v211
	s_waitcnt vmcnt(7)
	v_lshlrev_b32_e32 v7, 16, v214
	v_pk_add_f32 v[210:211], v[218:219], v[218:219] op_sel:[0,1] op_sel_hi:[1,0]
	v_pk_fma_f32 v[212:213], v[12:13], v[12:13], v[2:3]
	v_and_b32_e32 v5, 0xffff0000, v214
	v_lshlrev_b32_e32 v2, 16, v215
	v_and_b32_e32 v3, 0xffff0000, v215
	v_mov_b32_e32 v6, v210
	v_mov_b32_e32 v214, v216
	v_mov_b32_e32 v215, v7
	v_mul_f32_e32 v4, v5, v5
	v_pk_add_f32 v[210:211], v[210:211], v[216:217]
	v_pk_mul_f32 v[214:215], v[6:7], v[214:215]
	v_pk_add_f32 v[212:213], v[212:213], v[212:213] op_sel:[0,1] op_sel_hi:[1,0]
	v_mov_b32_e32 v211, v215
	v_mov_b32_e32 v213, v4
	v_mul_f32_e32 v4, v9, v9
	v_pk_add_f32 v[210:211], v[210:211], v[212:213]
	v_pk_fma_f32 v[212:213], v[8:9], v[8:9], v[4:5] op_sel_hi:[1,1,0]
	v_mul_f32_e32 v4, v11, v11
	v_mul_f32_e32 v16, v2, v2
	v_mul_f32_e32 v18, v3, v3
	v_pk_fma_f32 v[214:215], v[10:11], v[10:11], v[4:5] op_sel_hi:[1,1,0]
	v_mov_b32_e32 v213, v16
	v_mov_b32_e32 v215, v18
	v_pk_add_f32 v[212:213], v[212:213], v[214:215]
	v_and_b32_sdwa v242, v169, v235 dst_sel:DWORD dst_unused:UNUSED_PAD src0_sel:WORD_1 src1_sel:DWORD
	v_pk_add_f32 v[210:211], v[210:211], v[212:213]
	v_mov_b32_e32 v213, v238
	v_mov_b32_e32 v212, v210
	v_mov_b32_e32 v238, v211
	v_pk_add_f32 v[210:211], v[212:213], v[238:239]
	ds_bpermute_b32 v213, v171, v211
	ds_bpermute_b32 v212, v171, v210
	v_and_b32_sdwa v243, v31, v235 dst_sel:DWORD dst_unused:UNUSED_PAD src0_sel:WORD_1 src1_sel:DWORD
	v_add3_u32 v4, v169, v242, s44
	v_add3_u32 v6, v31, v243, s44
	v_and_b32_e32 v4, 0xffff0000, v4
	s_waitcnt lgkmcnt(0)
	v_pk_add_f32 v[210:211], v[210:211], v[212:213]
	ds_bpermute_b32 v213, v226, v211
	ds_bpermute_b32 v212, v226, v210
	v_and_b32_sdwa v16, v163, v235 dst_sel:DWORD dst_unused:UNUSED_PAD src0_sel:WORD_1 src1_sel:DWORD
	v_and_b32_e32 v6, 0xffff0000, v6
	v_or_b32_sdwa v215, v4, v241 dst_sel:DWORD dst_unused:UNUSED_PAD src0_sel:DWORD src1_sel:WORD_1
	v_and_b32_sdwa v4, v162, v235 dst_sel:DWORD dst_unused:UNUSED_PAD src0_sel:WORD_1 src1_sel:DWORD
	s_waitcnt lgkmcnt(0)
	v_pk_add_f32 v[210:211], v[210:211], v[212:213]
	ds_bpermute_b32 v213, v228, v211
	ds_bpermute_b32 v212, v228, v210
	v_add3_u32 v16, v163, v16, s44
	v_or_b32_sdwa v214, v6, v240 dst_sel:DWORD dst_unused:UNUSED_PAD src0_sel:DWORD src1_sel:WORD_1
	v_add3_u32 v4, v162, v4, s44
	v_and_b32_e32 v16, 0xffff0000, v16
	s_waitcnt lgkmcnt(0)
	v_pk_add_f32 v[210:211], v[210:211], v[212:213]
	ds_bpermute_b32 v213, v229, v211
	ds_bpermute_b32 v212, v229, v210
	global_store_dwordx2 v234, v[214:215], s[26:27] offset:3072 nt
	v_or_b32_sdwa v215, v16, v4 dst_sel:DWORD dst_unused:UNUSED_PAD src0_sel:DWORD src1_sel:WORD_1
	v_and_b32_sdwa v18, v165, v235 dst_sel:DWORD dst_unused:UNUSED_PAD src0_sel:WORD_1 src1_sel:DWORD
	v_and_b32_sdwa v6, v164, v235 dst_sel:DWORD dst_unused:UNUSED_PAD src0_sel:WORD_1 src1_sel:DWORD
	s_waitcnt lgkmcnt(0)
	v_pk_add_f32 v[210:211], v[210:211], v[212:213]
	ds_bpermute_b32 v213, v230, v211
	ds_bpermute_b32 v212, v230, v210
	v_add3_u32 v18, v165, v18, s44
	v_add3_u32 v6, v164, v6, s44
	v_and_b32_e32 v18, 0xffff0000, v18
	v_or_b32_sdwa v214, v18, v6 dst_sel:DWORD dst_unused:UNUSED_PAD src0_sel:DWORD src1_sel:WORD_1
	s_waitcnt lgkmcnt(0)
	v_pk_add_f32 v[210:211], v[210:211], v[212:213]
	ds_bpermute_b32 v213, v231, v211
	ds_bpermute_b32 v212, v231, v210
	global_store_dwordx2 v234, v[214:215], s[26:27] offset:3584 nt
	s_addc_u32 s19, s34, s15
	s_add_u32 s14, s35, s24
	s_addc_u32 s15, s36, s25
	s_waitcnt lgkmcnt(0)
	v_pk_add_f32 v[210:211], v[210:211], v[212:213]
	s_nop 0
	v_pk_fma_f32 v[180:181], v[210:211], s[10:11], v[180:181] op_sel_hi:[1,0,0]
	s_nop 0
	v_mul_f32_e32 v4, 0x4b800000, v181
	v_cmp_gt_f32_e64 s[4:5], s43, v181
	v_cmp_gt_f32_e32 vcc, s43, v180
	s_nop 0
	v_cndmask_b32_e64 v4, v181, v4, s[4:5]
	v_rsq_f32_e32 v4, v4
	v_mov_b32_e32 v181, 0
	v_mul_f32_e32 v6, 0x45800000, v4
	v_cndmask_b32_e64 v4, v4, v6, s[4:5]
	v_pk_mul_f32 v[206:207], v[206:207], v[4:5] op_sel_hi:[1,0]
	v_pk_mul_f32 v[208:209], v[208:209], v[4:5] op_sel_hi:[1,0]
	v_pk_fma_f32 v[206:207], v[42:43], v[206:207], v[126:127]
	v_pk_fma_f32 v[208:209], v[44:45], v[208:209], v[128:129]
	v_bfe_u32 v6, v206, 16, 1
	v_add3_u32 v6, v206, v6, s44
	v_bfe_u32 v16, v207, 16, 1
	v_lshrrev_b32_e32 v6, 16, v6
	v_add3_u32 v16, v207, v16, s44
	v_and_or_b32 v210, v16, s42, v6
	v_med3_f32 v16, v206, s45, v236
	v_med3_f32 v18, v207, s45, v236
	v_cvt_pk_fp8_f32 v181, v16, v18
	v_bfe_u32 v6, v208, 16, 1
	v_add3_u32 v6, v208, v6, s44
	v_bfe_u32 v16, v209, 16, 1
	v_pk_mul_f32 v[202:203], v[202:203], v[4:5] op_sel_hi:[1,0]
	v_lshrrev_b32_e32 v6, 16, v6
	v_med3_f32 v18, v208, s45, v236
	v_med3_f32 v206, v209, s45, v236
	v_add3_u32 v16, v209, v16, s44
	v_pk_fma_f32 v[202:203], v[106:107], v[202:203], v[110:111]
	v_cvt_pk_fp8_f32 v181, v18, v206 op_sel:[0,0,1]
	v_and_or_b32 v211, v16, s42, v6
	v_bfe_u32 v6, v202, 16, 1
	v_add3_u32 v6, v202, v6, s44
	v_bfe_u32 v16, v203, 16, 1
	v_lshrrev_b32_e32 v6, 16, v6
	v_add3_u32 v16, v203, v16, s44
	global_store_dwordx2 v234, v[210:211], s[16:17]
	global_store_dword v237, v181, s[18:19]
	v_pk_mul_f32 v[204:205], v[204:205], v[4:5] op_sel_hi:[1,0]
	v_and_or_b32 v206, v16, s42, v6
	v_med3_f32 v16, v202, s45, v236
	v_med3_f32 v18, v203, s45, v236
	v_mov_b32_e32 v181, 0
	v_pk_fma_f32 v[204:205], v[108:109], v[204:205], v[112:113]
	v_cvt_pk_fp8_f32 v181, v16, v18
	v_bfe_u32 v6, v204, 16, 1
	v_add3_u32 v6, v204, v6, s44
	v_bfe_u32 v16, v205, 16, 1
	v_pk_mul_f32 v[198:199], v[198:199], v[4:5] op_sel_hi:[1,0]
	v_lshrrev_b32_e32 v6, 16, v6
	v_med3_f32 v18, v204, s45, v236
	v_med3_f32 v202, v205, s45, v236
	v_add3_u32 v16, v205, v16, s44
	v_pk_fma_f32 v[198:199], v[86:87], v[198:199], v[102:103]
	v_cvt_pk_fp8_f32 v181, v18, v202 op_sel:[0,0,1]
	v_and_or_b32 v207, v16, s42, v6
	v_bfe_u32 v6, v198, 16, 1
	v_add3_u32 v6, v198, v6, s44
	v_bfe_u32 v16, v199, 16, 1
	v_lshrrev_b32_e32 v6, 16, v6
	v_add3_u32 v16, v199, v16, s44
	global_store_dwordx2 v234, v[206:207], s[16:17] offset:512
	global_store_dword v237, v181, s[18:19] offset:256
	v_pk_mul_f32 v[200:201], v[200:201], v[4:5] op_sel_hi:[1,0]
	v_and_or_b32 v202, v16, s42, v6
	v_med3_f32 v16, v198, s45, v236
	v_med3_f32 v18, v199, s45, v236
	v_mov_b32_e32 v181, 0
	v_pk_fma_f32 v[200:201], v[88:89], v[200:201], v[104:105]
	v_cvt_pk_fp8_f32 v181, v16, v18
	v_bfe_u32 v6, v200, 16, 1
	v_add3_u32 v6, v200, v6, s44
	v_bfe_u32 v16, v201, 16, 1
	v_pk_mul_f32 v[192:193], v[192:193], v[4:5] op_sel_hi:[1,0]
	v_lshrrev_b32_e32 v6, 16, v6
	v_med3_f32 v18, v200, s45, v236
	v_med3_f32 v198, v201, s45, v236
	v_add3_u32 v16, v201, v16, s44
	v_pk_fma_f32 v[192:193], v[78:79], v[192:193], v[82:83]
	v_cvt_pk_fp8_f32 v181, v18, v198 op_sel:[0,0,1]
	v_and_or_b32 v203, v16, s42, v6
	v_bfe_u32 v6, v192, 16, 1
	v_add3_u32 v6, v192, v6, s44
	v_bfe_u32 v16, v193, 16, 1
	v_lshrrev_b32_e32 v6, 16, v6
	v_add3_u32 v16, v193, v16, s44
	global_store_dwordx2 v234, v[202:203], s[16:17] offset:1024
	global_store_dword v237, v181, s[18:19] offset:512
	v_pk_mul_f32 v[196:197], v[196:197], v[4:5] op_sel_hi:[1,0]
	v_and_or_b32 v198, v16, s42, v6
	v_med3_f32 v16, v192, s45, v236
	v_med3_f32 v18, v193, s45, v236
	v_mov_b32_e32 v181, 0
	v_pk_fma_f32 v[196:197], v[80:81], v[196:197], v[84:85]
	v_cvt_pk_fp8_f32 v181, v16, v18
	v_bfe_u32 v6, v196, 16, 1
	v_add3_u32 v6, v196, v6, s44
	v_bfe_u32 v16, v197, 16, 1
	v_pk_mul_f32 v[190:191], v[190:191], v[4:5] op_sel_hi:[1,0]
	v_lshrrev_b32_e32 v6, 16, v6
	v_med3_f32 v18, v196, s45, v236
	v_med3_f32 v192, v197, s45, v236
	v_add3_u32 v16, v197, v16, s44
	v_pk_fma_f32 v[190:191], v[70:71], v[190:191], v[74:75]
	v_cvt_pk_fp8_f32 v181, v18, v192 op_sel:[0,0,1]
	v_and_or_b32 v199, v16, s42, v6
	v_bfe_u32 v6, v190, 16, 1
	v_add3_u32 v6, v190, v6, s44
	v_bfe_u32 v16, v191, 16, 1
	v_lshrrev_b32_e32 v6, 16, v6
	v_add3_u32 v16, v191, v16, s44
	global_store_dwordx2 v234, v[198:199], s[16:17] offset:1536
	global_store_dword v237, v181, s[18:19] offset:768
	v_pk_mul_f32 v[188:189], v[188:189], v[4:5] op_sel_hi:[1,0]
	v_and_or_b32 v192, v16, s42, v6
	v_med3_f32 v16, v190, s45, v236
	v_med3_f32 v18, v191, s45, v236
	v_mov_b32_e32 v181, 0
	v_pk_fma_f32 v[188:189], v[72:73], v[188:189], v[76:77]
	v_cvt_pk_fp8_f32 v181, v16, v18
	v_bfe_u32 v6, v188, 16, 1
	v_add3_u32 v6, v188, v6, s44
	v_bfe_u32 v16, v189, 16, 1
	v_pk_mul_f32 v[184:185], v[184:185], v[4:5] op_sel_hi:[1,0]
	v_lshrrev_b32_e32 v6, 16, v6
	v_med3_f32 v18, v188, s45, v236
	v_med3_f32 v188, v189, s45, v236
	v_add3_u32 v16, v189, v16, s44
	v_pk_fma_f32 v[184:185], v[90:91], v[184:185], v[98:99]
	v_cvt_pk_fp8_f32 v181, v18, v188 op_sel:[0,0,1]
	v_and_or_b32 v193, v16, s42, v6
	v_bfe_u32 v6, v184, 16, 1
	v_pk_mul_f32 v[186:187], v[186:187], v[4:5] op_sel_hi:[1,0]
	v_add3_u32 v6, v184, v6, s44
	v_bfe_u32 v16, v185, 16, 1
	v_pk_fma_f32 v[186:187], v[92:93], v[186:187], v[100:101]
	v_lshrrev_b32_e32 v6, 16, v6
	v_add3_u32 v16, v185, v16, s44
	global_store_dwordx2 v234, v[192:193], s[16:17] offset:2048
	global_store_dword v237, v181, s[18:19] offset:1024
	v_and_or_b32 v188, v16, s42, v6
	v_bfe_u32 v6, v186, 16, 1
	v_med3_f32 v16, v184, s45, v236
	v_med3_f32 v18, v185, s45, v236
	v_mov_b32_e32 v181, 0
	v_add3_u32 v6, v186, v6, s44
	v_cvt_pk_fp8_f32 v181, v16, v18
	v_bfe_u32 v16, v187, 16, 1
	v_pk_mul_f32 v[30:31], v[30:31], v[4:5] op_sel_hi:[1,0]
	v_lshrrev_b32_e32 v6, 16, v6
	v_add3_u32 v16, v187, v16, s44
	v_pk_fma_f32 v[30:31], v[94:95], v[30:31], v[118:119]
	v_and_or_b32 v189, v16, s42, v6
	v_bfe_u32 v6, v30, 16, 1
	v_add3_u32 v6, v30, v6, s44
	v_bfe_u32 v16, v31, 16, 1
	v_med3_f32 v18, v186, s45, v236
	v_med3_f32 v184, v187, s45, v236
	v_lshrrev_b32_e32 v6, 16, v6
	v_add3_u32 v16, v31, v16, s44
	v_cvt_pk_fp8_f32 v181, v18, v184 op_sel:[0,0,1]
	v_and_or_b32 v184, v16, s42, v6
	v_med3_f32 v16, v30, s45, v236
	v_med3_f32 v18, v31, s45, v236
	v_mov_b32_e32 v30, 0
	v_cvt_pk_fp8_f32 v30, v16, v18
	v_pk_mul_f32 v[168:169], v[168:169], v[4:5] op_sel_hi:[1,0]
	global_store_dwordx2 v234, v[188:189], s[16:17] offset:2560
	global_store_dword v237, v181, s[18:19] offset:1280
	v_pk_fma_f32 v[168:169], v[96:97], v[168:169], v[120:121]
	v_pk_mul_f32 v[162:163], v[162:163], v[4:5] op_sel_hi:[1,0]
	v_bfe_u32 v6, v168, 16, 1
	v_med3_f32 v18, v168, s45, v236
	v_med3_f32 v31, v169, s45, v236
	v_add3_u32 v6, v168, v6, s44
	v_bfe_u32 v16, v169, 16, 1
	v_cvt_pk_fp8_f32 v30, v18, v31 op_sel:[0,0,1]
	v_lshrrev_b32_e32 v6, 16, v6
	v_add3_u32 v16, v169, v16, s44
	v_and_or_b32 v185, v16, s42, v6
	global_store_dwordx2 v234, v[184:185], s[16:17] offset:3072
	global_store_dword v237, v30, s[18:19] offset:1536
	v_pk_mul_f32 v[30:31], v[164:165], v[4:5] op_sel_hi:[1,0]
	v_pk_fma_f32 v[162:163], v[116:117], v[162:163], v[124:125]
	v_pk_fma_f32 v[30:31], v[114:115], v[30:31], v[122:123]
	s_nop 0
	v_bfe_u32 v4, v30, 16, 1
	v_add3_u32 v4, v30, v4, s44
	v_med3_f32 v16, v30, s45, v236
	v_med3_f32 v18, v31, s45, v236
	v_mov_b32_e32 v30, 0
	v_cvt_pk_fp8_f32 v30, v16, v18
	v_med3_f32 v16, v162, s45, v236
	v_med3_f32 v18, v163, s45, v236
	v_bfe_u32 v6, v31, 16, 1
	v_cvt_pk_fp8_f32 v30, v16, v18 op_sel:[0,0,1]
	v_mul_f32_e32 v16, 0x4b800000, v180
	v_cndmask_b32_e32 v16, v180, v16, vcc
	v_lshrrev_b32_e32 v4, 16, v4
	v_add3_u32 v6, v31, v6, s44
	v_rsq_f32_e32 v16, v16
	v_and_or_b32 v164, v6, s42, v4
	v_bfe_u32 v4, v162, 16, 1
	v_add3_u32 v4, v162, v4, s44
	v_bfe_u32 v6, v163, 16, 1
	v_lshrrev_b32_e32 v4, 16, v4
	v_add3_u32 v6, v163, v6, s44
	v_and_or_b32 v165, v6, s42, v4
	v_mul_f32_e32 v4, 0x45800000, v16
	v_cndmask_b32_e32 v6, v16, v4, vcc
	global_store_dwordx2 v234, v[164:165], s[16:17] offset:3584
	global_store_dword v237, v30, s[18:19] offset:1792
	v_pk_mul_f32 v[30:31], v[6:7], v[194:195] op_sel_hi:[0,1]
	v_pk_mul_f32 v[162:163], v[6:7], v[182:183] op_sel_hi:[0,1]
	v_pk_fma_f32 v[158:159], v[34:35], v[162:163], v[158:159]
	v_pk_fma_f32 v[36:37], v[36:37], v[30:31], v[160:161]
	v_and_b32_sdwa v30, v159, v235 dst_sel:DWORD dst_unused:UNUSED_PAD src0_sel:WORD_1 src1_sel:DWORD
	v_and_b32_sdwa v18, v37, v235 dst_sel:DWORD dst_unused:UNUSED_PAD src0_sel:WORD_1 src1_sel:DWORD
	v_and_b32_sdwa v4, v36, v235 dst_sel:DWORD dst_unused:UNUSED_PAD src0_sel:WORD_1 src1_sel:DWORD
	v_and_b32_sdwa v16, v158, v235 dst_sel:DWORD dst_unused:UNUSED_PAD src0_sel:WORD_1 src1_sel:DWORD
	v_add3_u32 v18, v37, v18, s44
	v_add3_u32 v30, v159, v30, s44
	v_add3_u32 v16, v158, v16, s44
	v_add3_u32 v4, v36, v4, s44
	v_and_b32_e32 v18, 0xffff0000, v18
	v_and_b32_e32 v30, 0xffff0000, v30
	v_or_b32_sdwa v31, v18, v4 dst_sel:DWORD dst_unused:UNUSED_PAD src0_sel:DWORD src1_sel:WORD_1
	v_or_b32_sdwa v30, v30, v16 dst_sel:DWORD dst_unused:UNUSED_PAD src0_sel:DWORD src1_sel:WORD_1
	global_store_dwordx2 v234, v[30:31], s[14:15] nt
	v_mov_b32_e32 v30, v33
	v_mov_b32_e32 v31, v167
	v_mov_b32_e32 v33, v166
	v_pk_mul_f32 v[30:31], v[6:7], v[30:31] op_sel_hi:[0,1]
	v_pk_mul_f32 v[32:33], v[6:7], v[32:33] op_sel_hi:[0,1]
	v_pk_fma_f32 v[32:33], v[38:39], v[32:33], v[154:155]
	v_pk_fma_f32 v[34:35], v[40:41], v[30:31], v[156:157]
	v_and_b32_sdwa v30, v33, v235 dst_sel:DWORD dst_unused:UNUSED_PAD src0_sel:WORD_1 src1_sel:DWORD
	v_and_b32_sdwa v18, v35, v235 dst_sel:DWORD dst_unused:UNUSED_PAD src0_sel:WORD_1 src1_sel:DWORD
	v_and_b32_sdwa v4, v34, v235 dst_sel:DWORD dst_unused:UNUSED_PAD src0_sel:WORD_1 src1_sel:DWORD
	v_and_b32_sdwa v16, v32, v235 dst_sel:DWORD dst_unused:UNUSED_PAD src0_sel:WORD_1 src1_sel:DWORD
	v_add3_u32 v18, v35, v18, s44
	v_add3_u32 v30, v33, v30, s44
	v_add3_u32 v16, v32, v16, s44
	v_add3_u32 v4, v34, v4, s44
	v_and_b32_e32 v18, 0xffff0000, v18
	v_and_b32_e32 v30, 0xffff0000, v30
	v_or_b32_sdwa v31, v18, v4 dst_sel:DWORD dst_unused:UNUSED_PAD src0_sel:DWORD src1_sel:WORD_1
	v_or_b32_sdwa v30, v30, v16 dst_sel:DWORD dst_unused:UNUSED_PAD src0_sel:DWORD src1_sel:WORD_1
	v_mov_b32_e32 v38, v159
	v_mov_b32_e32 v39, v33
	global_store_dwordx2 v234, v[30:31], s[14:15] offset:512 nt
	v_mov_b32_e32 v30, v158
	v_mov_b32_e32 v31, v32
	v_pk_mul_f32 v[38:39], v[38:39], v[38:39]
	v_mov_b32_e32 v40, v37
	v_pk_fma_f32 v[30:31], v[30:31], v[30:31], v[38:39]
	v_mov_b32_e32 v38, v36
	v_mov_b32_e32 v39, v34
	v_pk_mul_f32 v[38:39], v[38:39], v[38:39]
	v_mov_b32_e32 v41, v35
	v_pk_fma_f32 v[38:39], v[40:41], v[40:41], v[38:39]
	v_pk_mul_f32 v[26:27], v[6:7], v[26:27] op_sel_hi:[0,1]
	v_pk_add_f32 v[30:31], v[30:31], v[38:39]
	v_pk_mul_f32 v[8:9], v[6:7], v[8:9] op_sel_hi:[0,1]
	v_pk_add_f32 v[38:39], v[30:31], v[30:31] op_sel_hi:[0,1]
	v_pk_mul_f32 v[30:31], v[6:7], v[28:29] op_sel_hi:[0,1]
	v_pk_fma_f32 v[28:29], v[46:47], v[26:27], v[150:151]
	v_pk_fma_f32 v[30:31], v[48:49], v[30:31], v[152:153]
	v_and_b32_sdwa v26, v29, v235 dst_sel:DWORD dst_unused:UNUSED_PAD src0_sel:WORD_1 src1_sel:DWORD
	v_and_b32_sdwa v18, v31, v235 dst_sel:DWORD dst_unused:UNUSED_PAD src0_sel:WORD_1 src1_sel:DWORD
	v_and_b32_sdwa v4, v30, v235 dst_sel:DWORD dst_unused:UNUSED_PAD src0_sel:WORD_1 src1_sel:DWORD
	v_and_b32_sdwa v16, v28, v235 dst_sel:DWORD dst_unused:UNUSED_PAD src0_sel:WORD_1 src1_sel:DWORD
	v_add3_u32 v18, v31, v18, s44
	v_add3_u32 v26, v29, v26, s44
	v_add3_u32 v16, v28, v16, s44
	v_add3_u32 v4, v30, v4, s44
	v_and_b32_e32 v18, 0xffff0000, v18
	v_and_b32_e32 v26, 0xffff0000, v26
	v_or_b32_sdwa v27, v18, v4 dst_sel:DWORD dst_unused:UNUSED_PAD src0_sel:DWORD src1_sel:WORD_1
	v_or_b32_sdwa v26, v26, v16 dst_sel:DWORD dst_unused:UNUSED_PAD src0_sel:DWORD src1_sel:WORD_1
	global_store_dwordx2 v234, v[26:27], s[14:15] offset:1024 nt
	v_pk_mul_f32 v[26:27], v[30:31], v[30:31]
	v_pk_mul_f32 v[40:41], v[28:29], v[28:29]
	v_mov_b32_e32 v16, v19
	v_pk_mov_b32 v[46:47], v[40:41], v[26:27] op_sel:[1,0]
	v_mov_b32_e32 v41, v27
	v_pk_add_f32 v[26:27], v[40:41], v[46:47]
	v_pk_mul_f32 v[16:17], v[16:17], v[6:7] op_sel_hi:[1,0]
	v_pk_add_f32 v[40:41], v[26:27], v[26:27] op_sel_hi:[0,1]
	v_pk_mul_f32 v[26:27], v[20:21], v[6:7] op_sel_hi:[1,0]
	v_pk_fma_f32 v[20:21], v[54:55], v[16:17], v[146:147]
	v_pk_fma_f32 v[26:27], v[56:57], v[26:27], v[148:149]
	v_and_b32_sdwa v18, v21, v235 dst_sel:DWORD dst_unused:UNUSED_PAD src0_sel:WORD_1 src1_sel:DWORD
	v_and_b32_sdwa v17, v27, v235 dst_sel:DWORD dst_unused:UNUSED_PAD src0_sel:WORD_1 src1_sel:DWORD
	v_and_b32_sdwa v4, v26, v235 dst_sel:DWORD dst_unused:UNUSED_PAD src0_sel:WORD_1 src1_sel:DWORD
	v_and_b32_sdwa v16, v20, v235 dst_sel:DWORD dst_unused:UNUSED_PAD src0_sel:WORD_1 src1_sel:DWORD
	v_add3_u32 v17, v27, v17, s44
	v_add3_u32 v18, v21, v18, s44
	v_add3_u32 v16, v20, v16, s44
	v_add3_u32 v4, v26, v4, s44
	v_and_b32_e32 v17, 0xffff0000, v17
	v_and_b32_e32 v18, 0xffff0000, v18
	v_or_b32_sdwa v17, v17, v4 dst_sel:DWORD dst_unused:UNUSED_PAD src0_sel:DWORD src1_sel:WORD_1
	v_or_b32_sdwa v16, v18, v16 dst_sel:DWORD dst_unused:UNUSED_PAD src0_sel:DWORD src1_sel:WORD_1
	global_store_dwordx2 v234, v[16:17], s[14:15] offset:1536 nt
	v_mov_b32_e32 v16, v22
	v_mov_b32_e32 v17, v24
	v_mov_b32_e32 v24, v23
	v_pk_mul_f32 v[18:19], v[6:7], v[16:17] op_sel_hi:[0,1]
	v_pk_mul_f32 v[16:17], v[6:7], v[24:25] op_sel_hi:[0,1]
	v_mul_f32_e32 v4, v20, v20
	v_pk_fma_f32 v[16:17], v[60:61], v[16:17], v[144:145]
	v_pk_fma_f32 v[18:19], v[58:59], v[18:19], v[142:143]
	v_pk_fma_f32 v[46:47], v[20:21], v[20:21], v[4:5] op_sel_hi:[1,1,0]
	v_mul_f32_e32 v4, v26, v26
	v_and_b32_sdwa v23, v17, v235 dst_sel:DWORD dst_unused:UNUSED_PAD src0_sel:WORD_1 src1_sel:DWORD
	v_and_b32_sdwa v24, v19, v235 dst_sel:DWORD dst_unused:UNUSED_PAD src0_sel:WORD_1 src1_sel:DWORD
	v_pk_fma_f32 v[48:49], v[26:27], v[26:27], v[4:5] op_sel_hi:[1,1,0]
	v_and_b32_sdwa v4, v16, v235 dst_sel:DWORD dst_unused:UNUSED_PAD src0_sel:WORD_1 src1_sel:DWORD
	v_and_b32_sdwa v22, v18, v235 dst_sel:DWORD dst_unused:UNUSED_PAD src0_sel:WORD_1 src1_sel:DWORD
	v_add3_u32 v23, v17, v23, s44
	v_add3_u32 v24, v19, v24, s44
	v_add3_u32 v22, v18, v22, s44
	v_add3_u32 v4, v16, v4, s44
	v_and_b32_e32 v23, 0xffff0000, v23
	v_and_b32_e32 v24, 0xffff0000, v24
	v_or_b32_sdwa v23, v23, v4 dst_sel:DWORD dst_unused:UNUSED_PAD src0_sel:DWORD src1_sel:WORD_1
	v_or_b32_sdwa v22, v24, v22 dst_sel:DWORD dst_unused:UNUSED_PAD src0_sel:DWORD src1_sel:WORD_1
	v_mul_f32_e32 v46, v18, v18
	v_mul_f32_e32 v48, v19, v19
	v_mul_f32_e32 v38, v16, v16
	v_mul_f32_e32 v40, v17, v17
	global_store_dwordx2 v234, v[22:23], s[14:15] offset:2048 nt
	v_pk_add_f32 v[22:23], v[46:47], v[48:49]
	v_pk_add_f32 v[24:25], v[40:41], v[38:39]
	v_pk_mul_f32 v[10:11], v[6:7], v[10:11] op_sel_hi:[0,1]
	v_pk_add_f32 v[22:23], v[22:23], v[24:25]
	v_mov_b32_e32 v24, v13
	v_mov_b32_e32 v25, v15
	v_mov_b32_e32 v13, v14
	v_pk_mul_f32 v[24:25], v[6:7], v[24:25] op_sel_hi:[0,1]
	v_pk_mul_f32 v[12:13], v[6:7], v[12:13] op_sel_hi:[0,1]
	v_pk_fma_f32 v[12:13], v[66:67], v[12:13], v[138:139]
	v_pk_fma_f32 v[14:15], v[68:69], v[24:25], v[140:141]
	v_pk_add_f32 v[22:23], v[22:23], v[22:23] op_sel_hi:[0,1]
	v_and_b32_sdwa v24, v15, v235 dst_sel:DWORD dst_unused:UNUSED_PAD src0_sel:WORD_1 src1_sel:DWORD
	v_and_b32_sdwa v25, v13, v235 dst_sel:DWORD dst_unused:UNUSED_PAD src0_sel:WORD_1 src1_sel:DWORD
	v_and_b32_sdwa v4, v14, v235 dst_sel:DWORD dst_unused:UNUSED_PAD src0_sel:WORD_1 src1_sel:DWORD
	v_and_b32_sdwa v22, v12, v235 dst_sel:DWORD dst_unused:UNUSED_PAD src0_sel:WORD_1 src1_sel:DWORD
	v_add3_u32 v24, v15, v24, s44
	v_add3_u32 v25, v13, v25, s44
	v_add3_u32 v22, v12, v22, s44
	v_add3_u32 v4, v14, v4, s44
	v_and_b32_e32 v24, 0xffff0000, v24
	v_and_b32_e32 v38, 0xffff0000, v25
	v_or_b32_sdwa v25, v24, v4 dst_sel:DWORD dst_unused:UNUSED_PAD src0_sel:DWORD src1_sel:WORD_1
	v_or_b32_sdwa v24, v38, v22 dst_sel:DWORD dst_unused:UNUSED_PAD src0_sel:DWORD src1_sel:WORD_1
	v_pk_mul_f32 v[38:39], v[14:15], v[14:15]
	v_pk_mul_f32 v[40:41], v[12:13], v[12:13]
	v_pk_fma_f32 v[8:9], v[62:63], v[8:9], v[134:135]
	v_pk_mov_b32 v[46:47], v[40:41], v[38:39] op_sel:[1,0]
	v_mov_b32_e32 v41, v39
	v_pk_fma_f32 v[10:11], v[64:65], v[10:11], v[136:137]
	v_mul_f32_e32 v4, v8, v8
	v_pk_add_f32 v[38:39], v[40:41], v[46:47]
	v_pk_fma_f32 v[40:41], v[8:9], v[8:9], v[4:5] op_sel_hi:[1,1,0]
	v_mul_f32_e32 v4, v10, v10
	v_pk_fma_f32 v[46:47], v[10:11], v[10:11], v[4:5] op_sel_hi:[1,1,0]
	v_mov_b32_e32 v4, v7
	v_pk_mul_f32 v[4:5], v[4:5], v[6:7] op_sel_hi:[1,0]
	v_pk_mul_f32 v[2:3], v[2:3], v[6:7] op_sel_hi:[1,0]
	v_pk_add_f32 v[38:39], v[38:39], v[38:39] op_sel_hi:[0,1]
	s_waitcnt vmcnt(29)
	v_pk_fma_f32 v[2:3], v[52:53], v[2:3], v[132:133]
	v_pk_fma_f32 v[4:5], v[50:51], v[4:5], v[130:131]
	v_mul_f32_e32 v22, v2, v2
	v_mul_f32_e32 v40, v4, v4
	v_mul_f32_e32 v46, v5, v5
	v_mul_f32_e32 v38, v3, v3
	v_pk_add_f32 v[6:7], v[40:41], v[46:47]
	v_pk_add_f32 v[22:23], v[38:39], v[22:23]
	global_store_dwordx2 v234, v[24:25], s[14:15] offset:2560 nt
	v_pk_add_f32 v[6:7], v[6:7], v[22:23]
	v_and_b32_sdwa v24, v11, v235 dst_sel:DWORD dst_unused:UNUSED_PAD src0_sel:WORD_1 src1_sel:DWORD
	v_add_f32_e32 v6, v6, v7
	ds_bpermute_b32 v7, v171, v6
	v_and_b32_sdwa v22, v10, v235 dst_sel:DWORD dst_unused:UNUSED_PAD src0_sel:WORD_1 src1_sel:DWORD
	v_and_b32_sdwa v25, v9, v235 dst_sel:DWORD dst_unused:UNUSED_PAD src0_sel:WORD_1 src1_sel:DWORD
	v_add3_u32 v24, v11, v24, s44
	v_add3_u32 v22, v10, v22, s44
	s_waitcnt lgkmcnt(0)
	v_add_f32_e32 v6, v6, v7
	ds_bpermute_b32 v7, v226, v6
	v_and_b32_e32 v24, 0xffff0000, v24
	v_and_b32_sdwa v23, v8, v235 dst_sel:DWORD dst_unused:UNUSED_PAD src0_sel:WORD_1 src1_sel:DWORD
	v_add3_u32 v23, v8, v23, s44
	s_waitcnt lgkmcnt(0)
	v_add_f32_e32 v6, v6, v7
	ds_bpermute_b32 v38, v228, v6
	v_add3_u32 v7, v9, v25, s44
	v_and_b32_e32 v25, 0xffff0000, v7
	v_or_b32_sdwa v7, v24, v22 dst_sel:DWORD dst_unused:UNUSED_PAD src0_sel:DWORD src1_sel:WORD_1
	s_waitcnt lgkmcnt(0)
	v_add_f32_e32 v22, v6, v38
	ds_bpermute_b32 v24, v229, v22
	v_or_b32_sdwa v6, v25, v23 dst_sel:DWORD dst_unused:UNUSED_PAD src0_sel:DWORD src1_sel:WORD_1
	global_store_dwordx2 v234, v[6:7], s[14:15] offset:3072 nt
	v_and_b32_sdwa v7, v4, v235 dst_sel:DWORD dst_unused:UNUSED_PAD src0_sel:WORD_1 src1_sel:DWORD
	v_and_b32_sdwa v25, v5, v235 dst_sel:DWORD dst_unused:UNUSED_PAD src0_sel:WORD_1 src1_sel:DWORD
	s_waitcnt lgkmcnt(0)
	v_add_f32_e32 v22, v22, v24
	ds_bpermute_b32 v23, v230, v22
	v_add3_u32 v24, v4, v7, s44
	v_and_b32_sdwa v7, v3, v235 dst_sel:DWORD dst_unused:UNUSED_PAD src0_sel:WORD_1 src1_sel:DWORD
	v_and_b32_sdwa v6, v2, v235 dst_sel:DWORD dst_unused:UNUSED_PAD src0_sel:WORD_1 src1_sel:DWORD
	v_add3_u32 v7, v3, v7, s44
	s_waitcnt lgkmcnt(0)
	v_add_f32_e32 v22, v22, v23
	ds_bpermute_b32 v23, v231, v22
	v_add3_u32 v25, v5, v25, s44
	v_add3_u32 v6, v2, v6, s44
	v_and_b32_e32 v7, 0xffff0000, v7
	v_and_b32_e32 v25, 0xffff0000, v25
	s_waitcnt lgkmcnt(0)
	v_add_f32_e32 v22, v22, v23
	v_fmamk_f32 v22, v22, 0x3a000000, v232
	v_cmp_gt_f32_e32 vcc, s43, v22
	v_mul_f32_e32 v23, 0x4b800000, v22
	v_or_b32_sdwa v7, v7, v6 dst_sel:DWORD dst_unused:UNUSED_PAD src0_sel:DWORD src1_sel:WORD_1
	v_cndmask_b32_e32 v22, v22, v23, vcc
	v_rsq_f32_e32 v22, v22
	v_or_b32_sdwa v6, v25, v24 dst_sel:DWORD dst_unused:UNUSED_PAD src0_sel:DWORD src1_sel:WORD_1
	global_store_dwordx2 v234, v[6:7], s[14:15] offset:3584 nt
	v_mov_b32_e32 v38, 0
	v_mul_f32_e32 v6, 0x45800000, v22
	v_cndmask_b32_e32 v6, v22, v6, vcc
	v_pk_mul_f32 v[22:23], v[158:159], v[6:7] op_sel_hi:[1,0]
	v_pk_mul_f32 v[24:25], v[36:37], v[6:7] op_sel_hi:[1,0]
	v_pk_fma_f32 v[22:23], v[42:43], v[22:23], v[126:127]
	v_pk_fma_f32 v[24:25], v[44:45], v[24:25], v[128:129]
	v_bfe_u32 v7, v22, 16, 1
	v_bfe_u32 v36, v23, 16, 1
	v_add3_u32 v7, v22, v7, s44
	v_add3_u32 v36, v23, v36, s44
	v_med3_f32 v22, v22, s45, v236
	v_med3_f32 v23, v23, s45, v236
	v_lshrrev_b32_e32 v7, 16, v7
	v_cvt_pk_fp8_f32 v38, v22, v23
	v_and_or_b32 v36, v36, s42, v7
	v_bfe_u32 v7, v24, 16, 1
	v_add3_u32 v7, v24, v7, s44
	v_bfe_u32 v22, v25, 16, 1
	v_lshrrev_b32_e32 v7, 16, v7
	v_med3_f32 v23, v24, s45, v236
	v_med3_f32 v24, v25, s45, v236
	v_add3_u32 v22, v25, v22, s44
	v_cvt_pk_fp8_f32 v38, v23, v24 op_sel:[0,0,1]
	v_and_or_b32 v37, v22, s42, v7
	v_pk_mul_f32 v[22:23], v[32:33], v[6:7] op_sel_hi:[1,0]
	v_pk_mul_f32 v[24:25], v[34:35], v[6:7] op_sel_hi:[1,0]
	v_pk_fma_f32 v[22:23], v[106:107], v[22:23], v[110:111]
	v_mov_b32_e32 v34, 0
	v_bfe_u32 v7, v22, 16, 1
	v_bfe_u32 v32, v23, 16, 1
	v_add3_u32 v7, v22, v7, s44
	v_add3_u32 v32, v23, v32, s44
	v_med3_f32 v22, v22, s45, v236
	v_med3_f32 v23, v23, s45, v236
	v_pk_fma_f32 v[24:25], v[108:109], v[24:25], v[112:113]
	v_lshrrev_b32_e32 v7, 16, v7
	v_cvt_pk_fp8_f32 v34, v22, v23
	v_and_or_b32 v32, v32, s42, v7
	v_bfe_u32 v7, v24, 16, 1
	v_add3_u32 v7, v24, v7, s44
	v_bfe_u32 v22, v25, 16, 1
	v_lshrrev_b32_e32 v7, 16, v7
	v_med3_f32 v23, v24, s45, v236
	v_med3_f32 v24, v25, s45, v236
	v_add3_u32 v22, v25, v22, s44
	v_cvt_pk_fp8_f32 v34, v23, v24 op_sel:[0,0,1]
	v_and_or_b32 v33, v22, s42, v7
	v_pk_mul_f32 v[22:23], v[28:29], v[6:7] op_sel_hi:[1,0]
	v_pk_mul_f32 v[24:25], v[30:31], v[6:7] op_sel_hi:[1,0]
	v_pk_fma_f32 v[22:23], v[86:87], v[22:23], v[102:103]
	v_pk_fma_f32 v[24:25], v[88:89], v[24:25], v[104:105]
	v_bfe_u32 v7, v22, 16, 1
	v_add3_u32 v7, v22, v7, s44
	v_bfe_u32 v28, v23, 16, 1
	v_lshrrev_b32_e32 v7, 16, v7
	v_add3_u32 v28, v23, v28, s44
	v_and_or_b32 v28, v28, s42, v7
	v_bfe_u32 v7, v24, 16, 1
	v_med3_f32 v22, v22, s45, v236
	v_med3_f32 v23, v23, s45, v236
	v_mov_b32_e32 v30, 0
	v_add3_u32 v7, v24, v7, s44
	v_cvt_pk_fp8_f32 v30, v22, v23
	v_lshrrev_b32_e32 v7, 16, v7
	v_bfe_u32 v22, v25, 16, 1
	v_pk_mul_f32 v[20:21], v[20:21], v[6:7] op_sel_hi:[1,0]
	v_med3_f32 v23, v24, s45, v236
	v_med3_f32 v24, v25, s45, v236
	v_add3_u32 v22, v25, v22, s44
	v_pk_fma_f32 v[20:21], v[78:79], v[20:21], v[82:83]
	v_cvt_pk_fp8_f32 v30, v23, v24 op_sel:[0,0,1]
	v_and_or_b32 v29, v22, s42, v7
	v_pk_mul_f32 v[22:23], v[26:27], v[6:7] op_sel_hi:[1,0]
	v_bfe_u32 v7, v20, 16, 1
	v_add3_u32 v7, v20, v7, s44
	v_bfe_u32 v24, v21, 16, 1
	v_pk_fma_f32 v[22:23], v[80:81], v[22:23], v[84:85]
	v_lshrrev_b32_e32 v7, 16, v7
	v_add3_u32 v24, v21, v24, s44
	v_and_or_b32 v24, v24, s42, v7
	v_bfe_u32 v7, v22, 16, 1
	v_add3_u32 v7, v22, v7, s44
	v_lshrrev_b32_e32 v7, 16, v7
	v_med3_f32 v20, v20, s45, v236
	v_med3_f32 v21, v21, s45, v236
	v_mov_b32_e32 v26, 0
	v_cvt_pk_fp8_f32 v26, v20, v21
	v_bfe_u32 v20, v23, 16, 1
	v_pk_mul_f32 v[18:19], v[18:19], v[6:7] op_sel_hi:[1,0]
	v_add3_u32 v20, v23, v20, s44
	v_pk_fma_f32 v[18:19], v[70:71], v[18:19], v[74:75]
	v_and_or_b32 v25, v20, s42, v7
	v_pk_mul_f32 v[16:17], v[16:17], v[6:7] op_sel_hi:[1,0]
	v_bfe_u32 v7, v18, 16, 1
	v_med3_f32 v21, v22, s45, v236
	v_med3_f32 v22, v23, s45, v236
	v_add3_u32 v7, v18, v7, s44
	v_bfe_u32 v20, v19, 16, 1
	v_cvt_pk_fp8_f32 v26, v21, v22 op_sel:[0,0,1]
	v_pk_fma_f32 v[16:17], v[72:73], v[16:17], v[76:77]
	v_lshrrev_b32_e32 v7, 16, v7
	v_add3_u32 v20, v19, v20, s44
	v_med3_f32 v18, v18, s45, v236
	v_med3_f32 v19, v19, s45, v236
	v_mov_b32_e32 v22, 0
	v_and_or_b32 v20, v20, s42, v7
	v_bfe_u32 v7, v16, 16, 1
	v_cvt_pk_fp8_f32 v22, v18, v19
	v_add3_u32 v7, v16, v7, s44
	v_lshrrev_b32_e32 v7, 16, v7
	v_bfe_u32 v18, v17, 16, 1
	v_med3_f32 v16, v16, s45, v236
	v_med3_f32 v19, v17, s45, v236
	v_pk_mul_f32 v[12:13], v[12:13], v[6:7] op_sel_hi:[1,0]
	v_cvt_pk_fp8_f32 v22, v16, v19 op_sel:[0,0,1]
	v_add3_u32 v16, v17, v18, s44
	v_pk_fma_f32 v[12:13], v[90:91], v[12:13], v[98:99]
	v_and_or_b32 v21, v16, s42, v7
	v_pk_mul_f32 v[14:15], v[14:15], v[6:7] op_sel_hi:[1,0]
	v_bfe_u32 v7, v12, 16, 1
	v_add3_u32 v7, v12, v7, s44
	v_bfe_u32 v16, v13, 16, 1
	v_pk_fma_f32 v[14:15], v[92:93], v[14:15], v[100:101]
	v_lshrrev_b32_e32 v7, 16, v7
	v_add3_u32 v16, v13, v16, s44
	v_and_or_b32 v16, v16, s42, v7
	v_bfe_u32 v7, v14, 16, 1
	v_add3_u32 v7, v14, v7, s44
	v_lshrrev_b32_e32 v7, 16, v7
	v_med3_f32 v12, v12, s45, v236
	v_med3_f32 v13, v13, s45, v236
	v_mov_b32_e32 v18, 0
	v_cvt_pk_fp8_f32 v18, v12, v13
	v_bfe_u32 v12, v15, 16, 1
	v_pk_mul_f32 v[8:9], v[8:9], v[6:7] op_sel_hi:[1,0]
	v_add3_u32 v12, v15, v12, s44
	v_pk_fma_f32 v[8:9], v[94:95], v[8:9], v[118:119]
	v_and_or_b32 v17, v12, s42, v7
	v_pk_mul_f32 v[10:11], v[10:11], v[6:7] op_sel_hi:[1,0]
	v_bfe_u32 v7, v8, 16, 1
	v_add3_u32 v7, v8, v7, s44
	v_bfe_u32 v12, v9, 16, 1
	v_pk_fma_f32 v[10:11], v[96:97], v[10:11], v[120:121]
	v_lshrrev_b32_e32 v7, 16, v7
	v_add3_u32 v12, v9, v12, s44
	v_and_or_b32 v12, v12, s42, v7
	v_bfe_u32 v7, v10, 16, 1
	v_add3_u32 v7, v10, v7, s44
	v_med3_f32 v13, v14, s45, v236
	v_med3_f32 v14, v15, s45, v236
	v_lshrrev_b32_e32 v7, 16, v7
	v_cvt_pk_fp8_f32 v18, v13, v14 op_sel:[0,0,1]
	v_med3_f32 v8, v8, s45, v236
	v_med3_f32 v9, v9, s45, v236
	v_mov_b32_e32 v14, 0
	v_pk_mul_f32 v[4:5], v[4:5], v[6:7] op_sel_hi:[1,0]
	v_cvt_pk_fp8_f32 v14, v8, v9
	v_bfe_u32 v8, v11, 16, 1
	v_pk_fma_f32 v[4:5], v[114:115], v[4:5], v[122:123]
	v_add3_u32 v8, v11, v8, s44
	v_pk_mul_f32 v[2:3], v[2:3], v[6:7] op_sel_hi:[1,0]
	v_bfe_u32 v6, v4, 16, 1
	v_and_or_b32 v13, v8, s42, v7
	v_add3_u32 v6, v4, v6, s44
	v_bfe_u32 v7, v5, 16, 1
	v_pk_fma_f32 v[2:3], v[116:117], v[2:3], v[124:125]
	v_lshrrev_b32_e32 v6, 16, v6
	v_add3_u32 v7, v5, v7, s44
	v_and_or_b32 v6, v7, s42, v6
	v_bfe_u32 v7, v2, 16, 1
	v_add3_u32 v7, v2, v7, s44
	v_bfe_u32 v8, v3, 16, 1
	v_lshrrev_b32_e32 v7, 16, v7
	v_add3_u32 v8, v3, v8, s44
	v_and_or_b32 v7, v8, s42, v7
	v_med3_f32 v4, v4, s45, v236
	v_med3_f32 v5, v5, s45, v236
	v_mov_b32_e32 v8, 0
	v_cvt_pk_fp8_f32 v8, v4, v5
	s_add_u32 s14, s11, s24
	v_med3_f32 v2, v2, s45, v236
	v_med3_f32 v3, v3, s45, v236
	s_addc_u32 s15, s13, s25
	v_med3_f32 v9, v10, s45, v236
	v_med3_f32 v10, v11, s45, v236
	v_cvt_pk_fp8_f32 v8, v2, v3 op_sel:[0,0,1]
	s_add_u32 s4, s33, s22
	v_cvt_pk_fp8_f32 v14, v9, v10 op_sel:[0,0,1]
	s_addc_u32 s5, s34, s23
	s_add_i32 s46, s46, s81
	s_add_i32 s8, s8, s37
	s_cmpk_lt_i32 s46, 0x100
	global_store_dwordx2 v234, v[36:37], s[14:15]
	global_store_dword v237, v38, s[4:5]
	global_store_dwordx2 v234, v[32:33], s[14:15] offset:512
	global_store_dword v237, v34, s[4:5] offset:256
	global_store_dwordx2 v234, v[28:29], s[14:15] offset:1024
	global_store_dword v237, v30, s[4:5] offset:512
	global_store_dwordx2 v234, v[24:25], s[14:15] offset:1536
	global_store_dword v237, v26, s[4:5] offset:768
	global_store_dwordx2 v234, v[20:21], s[14:15] offset:2048
	global_store_dword v237, v22, s[4:5] offset:1024
	global_store_dwordx2 v234, v[16:17], s[14:15] offset:2560
	global_store_dword v237, v18, s[4:5] offset:1280
	global_store_dwordx2 v234, v[12:13], s[14:15] offset:3072
	global_store_dword v237, v14, s[4:5] offset:1536
	global_store_dwordx2 v234, v[6:7], s[14:15] offset:3584
	global_store_dword v237, v8, s[4:5] offset:1792
	s_cbranch_scc0 .LBB0_3481

.LBB0_4362:
	v_cvt_pk_f32_fp8_e32 v[178:179], v173
	v_cvt_pk_f32_fp8_e32 v[204:205], v161
	v_cvt_pk_f32_fp8_e32 v[182:183], v170
	v_cvt_pk_f32_fp8_sdwa v[180:181], v173 src0_sel:WORD_1
	v_pk_add_f32 v[178:179], v[178:179], 0 op_sel_hi:[1,0]
	v_cvt_pk_f32_fp8_sdwa v[208:209], v161 src0_sel:WORD_1
	v_pk_add_f32 v[178:179], v[178:179], v[204:205]
	v_cvt_pk_f32_fp8_e32 v[204:205], v154
	v_cvt_pk_f32_fp8_e32 v[186:187], v167
	v_pk_add_f32 v[182:183], v[182:183], 0 op_sel_hi:[1,0]
	v_cvt_pk_f32_fp8_sdwa v[184:185], v170 src0_sel:WORD_1
	v_pk_add_f32 v[180:181], v[180:181], 0 op_sel_hi:[1,0]
	v_pk_add_f32 v[182:183], v[182:183], v[204:205]
	v_cvt_pk_f32_fp8_e32 v[204:205], v150
	v_pk_add_f32 v[180:181], v[180:181], v[208:209]
	v_cvt_pk_f32_fp8_sdwa v[208:209], v154 src0_sel:WORD_1
	v_cvt_pk_f32_fp8_e32 v[190:191], v165
	v_pk_add_f32 v[186:187], v[186:187], 0 op_sel_hi:[1,0]
	v_cvt_pk_f32_fp8_sdwa v[188:189], v167 src0_sel:WORD_1
	v_pk_add_f32 v[184:185], v[184:185], 0 op_sel_hi:[1,0]
	v_pk_add_f32 v[186:187], v[186:187], v[204:205]
	v_cvt_pk_f32_fp8_e32 v[204:205], v145
	v_pk_add_f32 v[184:185], v[184:185], v[208:209]
	v_cvt_pk_f32_fp8_sdwa v[208:209], v150 src0_sel:WORD_1
	v_cvt_pk_f32_fp8_e32 v[194:195], v164
	v_pk_add_f32 v[190:191], v[190:191], 0 op_sel_hi:[1,0]
	v_cvt_pk_f32_fp8_sdwa v[192:193], v165 src0_sel:WORD_1
	v_pk_add_f32 v[188:189], v[188:189], 0 op_sel_hi:[1,0]
	v_pk_add_f32 v[190:191], v[190:191], v[204:205]
	v_cvt_pk_f32_fp8_e32 v[204:205], v140
	v_pk_add_f32 v[188:189], v[188:189], v[208:209]
	v_cvt_pk_f32_fp8_sdwa v[208:209], v145 src0_sel:WORD_1
	v_cvt_pk_f32_fp8_e32 v[196:197], v163
	v_pk_add_f32 v[194:195], v[194:195], 0 op_sel_hi:[1,0]
	v_cvt_pk_f32_fp8_sdwa v[164:165], v164 src0_sel:WORD_1
	v_pk_add_f32 v[192:193], v[192:193], 0 op_sel_hi:[1,0]
	v_pk_add_f32 v[194:195], v[194:195], v[204:205]
	v_cvt_pk_f32_fp8_e32 v[204:205], v139
	v_pk_add_f32 v[192:193], v[192:193], v[208:209]
	v_cvt_pk_f32_fp8_sdwa v[208:209], v140 src0_sel:WORD_1
	v_cvt_pk_f32_fp8_e32 v[200:201], v162
	v_pk_add_f32 v[196:197], v[196:197], 0 op_sel_hi:[1,0]
	v_cvt_pk_f32_fp8_sdwa v[198:199], v163 src0_sel:WORD_1
	v_cvt_pk_f32_fp8_sdwa v[162:163], v162 src0_sel:WORD_1
	v_pk_add_f32 v[164:165], v[164:165], 0 op_sel_hi:[1,0]
	v_pk_add_f32 v[196:197], v[196:197], v[204:205]
	v_cvt_pk_f32_fp8_e32 v[204:205], v138
	v_pk_add_f32 v[164:165], v[164:165], v[208:209]
	v_cvt_pk_f32_fp8_sdwa v[208:209], v139 src0_sel:WORD_1
	v_cvt_pk_f32_fp8_sdwa v[138:139], v138 src0_sel:WORD_1
	v_cvt_pk_f32_fp8_e32 v[202:203], v158
	v_pk_add_f32 v[200:201], v[200:201], 0 op_sel_hi:[1,0]
	v_cvt_pk_f32_fp8_sdwa v[206:207], v158 src0_sel:WORD_1
	v_pk_add_f32 v[200:201], v[200:201], v[204:205]
	v_pk_add_f32 v[162:163], v[162:163], 0 op_sel_hi:[1,0]
	v_cvt_pk_f32_fp8_e32 v[204:205], v137
	v_pk_add_f32 v[138:139], v[162:163], v[138:139]
	v_cvt_pk_f32_fp8_sdwa v[162:163], v137 src0_sel:WORD_1
	v_pk_add_f32 v[202:203], v[202:203], 0 op_sel_hi:[1,0]
	v_pk_add_f32 v[198:199], v[198:199], 0 op_sel_hi:[1,0]
	v_pk_add_f32 v[202:203], v[202:203], v[204:205]
	v_pk_add_f32 v[204:205], v[206:207], 0 op_sel_hi:[1,0]
	v_pk_add_f32 v[198:199], v[198:199], v[208:209]
	v_pk_add_f32 v[162:163], v[204:205], v[162:163]
	v_cvt_pk_f32_fp8_e32 v[204:205], v136
	v_cvt_pk_f32_fp8_sdwa v[136:137], v136 src0_sel:WORD_1
	v_cvt_pk_f32_fp8_e32 v[206:207], v135
	v_cvt_pk_f32_fp8_sdwa v[208:209], v135 src0_sel:WORD_1
	v_pk_add_f32 v[178:179], v[178:179], v[204:205]
	v_pk_add_f32 v[136:137], v[180:181], v[136:137]
	v_pk_add_f32 v[180:181], v[182:183], v[206:207]
	v_pk_add_f32 v[182:183], v[184:185], v[208:209]
	v_cvt_pk_f32_fp8_e32 v[184:185], v134
	v_cvt_pk_f32_fp8_sdwa v[134:135], v134 src0_sel:WORD_1
	v_cvt_pk_f32_fp8_e32 v[204:205], v133
	v_cvt_pk_f32_fp8_sdwa v[206:207], v133 src0_sel:WORD_1
	v_pk_add_f32 v[184:185], v[186:187], v[184:185]
	v_pk_add_f32 v[134:135], v[188:189], v[134:135]
	v_pk_add_f32 v[186:187], v[190:191], v[204:205]
	v_pk_add_f32 v[188:189], v[192:193], v[206:207]
	v_cvt_pk_f32_fp8_e32 v[190:191], v132
	v_cvt_pk_f32_fp8_sdwa v[132:133], v132 src0_sel:WORD_1
	v_cvt_pk_f32_fp8_e32 v[192:193], v131
	v_cvt_pk_f32_fp8_sdwa v[204:205], v131 src0_sel:WORD_1
	v_pk_add_f32 v[190:191], v[194:195], v[190:191]
	v_pk_add_f32 v[132:133], v[164:165], v[132:133]
	v_pk_add_f32 v[164:165], v[196:197], v[192:193]
	v_cvt_pk_f32_fp8_e32 v[194:195], v130
	v_cvt_pk_f32_fp8_sdwa v[130:131], v130 src0_sel:WORD_1
	v_cvt_pk_f32_fp8_e32 v[196:197], v129
	v_pk_add_f32 v[192:193], v[198:199], v[204:205]
	v_cvt_pk_f32_fp8_sdwa v[198:199], v129 src0_sel:WORD_1
	v_pk_add_f32 v[130:131], v[138:139], v[130:131]
	v_pk_add_f32 v[138:139], v[202:203], v[196:197]
	v_cvt_pk_f32_fp8_e32 v[196:197], v128
	v_cvt_pk_f32_fp8_sdwa v[128:129], v128 src0_sel:WORD_1
	v_pk_add_f32 v[162:163], v[162:163], v[198:199]
	v_cvt_pk_f32_fp8_e32 v[198:199], v127
	v_pk_add_f32 v[194:195], v[200:201], v[194:195]
	v_cvt_pk_f32_fp8_sdwa v[200:201], v127 src0_sel:WORD_1
	v_cvt_pk_f32_fp8_e32 v[216:217], v120
	v_cvt_pk_f32_fp8_e32 v[218:219], v121
	v_cvt_pk_f32_fp8_sdwa v[220:221], v120 src0_sel:WORD_1
	v_cvt_pk_f32_fp8_sdwa v[120:121], v121 src0_sel:WORD_1
	v_pk_add_f32 v[128:129], v[136:137], v[128:129]
	v_cvt_pk_f32_fp8_e32 v[136:137], v119
	v_cvt_pk_f32_fp8_e32 v[202:203], v126
	v_cvt_pk_f32_fp8_sdwa v[126:127], v126 src0_sel:WORD_1
	v_pk_add_f32 v[180:181], v[180:181], v[198:199]
	v_pk_add_f32 v[120:121], v[128:129], v[120:121]
	v_cvt_pk_f32_fp8_sdwa v[128:129], v119 src0_sel:WORD_1
	v_pk_add_f32 v[136:137], v[180:181], v[136:137]
	v_pk_add_f32 v[180:181], v[182:183], v[200:201]
	v_cvt_pk_f32_fp8_e32 v[182:183], v118
	v_cvt_pk_f32_fp8_sdwa v[118:119], v118 src0_sel:WORD_1
	v_cvt_pk_f32_fp8_e32 v[204:205], v125
	v_cvt_pk_f32_fp8_sdwa v[206:207], v125 src0_sel:WORD_1
	v_pk_add_f32 v[126:127], v[134:135], v[126:127]
	v_cvt_pk_f32_fp8_e32 v[134:135], v113
	v_pk_add_f32 v[118:119], v[126:127], v[118:119]
	v_cvt_pk_f32_fp8_sdwa v[126:127], v113 src0_sel:WORD_1
	v_pk_add_f32 v[128:129], v[180:181], v[128:129]
	v_pk_add_f32 v[180:181], v[184:185], v[202:203]
	v_cvt_pk_f32_fp8_e32 v[208:209], v124
	v_pk_add_f32 v[180:181], v[180:181], v[182:183]
	v_pk_add_f32 v[182:183], v[186:187], v[204:205]
	v_cvt_pk_f32_fp8_sdwa v[124:125], v124 src0_sel:WORD_1
	v_pk_add_f32 v[134:135], v[182:183], v[134:135]
	v_pk_add_f32 v[182:183], v[188:189], v[206:207]
	v_cvt_pk_f32_fp8_e32 v[210:211], v123
	v_pk_add_f32 v[126:127], v[182:183], v[126:127]
	v_cvt_pk_f32_fp8_sdwa v[182:183], v108 src0_sel:WORD_1
	v_cvt_pk_f32_fp8_sdwa v[212:213], v123 src0_sel:WORD_1
	v_pk_add_f32 v[124:125], v[132:133], v[124:125]
	v_cvt_pk_f32_fp8_e32 v[132:133], v107
	v_pk_add_f32 v[124:125], v[124:125], v[182:183]
	v_cvt_pk_f32_fp8_sdwa v[182:183], v107 src0_sel:WORD_1
	v_pk_add_f32 v[164:165], v[164:165], v[210:211]
	v_cvt_pk_f32_fp8_e32 v[214:215], v122
	v_cvt_pk_f32_fp8_sdwa v[122:123], v122 src0_sel:WORD_1
	v_pk_add_f32 v[132:133], v[164:165], v[132:133]
	v_pk_add_f32 v[164:165], v[192:193], v[212:213]
	v_cvt_pk_f32_fp8_e32 v[184:185], v108
	v_pk_add_f32 v[164:165], v[164:165], v[182:183]
	v_cvt_pk_f32_fp8_sdwa v[182:183], v99 src0_sel:WORD_1
	v_pk_add_f32 v[122:123], v[130:131], v[122:123]
	v_cvt_pk_f32_fp8_e32 v[130:131], v97
	v_pk_add_f32 v[138:139], v[138:139], v[216:217]
	v_pk_add_f32 v[122:123], v[122:123], v[182:183]
	v_cvt_pk_f32_fp8_sdwa v[182:183], v97 src0_sel:WORD_1
	v_pk_add_f32 v[186:187], v[190:191], v[208:209]
	v_pk_add_f32 v[130:131], v[138:139], v[130:131]
	v_pk_add_f32 v[138:139], v[162:163], v[220:221]
	v_pk_add_f32 v[184:185], v[186:187], v[184:185]
	v_cvt_pk_f32_fp8_e32 v[186:187], v99
	v_pk_add_f32 v[138:139], v[138:139], v[182:183]
	v_cvt_pk_f32_fp8_e32 v[162:163], v96
	v_cvt_pk_f32_fp8_sdwa v[96:97], v96 src0_sel:WORD_1
	v_cvt_pk_f32_fp8_e32 v[182:183], v94
	v_pk_add_f32 v[178:179], v[178:179], v[196:197]
	v_pk_add_f32 v[188:189], v[194:195], v[214:215]
	v_pk_add_f32 v[178:179], v[178:179], v[218:219]
	v_pk_add_f32 v[186:187], v[188:189], v[186:187]
	v_cvt_pk_f32_fp8_sdwa v[188:189], v94 src0_sel:WORD_1
	v_pk_add_f32 v[96:97], v[120:121], v[96:97]
	v_pk_add_f32 v[120:121], v[136:137], v[182:183]
	v_cvt_pk_f32_fp8_e32 v[182:183], v85
	v_pk_add_f32 v[162:163], v[178:179], v[162:163]
	v_cvt_pk_f32_fp8_e32 v[136:137], v87
	v_cvt_pk_f32_fp8_sdwa v[178:179], v87 src0_sel:WORD_1
	v_pk_add_f32 v[128:129], v[128:129], v[188:189]
	v_cvt_pk_f32_fp8_sdwa v[188:189], v85 src0_sel:WORD_1
	v_pk_add_f32 v[134:135], v[134:135], v[182:183]
	v_cvt_pk_f32_fp8_e32 v[182:183], v79
	v_pk_add_f32 v[136:137], v[180:181], v[136:137]
	v_pk_add_f32 v[118:119], v[118:119], v[178:179]
	v_cvt_pk_f32_fp8_e32 v[178:179], v82
	v_cvt_pk_f32_fp8_sdwa v[180:181], v82 src0_sel:WORD_1
	v_pk_add_f32 v[126:127], v[126:127], v[188:189]
	v_cvt_pk_f32_fp8_sdwa v[188:189], v79 src0_sel:WORD_1
	v_pk_add_f32 v[132:133], v[132:133], v[182:183]
	v_cvt_pk_f32_fp8_sdwa v[182:183], v76 src0_sel:WORD_1
	v_pk_add_f32 v[178:179], v[184:185], v[178:179]
	v_pk_add_f32 v[124:125], v[124:125], v[180:181]
	v_cvt_pk_f32_fp8_e32 v[180:181], v76
	v_cvt_pk_f32_fp8_e32 v[184:185], v73
	v_pk_add_f32 v[164:165], v[164:165], v[188:189]
	v_cvt_pk_f32_fp8_sdwa v[188:189], v73 src0_sel:WORD_1
	v_pk_add_f32 v[122:123], v[122:123], v[182:183]
	v_cvt_pk_f32_fp8_e32 v[182:183], v72
	v_cvt_pk_f32_fp8_sdwa v[72:73], v72 src0_sel:WORD_1
	v_pk_add_f32 v[180:181], v[186:187], v[180:181]
	v_pk_add_f32 v[130:131], v[130:131], v[184:185]
	v_cvt_pk_f32_fp8_e32 v[184:185], v70
	v_cvt_pk_f32_fp8_sdwa v[186:187], v70 src0_sel:WORD_1
	v_cvt_pk_f32_fp8_e32 v[206:207], v71
	v_cvt_pk_f32_fp8_sdwa v[70:71], v71 src0_sel:WORD_1
	v_cvt_pk_f32_fp8_sdwa v[190:191], v69 src0_sel:WORD_1
	v_pk_add_f32 v[72:73], v[96:97], v[72:73]
	v_cvt_pk_f32_fp8_e32 v[96:97], v67
	v_pk_add_f32 v[138:139], v[138:139], v[188:189]
	v_cvt_pk_f32_fp8_e32 v[188:189], v69
	v_cvt_pk_f32_fp8_e32 v[194:195], v66
	v_cvt_pk_f32_fp8_sdwa v[196:197], v66 src0_sel:WORD_1
	v_cvt_pk_f32_fp8_e32 v[204:205], v28
	v_cvt_pk_f32_fp8_sdwa v[208:209], v28 src0_sel:WORD_1
	v_pk_add_f32 v[70:71], v[72:73], v[70:71]
	v_cvt_pk_f32_fp8_sdwa v[66:67], v67 src0_sel:WORD_1
	v_pk_add_f32 v[72:73], v[120:121], v[184:185]
	v_cvt_pk_f32_fp8_e32 v[120:121], v29
	v_cvt_pk_f32_fp8_sdwa v[28:29], v29 src0_sel:WORD_1
	v_cvt_pk_f32_fp8_e32 v[192:193], v68
	v_cvt_pk_f32_fp8_sdwa v[68:69], v68 src0_sel:WORD_1
	v_pk_add_f32 v[72:73], v[72:73], v[96:97]
	v_pk_add_f32 v[96:97], v[128:129], v[186:187]
	v_pk_add_f32 v[118:119], v[118:119], v[190:191]
	v_pk_add_f32 v[66:67], v[96:97], v[66:67]
	v_pk_add_f32 v[96:97], v[136:137], v[188:189]
	v_pk_add_f32 v[28:29], v[118:119], v[28:29]
	v_cvt_pk_f32_fp8_sdwa v[118:119], v27 src0_sel:WORD_1
	v_cvt_pk_f32_fp8_e32 v[198:199], v31
	v_pk_add_f32 v[96:97], v[96:97], v[120:121]
	v_cvt_pk_f32_fp8_e32 v[120:121], v27
	v_pk_add_f32 v[68:69], v[126:127], v[68:69]
	v_cvt_pk_f32_fp8_e32 v[126:127], v26
	v_cvt_pk_f32_fp8_sdwa v[26:27], v26 src0_sel:WORD_1
	v_cvt_pk_f32_fp8_sdwa v[200:201], v31 src0_sel:WORD_1
	v_cvt_pk_f32_fp8_e32 v[202:203], v30
	v_cvt_pk_f32_fp8_sdwa v[30:31], v30 src0_sel:WORD_1
	v_pk_add_f32 v[128:129], v[134:135], v[192:193]
	v_pk_add_f32 v[68:69], v[68:69], v[118:119]
	v_pk_add_f32 v[118:119], v[178:179], v[194:195]
	v_pk_add_f32 v[124:125], v[124:125], v[196:197]
	v_pk_add_f32 v[120:121], v[128:129], v[120:121]
	v_pk_add_f32 v[118:119], v[118:119], v[126:127]
	v_cvt_pk_f32_fp8_e32 v[126:127], v25
	v_pk_add_f32 v[26:27], v[124:125], v[26:27]
	v_cvt_pk_f32_fp8_sdwa v[124:125], v25 src0_sel:WORD_1
	v_pk_add_f32 v[128:129], v[132:133], v[198:199]
	v_cvt_pk_f32_fp8_e32 v[132:133], v24
	v_cvt_pk_f32_fp8_sdwa v[24:25], v24 src0_sel:WORD_1
	v_pk_add_f32 v[30:31], v[122:123], v[30:31]
	v_cvt_pk_f32_fp8_e32 v[122:123], v0
	v_pk_add_f32 v[126:127], v[128:129], v[126:127]
	v_pk_add_f32 v[24:25], v[30:31], v[24:25]
	v_cvt_pk_f32_fp8_sdwa v[30:31], v0 src0_sel:WORD_1
	v_pk_add_f32 v[128:129], v[164:165], v[200:201]
	v_pk_add_f32 v[130:131], v[130:131], v[204:205]
	v_pk_add_f32 v[124:125], v[128:129], v[124:125]
	v_pk_add_f32 v[128:129], v[180:181], v[202:203]
	v_pk_add_f32 v[122:123], v[130:131], v[122:123]
	v_pk_add_f32 v[130:131], v[138:139], v[208:209]
	v_pk_add_f32 v[128:129], v[128:129], v[132:133]
	v_pk_add_f32 v[130:131], v[130:131], v[30:31]
	v_cvt_pk_f32_fp8_e32 v[30:31], v84
	v_cvt_pk_f32_fp8_sdwa v[84:85], v84 src0_sel:WORD_1
	v_cvt_pk_f32_fp8_e32 v[132:133], v83
	v_cvt_pk_f32_fp8_sdwa v[82:83], v83 src0_sel:WORD_1
	v_pk_add_f32 v[162:163], v[162:163], v[182:183]
	v_pk_add_f32 v[70:71], v[70:71], v[84:85]
	v_pk_add_f32 v[162:163], v[162:163], v[206:207]
	v_pk_add_f32 v[84:85], v[72:73], v[132:133]
	v_pk_add_f32 v[134:135], v[162:163], v[30:31]
	v_pk_add_f32 v[82:83], v[66:67], v[82:83]
	v_cvt_pk_f32_fp8_e32 v[30:31], v81
	v_cvt_pk_f32_fp8_sdwa v[66:67], v81 src0_sel:WORD_1
	v_cvt_pk_f32_fp8_e32 v[72:73], v80
	v_cvt_pk_f32_fp8_sdwa v[80:81], v80 src0_sel:WORD_1
	v_pk_add_f32 v[96:97], v[96:97], v[30:31]
	v_cvt_pk_f32_fp8_sdwa v[30:31], v78 src0_sel:WORD_1
	v_pk_add_f32 v[132:133], v[28:29], v[66:67]
	v_pk_add_f32 v[80:81], v[68:69], v[80:81]
	v_cvt_pk_f32_fp8_sdwa v[68:69], v77 src0_sel:WORD_1
	v_cvt_pk_f32_fp8_e32 v[28:29], v78
	v_cvt_pk_f32_fp8_e32 v[66:67], v77
	v_pk_add_f32 v[78:79], v[26:27], v[30:31]
	v_pk_add_f32 v[124:125], v[124:125], v[68:69]
	v_cvt_pk_f32_fp8_e32 v[26:27], v75
	v_cvt_pk_f32_fp8_sdwa v[68:69], v74 src0_sel:WORD_1
	v_pk_add_f32 v[76:77], v[118:119], v[28:29]
	v_pk_add_f32 v[118:119], v[126:127], v[66:67]
	v_cvt_pk_f32_fp8_sdwa v[30:31], v75 src0_sel:WORD_1
	v_cvt_pk_f32_fp8_e32 v[66:67], v74
	v_pk_add_f32 v[28:29], v[128:129], v[26:27]
	v_pk_add_f32 v[26:27], v[130:131], v[68:69]
	v_mov_b32_e32 v68, v135
	v_mov_b32_e32 v69, v85
	v_pk_add_f32 v[120:121], v[120:121], v[72:73]
	v_pk_add_f32 v[30:31], v[24:25], v[30:31]
	v_pk_add_f32 v[24:25], v[122:123], v[66:67]
	v_mov_b32_e32 v66, v134
	v_mov_b32_e32 v67, v84
	v_pk_mul_f32 v[68:69], v[68:69], v[68:69]
	v_mov_b32_e32 v72, v71
	v_mov_b32_e32 v73, v83
	v_pk_fma_f32 v[66:67], v[66:67], v[66:67], v[68:69]
	v_mov_b32_e32 v68, v70
	v_mov_b32_e32 v69, v82
	v_pk_mul_f32 v[72:73], v[72:73], v[72:73]
	v_mul_f32_e32 v0, v121, v121
	v_pk_fma_f32 v[68:69], v[68:69], v[68:69], v[72:73]
	v_mov_b32_e32 v72, v97
	v_mov_b32_e32 v73, v133
	v_pk_add_f32 v[66:67], v[66:67], v[68:69]
	v_mov_b32_e32 v68, v96
	v_mov_b32_e32 v69, v132
	v_pk_mul_f32 v[72:73], v[72:73], v[72:73]
	v_pk_add_f32 v[66:67], v[66:67], v[66:67] op_sel:[0,1] op_sel_hi:[1,0]
	v_pk_fma_f32 v[68:69], v[68:69], v[68:69], v[72:73]
	v_pk_fma_f32 v[72:73], v[120:121], v[120:121], v[0:1] op_sel_hi:[1,1,0]
	v_mul_f32_e32 v0, v81, v81
	v_pk_add_f32 v[68:69], v[68:69], v[68:69] op_sel:[0,1] op_sel_hi:[1,0]
	v_pk_fma_f32 v[74:75], v[80:81], v[80:81], v[0:1] op_sel_hi:[1,1,0]
	v_pk_mul_f32 v[122:123], v[76:77], v[76:77]
	v_pk_mul_f32 v[126:127], v[78:79], v[78:79]
	v_mov_b32_e32 v67, v122
	v_mov_b32_e32 v69, v123
	v_mov_b32_e32 v73, v126
	v_mov_b32_e32 v75, v127
	v_pk_add_f32 v[66:67], v[66:67], v[68:69]
	v_pk_add_f32 v[68:69], v[72:73], v[74:75]
	v_mov_b32_e32 v72, v119
	v_mov_b32_e32 v73, v125
	v_pk_add_f32 v[66:67], v[66:67], v[68:69]
	v_mov_b32_e32 v68, v118
	v_mov_b32_e32 v69, v124
	v_pk_mul_f32 v[72:73], v[72:73], v[72:73]
	v_mul_f32_e32 v0, v29, v29
	v_pk_fma_f32 v[68:69], v[68:69], v[68:69], v[72:73]
	v_pk_fma_f32 v[72:73], v[28:29], v[28:29], v[0:1] op_sel_hi:[1,1,0]
	v_mul_f32_e32 v0, v31, v31
	v_pk_add_f32 v[66:67], v[66:67], v[66:67] op_sel:[0,1] op_sel_hi:[1,0]
	v_pk_add_f32 v[68:69], v[68:69], v[68:69] op_sel:[0,1] op_sel_hi:[1,0]
	v_pk_fma_f32 v[74:75], v[30:31], v[30:31], v[0:1] op_sel_hi:[1,1,0]
	v_pk_mul_f32 v[122:123], v[24:25], v[24:25]
	v_pk_mul_f32 v[126:127], v[26:27], v[26:27]
	v_mov_b32_e32 v67, v122
	v_mov_b32_e32 v69, v123
	v_mov_b32_e32 v73, v126
	v_mov_b32_e32 v75, v127
	v_pk_add_f32 v[66:67], v[66:67], v[68:69]
	v_pk_add_f32 v[68:69], v[72:73], v[74:75]
	s_lshl_b64 s[0:1], s[8:9], 11
	v_pk_add_f32 v[66:67], v[66:67], v[68:69]
	s_lshl_b64 s[0:1], s[0:1], 2
	v_add_f32_e32 v0, v66, v67
	ds_bpermute_b32 v66, v32, v0
	v_readlane_b32 s16, v249, 5
	v_readlane_b32 s17, v249, 6
	s_add_u32 s0, s16, s0
	s_waitcnt vmcnt(7)
	v_lshlrev_b32_e32 v126, 16, v22
	s_waitcnt lgkmcnt(0)
	v_add_f32_e32 v0, v0, v66
	ds_bpermute_b32 v66, v33, v0
	v_and_b32_e32 v127, 0xffff0000, v22
	v_lshlrev_b32_e32 v22, 16, v23
	v_and_b32_e32 v23, 0xffff0000, v23
	s_addc_u32 s1, s17, s1
	s_waitcnt lgkmcnt(0)
	v_add_f32_e32 v0, v0, v66
	ds_bpermute_b32 v66, v34, v0
	s_add_i32 s12, s12, 8
	s_add_i32 s8, s8, 1
	s_cmpk_eq_i32 s12, 0x4f
	s_waitcnt vmcnt(5)
	v_mov_b32_e32 v87, v111
	s_waitcnt lgkmcnt(0)
	v_add_f32_e32 v0, v0, v66
	ds_bpermute_b32 v66, v35, v0
	v_mov_b32_e32 v94, v110
	v_mov_b32_e32 v99, v105
	v_mov_b32_e32 v107, v104
	v_mov_b32_e32 v108, v103
	s_waitcnt lgkmcnt(0)
	v_add_f32_e32 v0, v0, v66
	ds_bpermute_b32 v66, v36, v0
	v_mov_b32_e32 v113, v102
	v_mov_b32_e32 v136, v65
	v_mov_b32_e32 v137, v50
	v_mov_b32_e32 v138, v51
	s_waitcnt lgkmcnt(0)
	v_add_f32_e32 v0, v0, v66
	ds_bpermute_b32 v66, v37, v0
	v_mov_b32_e32 v139, v52
	v_mov_b32_e32 v140, v53
	v_mov_b32_e32 v145, v54
	v_mov_b32_e32 v150, v55
	s_waitcnt lgkmcnt(0)
	v_add_f32_e32 v0, v0, v66
	v_fmamk_f32 v0, v0, 0x34000000, v40
	v_mul_f32_e32 v66, 0x4b800000, v0
	v_cmp_gt_f32_e32 vcc, s25, v0
	v_mov_b32_e32 v154, v56
	v_mov_b32_e32 v161, v57
	v_cndmask_b32_e32 v0, v0, v66, vcc
	v_rsq_f32_e32 v0, v0
	v_mov_b32_e32 v158, v42
	v_mov_b32_e32 v162, v43
	v_mov_b32_e32 v163, v44
	v_mul_f32_e32 v66, 0x45800000, v0
	v_cndmask_b32_e32 v74, v0, v66, vcc
	v_mov_b32_e32 v66, v38
	v_lshlrev_b32_e32 v0, 4, v2
	v_add_u32_e32 v75, 0, v66
	ds_read_b128 v[66:69], v75
	v_pk_mul_f32 v[130:131], v[70:71], v[74:75] op_sel_hi:[1,0]
	ds_read_b128 v[70:73], v75 offset:1024
	v_pk_mul_f32 v[128:129], v[134:135], v[74:75] op_sel_hi:[1,0]
	v_lshl_add_u64 v[122:123], s[0:1], 0, v[0:1]
	s_waitcnt lgkmcnt(1)
	v_pk_fma_f32 v[68:69], v[68:69], v[130:131], v[22:23]
	v_pk_fma_f32 v[66:67], v[66:67], v[128:129], v[126:127]
	global_store_dwordx4 v0, v[66:69], s[0:1] nt
	v_pk_mul_f32 v[22:23], v[82:83], v[74:75] op_sel_hi:[1,0]
	v_pk_mul_f32 v[82:83], v[132:133], v[74:75] op_sel_hi:[1,0]
	v_lshlrev_b32_e32 v66, 16, v20
	v_and_b32_e32 v67, 0xffff0000, v20
	v_lshlrev_b32_e32 v20, 16, v21
	v_and_b32_e32 v21, 0xffff0000, v21
	v_pk_mul_f32 v[68:69], v[84:85], v[74:75] op_sel_hi:[1,0]
	s_waitcnt lgkmcnt(0)
	v_pk_fma_f32 v[22:23], v[72:73], v[22:23], v[20:21]
	v_pk_fma_f32 v[20:21], v[70:71], v[68:69], v[66:67]
	global_store_dwordx4 v0, v[20:23], s[0:1] offset:1024 nt
	ds_read_b128 v[20:23], v75 offset:2048
	ds_read_b128 v[66:69], v75 offset:3072
	v_lshlrev_b32_e32 v70, 16, v18
	v_and_b32_e32 v71, 0xffff0000, v18
	v_lshlrev_b32_e32 v18, 16, v19
	v_and_b32_e32 v19, 0xffff0000, v19
	v_pk_mul_f32 v[72:73], v[96:97], v[74:75] op_sel_hi:[1,0]
	s_waitcnt lgkmcnt(1)
	v_pk_fma_f32 v[22:23], v[22:23], v[82:83], v[18:19]
	v_pk_fma_f32 v[20:21], v[20:21], v[72:73], v[70:71]
	global_store_dwordx4 v0, v[20:23], s[0:1] offset:2048 nt
	v_pk_mul_f32 v[18:19], v[80:81], v[74:75] op_sel_hi:[1,0]
	v_pk_mul_f32 v[70:71], v[78:79], v[74:75] op_sel_hi:[1,0]
	s_waitcnt vmcnt(7)
	v_lshlrev_b32_e32 v20, 16, v16
	v_and_b32_e32 v21, 0xffff0000, v16
	v_lshlrev_b32_e32 v16, 16, v17
	v_and_b32_e32 v17, 0xffff0000, v17
	v_pk_mul_f32 v[22:23], v[120:121], v[74:75] op_sel_hi:[1,0]
	s_waitcnt lgkmcnt(0)
	v_pk_fma_f32 v[18:19], v[68:69], v[18:19], v[16:17]
	v_pk_fma_f32 v[16:17], v[66:67], v[22:23], v[20:21]
	global_store_dwordx4 v0, v[16:19], s[0:1] offset:3072 nt
	ds_read_b128 v[16:19], v75 offset:4096
	ds_read_b128 v[20:23], v75 offset:5120
	s_waitcnt vmcnt(7)
	v_lshlrev_b32_e32 v66, 16, v14
	v_and_b32_e32 v67, 0xffff0000, v14
	v_pk_mul_f32 v[68:69], v[76:77], v[74:75] op_sel_hi:[1,0]
	v_lshlrev_b32_e32 v14, 16, v15
	v_and_b32_e32 v15, 0xffff0000, v15
	s_waitcnt lgkmcnt(1)
	v_pk_fma_f32 v[16:17], v[16:17], v[68:69], v[66:67]
	v_add_co_u32_e32 v66, vcc, s26, v122
	v_pk_fma_f32 v[18:19], v[18:19], v[70:71], v[14:15]
	s_nop 0
	v_addc_co_u32_e32 v67, vcc, 0, v123, vcc
	global_store_dwordx4 v[66:67], v[16:19], off nt
	v_pk_mul_f32 v[14:15], v[124:125], v[74:75] op_sel_hi:[1,0]
	v_mov_b32_e32 v0, v176
	s_waitcnt vmcnt(7)
	v_lshlrev_b32_e32 v16, 16, v12
	v_and_b32_e32 v17, 0xffff0000, v12
	v_lshlrev_b32_e32 v12, 16, v13
	v_and_b32_e32 v13, 0xffff0000, v13
	v_pk_mul_f32 v[18:19], v[118:119], v[74:75] op_sel_hi:[1,0]
	s_waitcnt lgkmcnt(0)
	v_pk_fma_f32 v[14:15], v[14:15], v[22:23], v[12:13]
	v_pk_fma_f32 v[12:13], v[18:19], v[20:21], v[16:17]
	global_store_dwordx4 v[66:67], v[12:15], off offset:1024 nt
	ds_read_b128 v[12:15], v75 offset:6144
	ds_read_b128 v[16:19], v75 offset:7168
	s_waitcnt vmcnt(7)
	v_lshlrev_b32_e32 v20, 16, v10
	v_and_b32_e32 v21, 0xffff0000, v10
	v_lshlrev_b32_e32 v10, 16, v11
	v_and_b32_e32 v11, 0xffff0000, v11
	v_pk_mul_f32 v[22:23], v[28:29], v[74:75] op_sel_hi:[1,0]
	v_pk_mul_f32 v[28:29], v[30:31], v[74:75] op_sel_hi:[1,0]
	s_waitcnt lgkmcnt(1)
	v_pk_fma_f32 v[12:13], v[22:23], v[12:13], v[20:21]
	v_pk_fma_f32 v[14:15], v[28:29], v[14:15], v[10:11]
	global_store_dwordx4 v[66:67], v[12:15], off offset:2048 nt
	v_pk_mul_f32 v[10:11], v[26:27], v[74:75] op_sel_hi:[1,0]
	v_mov_b32_e32 v26, v172
	s_waitcnt vmcnt(7)
	v_lshlrev_b32_e32 v12, 16, v8
	v_and_b32_e32 v13, 0xffff0000, v8
	v_lshlrev_b32_e32 v8, 16, v9
	v_and_b32_e32 v9, 0xffff0000, v9
	v_pk_mul_f32 v[14:15], v[24:25], v[74:75] op_sel_hi:[1,0]
	s_waitcnt lgkmcnt(0)
	v_pk_fma_f32 v[10:11], v[10:11], v[18:19], v[8:9]
	v_pk_fma_f32 v[8:9], v[14:15], v[16:17], v[12:13]
	global_store_dwordx4 v[66:67], v[8:11], off offset:3072 nt
	v_mov_b32_e32 v24, v175
	v_mov_b32_e32 v25, v174
	v_mov_b32_e32 v27, v171
	v_mov_b32_e32 v29, v169
	v_mov_b32_e32 v67, v168
	v_mov_b32_e32 v71, v166
	v_mov_b32_e32 v28, v160
	v_mov_b32_e32 v30, v159
	v_mov_b32_e32 v31, v157
	v_mov_b32_e32 v66, v156
	v_mov_b32_e32 v68, v155
	v_mov_b32_e32 v69, v153
	v_mov_b32_e32 v70, v152
	v_mov_b32_e32 v72, v151
	v_mov_b32_e32 v73, v117
	v_mov_b32_e32 v76, v116
	v_mov_b32_e32 v79, v115
	v_mov_b32_e32 v82, v114
	v_mov_b32_e32 v85, v112
	v_mov_b32_e32 v96, v109
	v_mov_b32_e32 v97, v106
	v_mov_b32_e32 v118, v101
	v_mov_b32_e32 v119, v100
	v_mov_b32_e32 v121, v98
	v_mov_b32_e32 v120, v95
	v_mov_b32_e32 v122, v93
	v_mov_b32_e32 v123, v92
	v_mov_b32_e32 v124, v91
	v_mov_b32_e32 v125, v90
	v_mov_b32_e32 v126, v89
	v_mov_b32_e32 v127, v88
	v_mov_b32_e32 v128, v86
	v_mov_b32_e32 v129, v58
	v_mov_b32_e32 v130, v59
	v_mov_b32_e32 v131, v60
	v_mov_b32_e32 v132, v61
	v_mov_b32_e32 v133, v62
	v_mov_b32_e32 v134, v63
	v_mov_b32_e32 v135, v64
	v_mov_b32_e32 v164, v45
	v_mov_b32_e32 v165, v46
	v_mov_b32_e32 v167, v47
	v_mov_b32_e32 v170, v48
	v_mov_b32_e32 v173, v49
	v_mov_b32_e32 v84, v141
	v_mov_b32_e32 v83, v142
	v_mov_b32_e32 v81, v143
	v_mov_b32_e32 v80, v144
	v_mov_b32_e32 v78, v146
	v_mov_b32_e32 v77, v147
	v_mov_b32_e32 v75, v148
	v_mov_b32_e32 v74, v149
	v_readlane_b32 s18, v249, 7
	v_readlane_b32 s19, v249, 8
	s_cbranch_scc1 .LBB0_4358
